# v29: out-proj epilogue: 4 gate loads issued together, 4 residual-row steps in flight (was 2); conv phase pads between dependent packed ops
# speedup vs baseline: 1.0029x; 1.0010x over previous
; #define GAS __attribute__((address_space(1)))
;     __device__ __forceinline__ void operator()(const f32x4 (&acc)[2][2][4][2], const Unit& u, int wr, int wc, int fr, int fq) const {
;         const int row0 = u.pm * 256 + wr * 64 + fr, col0 = u.pn * 256 + wc * 32 + 4 * fq; const float* gp = gate + (u.pm >> 3) * MODW + col0;
;         f32x4 gv[2][2];
; #pragma unroll
;         for (int bj = 0; bj < 2; ++bj)
; #pragma unroll
;             for (int n = 0; n < 2; ++n) gv[bj][n] = *(const GAS f32x4*)(gp + bj * 128 + n * 16) * scale;
;         size_t off0 = (size_t)row0 * DM + col0; asm volatile("" : "+v"(off0));
;         f32x4 B0[4], B1[4];
;     ...
;         ER_LOAD(B0, 0); ER_LOAD(B1, 1); ER_STORE(B0, 0); ER_LOAD(B0, 2); ER_STORE(B1, 1); ER_LOAD(B1, 3); ER_STORE(B0, 2); ER_LOAD(B0, 4); ER_STORE(B1, 3); ER_LOAD(B1, 5);
;         ER_STORE(B0, 4); ER_LOAD(B0, 6); ER_STORE(B1, 5); ER_LOAD(B1, 7); ER_STORE(B0, 6); ER_STORE(B1, 7);
.LBB0_2085:
	s_lshr_b32 s23, s30, 3
	s_mul_i32 s34, s23, 0x6000
	s_ashr_i32 s35, s34, 31
	s_lshl_b64 s[34:35], s[34:35], 2
	v_lshl_or_b32 v6, s31, 8, v183
	s_add_u32 s34, s49, s34
	s_addc_u32 s35, s50, s35
	v_ashrrev_i32_e32 v7, 31, v6
	s_nop 15
	s_nop 15
	v_lshl_add_u64 v[8:9], v[6:7], 2, s[34:35]
	global_load_dwordx4 v[18:21], v[8:9], off
	global_load_dwordx4 v[236:239], v[8:9], off offset:64
	global_load_dwordx4 v[240:243], v[8:9], off offset:512
	global_load_dwordx4 v[244:247], v[8:9], off offset:576
	v_readlane_b32 s60, v249, 15
	v_readlane_b32 s61, v249, 16
	s_mov_b32 s23, 0x80000
	v_readlane_b32 s62, v249, 17
	v_readlane_b32 s63, v249, 18
	v_readlane_b32 s64, v249, 19
	v_readlane_b32 s65, v249, 20
	v_readlane_b32 s66, v249, 21
	v_readlane_b32 s67, v249, 22
	v_readlane_b32 s68, v249, 23
	v_readlane_b32 s69, v249, 24
	v_readlane_b32 s70, v249, 25
	v_readlane_b32 s71, v249, 26
	v_readlane_b32 s72, v249, 27
	v_readlane_b32 s73, v249, 28
	v_readlane_b32 s74, v249, 29
	v_readlane_b32 s75, v249, 30
	v_lshl_add_u32 v2, s30, 8, v1
	v_ashrrev_i32_e32 v3, 31, v2
	v_lshlrev_b64 v[2:3], 12, v[2:3]
	v_lshl_add_u64 v[188:189], v[2:3], 0, v[6:7]
	v_lshl_add_u64 v[174:175], v[188:189], 2, s[60:61]
	global_load_dwordx4 v[2:5], v[174:175], off
	global_load_dwordx4 v[6:9], v[174:175], off offset:64
	global_load_dwordx4 v[10:13], v[174:175], off offset:512
	global_load_dwordx4 v[14:17], v[174:175], off offset:576
	v_add_co_u32_e32 v176, vcc, s57, v174
	v_lshl_add_u64 v[200:201], v[174:175], 0, s[20:21]
	s_nop 0
	v_addc_co_u32_e32 v177, vcc, 0, v175, vcc
	global_load_dwordx4 v[176:179], v[176:177], off
	s_nop 0
	global_load_dwordx4 v[192:195], v[200:201], off offset:64
	global_load_dwordx4 v[196:199], v[200:201], off offset:512
	s_nop 0
	global_load_dwordx4 v[200:203], v[200:201], off offset:576
	s_mov_b64 s[36:37], 0x80000
	v_lshl_add_u64 v[204:205], v[174:175], 0, s[36:37]
	global_load_dwordx4 v[216:219], v[204:205], off
	global_load_dwordx4 v[212:215], v[204:205], off offset:64
	global_load_dwordx4 v[208:211], v[204:205], off offset:512
	s_nop 0
	global_load_dwordx4 v[204:207], v[204:205], off offset:576
	s_mov_b64 s[36:37], 0xc0000
	v_lshl_add_u64 v[232:233], v[174:175], 0, s[36:37]
	global_load_dwordx4 v[220:223], v[232:233], off
	global_load_dwordx4 v[224:227], v[232:233], off offset:64
	global_load_dwordx4 v[228:231], v[232:233], off offset:512
	s_nop 0
	global_load_dwordx4 v[232:235], v[232:233], off offset:576
	v_readlane_b32 s30, v248, 6
	v_readlane_b32 s31, v248, 7
	s_waitcnt vmcnt(19)
	v_pk_mul_f32 v[30:31], v[20:21], s[18:19] op_sel_hi:[1,0]
	v_pk_mul_f32 v[32:33], v[18:19], s[18:19] op_sel_hi:[1,0]
	s_waitcnt vmcnt(18)
	v_pk_mul_f32 v[18:19], v[238:239], s[18:19] op_sel_hi:[1,0]
	v_pk_mul_f32 v[20:21], v[236:237], s[18:19] op_sel_hi:[1,0]
	s_waitcnt vmcnt(17)
	v_pk_mul_f32 v[22:23], v[242:243], s[18:19] op_sel_hi:[1,0]
	v_pk_mul_f32 v[24:25], v[240:241], s[18:19] op_sel_hi:[1,0]
	s_waitcnt vmcnt(16)
	v_pk_mul_f32 v[28:29], v[244:245], s[18:19] op_sel_hi:[1,0]
	v_pk_mul_f32 v[26:27], v[246:247], s[18:19] op_sel_hi:[1,0]
	s_waitcnt vmcnt(15)
	v_pk_fma_f32 v[4:5], v[160:161], v[30:31], v[4:5]
	v_pk_fma_f32 v[2:3], v[158:159], v[32:33], v[2:3]
	v_lshl_add_u64 v[158:159], v[188:189], 1, s[30:31]
	v_cvt_pk_bf16_f32 v2, v2, v3
	v_cvt_pk_bf16_f32 v3, v4, v5
	s_waitcnt vmcnt(14)
	v_pk_fma_f32 v[4:5], v[154:155], v[20:21], v[6:7]
	global_store_dwordx2 v[158:159], v[2:3], off
	v_pk_fma_f32 v[2:3], v[156:157], v[18:19], v[8:9]
	v_cvt_pk_bf16_f32 v4, v4, v5
	s_mov_b64 s[30:31], 0x80000
	v_cvt_pk_bf16_f32 v5, v2, v3
	global_store_dwordx2 v[158:159], v[4:5], off offset:32
	s_waitcnt vmcnt(15)
	v_pk_fma_f32 v[4:5], v[150:151], v[24:25], v[10:11]
	v_pk_fma_f32 v[2:3], v[152:153], v[22:23], v[12:13]
	v_cvt_pk_bf16_f32 v4, v4, v5
	s_waitcnt vmcnt(13)
	v_pk_fma_f32 v[144:145], v[144:145], v[30:31], v[178:179]
	v_cvt_pk_bf16_f32 v5, v2, v3
	global_store_dwordx2 v[158:159], v[4:5], off offset:256
	v_pk_fma_f32 v[4:5], v[146:147], v[28:29], v[14:15]
	v_pk_fma_f32 v[2:3], v[148:149], v[26:27], v[16:17]
	v_cvt_pk_bf16_f32 v4, v4, v5
	v_pk_fma_f32 v[142:143], v[142:143], v[32:33], v[176:177]
	v_cvt_pk_bf16_f32 v5, v2, v3
	global_store_dwordx2 v[158:159], v[4:5], off offset:288
	s_mov_b64 s[36:37], 0x200000
	v_lshl_add_u64 v[2:3], v[174:175], 0, s[36:37]
	global_load_dwordx4 v[14:17], v[2:3], off
	global_load_dwordx4 v[10:13], v[2:3], off offset:64
	global_load_dwordx4 v[6:9], v[2:3], off offset:512
	s_nop 0
	global_load_dwordx4 v[2:5], v[2:3], off offset:576
	s_nop 0
	s_nop 0
	s_mov_b32 s23, 0x20000
	s_mov_b64 s[30:31], 0x20000
	v_add_co_u32_e32 v146, vcc, s23, v158
	v_cvt_pk_bf16_f32 v142, v142, v143
	v_cvt_pk_bf16_f32 v143, v144, v145
	v_lshl_add_u64 v[144:145], v[158:159], 0, s[30:31]
	s_nop 0
	v_addc_co_u32_e32 v147, vcc, 0, v159, vcc
	s_waitcnt vmcnt(18)
	v_pk_fma_f32 v[138:139], v[138:139], v[20:21], v[192:193]
	s_waitcnt vmcnt(17)
	v_pk_fma_f32 v[134:135], v[134:135], v[24:25], v[196:197]
	s_waitcnt vmcnt(16)
	v_pk_fma_f32 v[132:133], v[132:133], v[26:27], v[202:203]
	v_pk_fma_f32 v[130:131], v[130:131], v[28:29], v[200:201]
	s_mov_b32 s23, 0xc0000
	global_store_dwordx2 v[146:147], v[142:143], off
	v_pk_fma_f32 v[140:141], v[140:141], v[18:19], v[194:195]
	v_cvt_pk_bf16_f32 v138, v138, v139
	v_pk_fma_f32 v[136:137], v[136:137], v[22:23], v[198:199]
	v_cvt_pk_bf16_f32 v139, v140, v141
	global_store_dwordx2 v[144:145], v[138:139], off offset:32
	v_cvt_pk_bf16_f32 v134, v134, v135
	v_cvt_pk_bf16_f32 v135, v136, v137
	global_store_dwordx2 v[144:145], v[134:135], off offset:256
	v_cvt_pk_bf16_f32 v130, v130, v131
	v_cvt_pk_bf16_f32 v131, v132, v133
	global_store_dwordx2 v[144:145], v[130:131], off offset:288
	s_mov_b64 s[36:37], 0x240000
	v_lshl_add_u64 v[200:201], v[174:175], 0, s[36:37]
	global_load_dwordx4 v[176:179], v[200:201], off
	global_load_dwordx4 v[192:195], v[200:201], off offset:64
	global_load_dwordx4 v[196:199], v[200:201], off offset:512
	s_nop 0
	global_load_dwordx4 v[200:203], v[200:201], off offset:576
	s_mov_b64 s[30:31], 0xc0000
	s_nop 0
	s_mov_b32 s23, 0x200000
	s_mov_b64 s[30:31], 0x200000
	s_waitcnt vmcnt(23)
;     __device__ __forceinline__ void operator()(const f32x4 (&acc)[2][2][4][2], const Unit& u, int wr, int wc, int fr, int fq) const {
;     ...
;         ER_LOAD(B0, 0); ER_LOAD(B1, 1); ER_STORE(B0, 0); ER_LOAD(B0, 2); ER_STORE(B1, 1); ER_LOAD(B1, 3); ER_STORE(B0, 2); ER_LOAD(B0, 4); ER_STORE(B1, 3); ER_LOAD(B1, 5);
;         ER_STORE(B0, 4); ER_LOAD(B0, 6); ER_STORE(B1, 5); ER_LOAD(B1, 7); ER_STORE(B0, 6); ER_STORE(B1, 7);
	v_pk_fma_f32 v[218:219], v[128:129], v[30:31], v[218:219]
	v_pk_fma_f32 v[216:217], v[126:127], v[32:33], v[216:217]
	v_add_co_u32_e32 v126, vcc, s57, v158
	v_cvt_pk_bf16_f32 v216, v216, v217
	v_cvt_pk_bf16_f32 v217, v218, v219
	v_lshl_add_u64 v[218:219], v[158:159], 0, s[20:21]
	s_nop 0
	v_addc_co_u32_e32 v127, vcc, 0, v159, vcc
	s_waitcnt vmcnt(22)
	v_pk_fma_f32 v[212:213], v[122:123], v[20:21], v[212:213]
	s_waitcnt vmcnt(21)
	v_pk_fma_f32 v[208:209], v[118:119], v[24:25], v[208:209]
	s_waitcnt vmcnt(20)
	v_pk_fma_f32 v[206:207], v[116:117], v[26:27], v[206:207]
	v_pk_fma_f32 v[204:205], v[114:115], v[28:29], v[204:205]
	global_store_dwordx2 v[126:127], v[216:217], off
	v_pk_fma_f32 v[214:215], v[124:125], v[18:19], v[214:215]
	v_cvt_pk_bf16_f32 v212, v212, v213
	v_pk_fma_f32 v[210:211], v[120:121], v[22:23], v[210:211]
	v_cvt_pk_bf16_f32 v213, v214, v215
	global_store_dwordx2 v[218:219], v[212:213], off offset:32
	v_cvt_pk_bf16_f32 v208, v208, v209
	v_cvt_pk_bf16_f32 v209, v210, v211
	global_store_dwordx2 v[218:219], v[208:209], off offset:256
	v_cvt_pk_bf16_f32 v204, v204, v205
	v_cvt_pk_bf16_f32 v205, v206, v207
	global_store_dwordx2 v[218:219], v[204:205], off offset:288
	s_mov_b64 s[36:37], 0x280000
	v_lshl_add_u64 v[204:205], v[174:175], 0, s[36:37]
	global_load_dwordx4 v[216:219], v[204:205], off
	global_load_dwordx4 v[212:215], v[204:205], off offset:64
	global_load_dwordx4 v[208:211], v[204:205], off offset:512
	s_nop 0
	global_load_dwordx4 v[204:207], v[204:205], off offset:576
	s_nop 0
	s_mov_b32 s23, 0x60000
	s_mov_b64 s[30:31], 0x60000
	s_waitcnt vmcnt(27)
	v_pk_fma_f32 v[112:113], v[112:113], v[30:31], v[222:223]
	v_pk_fma_f32 v[110:111], v[110:111], v[32:33], v[220:221]
	v_add_co_u32_e32 v114, vcc, s23, v158
	v_cvt_pk_bf16_f32 v110, v110, v111
	v_cvt_pk_bf16_f32 v111, v112, v113
	v_lshl_add_u64 v[112:113], v[158:159], 0, s[30:31]
	s_nop 0
	v_addc_co_u32_e32 v115, vcc, 0, v159, vcc
	s_waitcnt vmcnt(26)
	v_pk_fma_f32 v[106:107], v[106:107], v[20:21], v[224:225]
	s_waitcnt vmcnt(25)
	v_pk_fma_f32 v[102:103], v[102:103], v[24:25], v[228:229]
	s_waitcnt vmcnt(24)
	v_pk_fma_f32 v[100:101], v[100:101], v[26:27], v[234:235]
	v_pk_fma_f32 v[98:99], v[98:99], v[28:29], v[232:233]
	s_mov_b32 s23, 0x240000
	global_store_dwordx2 v[114:115], v[110:111], off
	v_pk_fma_f32 v[108:109], v[108:109], v[18:19], v[226:227]
	v_cvt_pk_bf16_f32 v106, v106, v107
	v_pk_fma_f32 v[104:105], v[104:105], v[22:23], v[230:231]
	v_cvt_pk_bf16_f32 v107, v108, v109
	global_store_dwordx2 v[112:113], v[106:107], off offset:32
	v_cvt_pk_bf16_f32 v102, v102, v103
	v_cvt_pk_bf16_f32 v103, v104, v105
	global_store_dwordx2 v[112:113], v[102:103], off offset:256
	v_cvt_pk_bf16_f32 v98, v98, v99
	v_cvt_pk_bf16_f32 v99, v100, v101
	global_store_dwordx2 v[112:113], v[98:99], off offset:288
	s_mov_b64 s[36:37], 0x2c0000
	v_lshl_add_u64 v[232:233], v[174:175], 0, s[36:37]
	global_load_dwordx4 v[220:223], v[232:233], off
	global_load_dwordx4 v[224:227], v[232:233], off offset:64
	global_load_dwordx4 v[228:231], v[232:233], off offset:512
	s_nop 0
	global_load_dwordx4 v[232:235], v[232:233], off offset:576
	s_mov_b64 s[30:31], 0x240000
	s_nop 0
	s_mov_b32 s23, 0x100000
	s_mov_b64 s[30:31], 0x100000
	s_waitcnt vmcnt(27)
	v_pk_fma_f32 v[16:17], v[96:97], v[30:31], v[16:17]
	v_pk_fma_f32 v[14:15], v[94:95], v[32:33], v[14:15]
	v_add_co_u32_e32 v94, vcc, s23, v158
	v_cvt_pk_bf16_f32 v14, v14, v15
	v_cvt_pk_bf16_f32 v15, v16, v17
	v_lshl_add_u64 v[16:17], v[158:159], 0, s[30:31]
	s_nop 0
	v_addc_co_u32_e32 v95, vcc, 0, v159, vcc
	s_waitcnt vmcnt(26)
	v_pk_fma_f32 v[10:11], v[90:91], v[20:21], v[10:11]
	s_waitcnt vmcnt(25)
	v_pk_fma_f32 v[6:7], v[86:87], v[24:25], v[6:7]
	s_waitcnt vmcnt(24)
	v_pk_fma_f32 v[4:5], v[84:85], v[26:27], v[4:5]
	v_pk_fma_f32 v[2:3], v[82:83], v[28:29], v[2:3]
	s_mov_b32 s23, 0x280000
	global_store_dwordx2 v[94:95], v[14:15], off
	v_pk_fma_f32 v[12:13], v[92:93], v[18:19], v[12:13]
	v_cvt_pk_bf16_f32 v10, v10, v11
	v_pk_fma_f32 v[8:9], v[88:89], v[22:23], v[8:9]
	v_cvt_pk_bf16_f32 v11, v12, v13
	global_store_dwordx2 v[16:17], v[10:11], off offset:32
	v_cvt_pk_bf16_f32 v6, v6, v7
	v_cvt_pk_bf16_f32 v7, v8, v9
	global_store_dwordx2 v[16:17], v[6:7], off offset:256
	v_cvt_pk_bf16_f32 v2, v2, v3
	v_cvt_pk_bf16_f32 v3, v4, v5
	s_mov_b64 s[30:31], 0x280000
	global_store_dwordx2 v[16:17], v[2:3], off offset:288
	s_nop 0
	s_mov_b32 s23, 0x120000
	s_mov_b64 s[30:31], 0x120000
	s_waitcnt vmcnt(23)
;     __device__ __forceinline__ void operator()(const f32x4 (&acc)[2][2][4][2], const Unit& u, int wr, int wc, int fr, int fq) const {
;     ...
;         ER_LOAD(B0, 0); ER_LOAD(B1, 1); ER_STORE(B0, 0); ER_LOAD(B0, 2); ER_STORE(B1, 1); ER_LOAD(B1, 3); ER_STORE(B0, 2); ER_LOAD(B0, 4); ER_STORE(B1, 3); ER_LOAD(B1, 5);
;         ER_STORE(B0, 4); ER_LOAD(B0, 6); ER_STORE(B1, 5); ER_LOAD(B1, 7); ER_STORE(B0, 6); ER_STORE(B1, 7);
	v_pk_fma_f32 v[80:81], v[80:81], v[30:31], v[178:179]
	v_pk_fma_f32 v[78:79], v[78:79], v[32:33], v[176:177]
	v_add_co_u32_e32 v82, vcc, s23, v158
	v_cvt_pk_bf16_f32 v78, v78, v79
	v_cvt_pk_bf16_f32 v79, v80, v81
	v_lshl_add_u64 v[80:81], v[158:159], 0, s[30:31]
	s_nop 0
	v_addc_co_u32_e32 v83, vcc, 0, v159, vcc
	s_waitcnt vmcnt(22)
	v_pk_fma_f32 v[74:75], v[74:75], v[20:21], v[192:193]
	s_waitcnt vmcnt(21)
	v_pk_fma_f32 v[70:71], v[70:71], v[24:25], v[196:197]
	s_waitcnt vmcnt(20)
	v_pk_fma_f32 v[68:69], v[68:69], v[26:27], v[202:203]
	v_pk_fma_f32 v[66:67], v[66:67], v[28:29], v[200:201]
	s_mov_b32 s23, 0x2c0000
	global_store_dwordx2 v[82:83], v[78:79], off
	v_pk_fma_f32 v[76:77], v[76:77], v[18:19], v[194:195]
	v_cvt_pk_bf16_f32 v74, v74, v75
	v_pk_fma_f32 v[72:73], v[72:73], v[22:23], v[198:199]
	v_cvt_pk_bf16_f32 v75, v76, v77
	global_store_dwordx2 v[80:81], v[74:75], off offset:32
	v_cvt_pk_bf16_f32 v70, v70, v71
	v_cvt_pk_bf16_f32 v71, v72, v73
	global_store_dwordx2 v[80:81], v[70:71], off offset:256
	v_cvt_pk_bf16_f32 v66, v66, v67
	v_cvt_pk_bf16_f32 v67, v68, v69
	global_store_dwordx2 v[80:81], v[66:67], off offset:288
	s_mov_b64 s[30:31], 0x2c0000
	s_nop 0
	s_mov_b32 s23, 0x140000
	s_mov_b64 s[30:31], 0x140000
	s_waitcnt vmcnt(19)
	v_pk_fma_f32 v[218:219], v[64:65], v[30:31], v[218:219]
	v_pk_fma_f32 v[216:217], v[62:63], v[32:33], v[216:217]
	v_add_co_u32_e32 v62, vcc, s23, v158
	v_cvt_pk_bf16_f32 v216, v216, v217
	v_cvt_pk_bf16_f32 v217, v218, v219
	v_lshl_add_u64 v[218:219], v[158:159], 0, s[30:31]
	s_nop 0
	v_addc_co_u32_e32 v63, vcc, 0, v159, vcc
	s_waitcnt vmcnt(18)
	v_pk_fma_f32 v[212:213], v[58:59], v[20:21], v[212:213]
	s_waitcnt vmcnt(17)
	v_pk_fma_f32 v[208:209], v[50:51], v[24:25], v[208:209]
	global_store_dwordx2 v[62:63], v[216:217], off
	v_pk_fma_f32 v[214:215], v[60:61], v[18:19], v[214:215]
	v_cvt_pk_bf16_f32 v212, v212, v213
	s_mov_b32 s23, 0x160000
	v_cvt_pk_bf16_f32 v213, v214, v215
	global_store_dwordx2 v[218:219], v[212:213], off offset:32
	v_cvt_pk_bf16_f32 v208, v208, v209
	v_pk_fma_f32 v[210:211], v[52:53], v[22:23], v[210:211]
	s_waitcnt vmcnt(18)
	v_pk_fma_f32 v[206:207], v[48:49], v[26:27], v[206:207]
	v_cvt_pk_bf16_f32 v209, v210, v211
	global_store_dwordx2 v[218:219], v[208:209], off offset:256
	v_pk_fma_f32 v[204:205], v[46:47], v[28:29], v[204:205]
	v_add_co_u32_e32 v6, vcc, s23, v158
	v_cvt_pk_bf16_f32 v204, v204, v205
	v_cvt_pk_bf16_f32 v205, v206, v207
	global_store_dwordx2 v[218:219], v[204:205], off offset:288
	s_nop 0
	v_addc_co_u32_e32 v7, vcc, 0, v159, vcc
	s_mov_b64 s[30:31], 0x160000
	s_andn2_b64 vcc, exec, s[2:3]
	s_waitcnt vmcnt(15)
	v_pk_fma_f32 v[4:5], v[54:55], v[32:33], v[220:221]
	v_pk_fma_f32 v[2:3], v[56:57], v[30:31], v[222:223]
	v_cvt_pk_bf16_f32 v4, v4, v5
	s_nop 0
	v_cvt_pk_bf16_f32 v5, v2, v3
	global_store_dwordx2 v[6:7], v[4:5], off
	s_waitcnt vmcnt(15)
	v_pk_fma_f32 v[6:7], v[42:43], v[20:21], v[224:225]
	v_lshl_add_u64 v[2:3], v[158:159], 0, s[30:31]
	v_pk_fma_f32 v[4:5], v[44:45], v[18:19], v[226:227]
	v_cvt_pk_bf16_f32 v6, v6, v7
	s_mov_b64 s[30:31], -1
	v_cvt_pk_bf16_f32 v7, v4, v5
	global_store_dwordx2 v[2:3], v[6:7], off offset:32
	s_waitcnt vmcnt(15)
	v_pk_fma_f32 v[6:7], v[38:39], v[24:25], v[228:229]
	v_pk_fma_f32 v[4:5], v[40:41], v[22:23], v[230:231]
	v_cvt_pk_bf16_f32 v6, v6, v7
	s_nop 0
	v_cvt_pk_bf16_f32 v7, v4, v5
	global_store_dwordx2 v[2:3], v[6:7], off offset:256
	s_waitcnt vmcnt(15)
	v_pk_fma_f32 v[6:7], v[34:35], v[28:29], v[232:233]
	v_pk_fma_f32 v[4:5], v[36:37], v[26:27], v[234:235]
	v_cvt_pk_bf16_f32 v6, v6, v7
	s_nop 0
	v_cvt_pk_bf16_f32 v7, v4, v5
	global_store_dwordx2 v[2:3], v[6:7], off offset:288
	s_cbranch_vccnz .LBB0_2074
	s_andn2_b64 vcc, exec, s[0:1]
	s_cbranch_vccnz .LBB0_2073
	s_barrier
	s_branch .LBB0_2073

; #define GAS __attribute__((address_space(1)))
; #define CV_LOAD(G_, V_, r0_) do { _Pragma("unroll") for (int i_ = 0; i_ < 8; ++i_) { G_[i_] = *(const GAS v2u*)(ap + (size_t)((r0_) + i_) * F2); V_[i_] = *(const GAS v2u*)(ap + (size_t)((r0_) + i_) * F2 + 128); } } while (0)
; __device__ __forceinline__ void conv_phase(Frame& F) {
;     ...
;         for (int j = 0; j < 3; ++j) { const f32x4 a = *(const GAS f32x4*)(F.cvw + (size_t)j * F2 + ch) * (1.f / S_A), b = *(const GAS f32x4*)(F.cvw + (size_t)j * F2 + ch + 4) * (1.f / S_A);
;             const f32x4 c = *(const GAS f32x4*)(F.cvw + (size_t)j * F2 + DFF + ch) * (1.f / S_A), d = *(const GAS f32x4*)(F.cvw + (size_t)j * F2 + DFF + ch + 4) * (1.f / S_A);
;             wg[j][0] = (f32x2){a.x, a.y}; wg[j][1] = (f32x2){a.z, a.w}; wg[j][2] = (f32x2){b.x, b.y}; wg[j][3] = (f32x2){b.z, b.w};
;             wv[j][0] = (f32x2){c.x, c.y}; wv[j][1] = (f32x2){c.z, c.w}; wv[j][2] = (f32x2){d.x, d.y}; wv[j][3] = (f32x2){d.z, d.w}; }
;         { const f32x4 a = *(const GAS f32x4*)(F.cvb + ch), b = *(const GAS f32x4*)(F.cvb + ch + 4), c = *(const GAS f32x4*)(F.cvb + DFF + ch), d = *(const GAS f32x4*)(F.cvb + DFF + ch + 4);
;           bg[0] = (f32x2){a.x, a.y}; bg[1] = (f32x2){a.z, a.w}; bg[2] = (f32x2){b.x, b.y}; bg[3] = (f32x2){b.z, b.w}; bv[0] = (f32x2){c.x, c.y}; bv[1] = (f32x2){c.z, c.w}; bv[2] = (f32x2){d.x, d.y}; bv[3] = (f32x2){d.z, d.w}; }
;         f32x2 g1[4], g2[4], v1[4], v2[4];
;         const bool first = (t0 & (SEQ - 1)) == 0;
;         const unsigned char* ap = (const unsigned char*)F.A + (size_t)t0 * F2 + acol;
;         if (first) {
; #pragma unroll
;             for (int e = 0; e < 4; ++e) { g1[e] = g2[e] = v1[e] = v2[e] = (f32x2){0.f, 0.f}; }
;         } else {
;             const v2u ga = *(const GAS v2u*)(ap - F2), gb = *(const GAS v2u*)(ap - 2 * (size_t)F2), va = *(const GAS v2u*)(ap - F2 + 128), vb = *(const GAS v2u*)(ap - 2 * (size_t)F2 + 128);
;             unpack8_fp8(ga, g1); unpack8_fp8(gb, g2); unpack8_fp8(va, v1); unpack8_fp8(vb, v2);
;         }
;         v2u GA[8], VA[8], GB[8], VB[8];
;     ...
;         CV_LOAD(GA, VA, 0); CV_LOAD(GB, VB, 8); CV_COMP(GA, VA, 0); CV_LOAD(GA, VA, 16); CV_COMP(GB, VB, 8); CV_LOAD(GB, VB, 24); CV_COMP(GA, VA, 16); CV_COMP(GB, VB, 24);
.LBB0_2568:
	s_or_b64 exec, exec, s[22:23]
	v_add_co_u32_e32 v74, vcc, s25, v72
	s_waitcnt vmcnt(14)
	v_pk_mul_f32 v[62:63], v[62:63], s[44:45] op_sel_hi:[1,0]
	v_addc_co_u32_e32 v75, vcc, 0, v73, vcc
	global_load_dwordx2 v[160:161], v[72:73], off nt
	global_load_dwordx2 v[176:177], v[72:73], off offset:128 nt
	global_load_dwordx2 v[182:183], v[74:75], off offset:1536 nt
	global_load_dwordx2 v[170:171], v[74:75], off offset:1664 nt
	v_add_co_u32_e32 v74, vcc, s26, v72
	s_waitcnt vmcnt(14)
	v_pk_mul_f32 v[50:51], v[50:51], s[44:45] op_sel_hi:[1,0]
	v_addc_co_u32_e32 v75, vcc, 0, v73, vcc
	v_add_co_u32_e32 v76, vcc, s27, v72
	s_waitcnt vmcnt(6)
	v_pk_mul_f32 v[14:15], v[14:15], s[82:83] op_sel_hi:[1,0]
	s_nop 0
	v_pk_fma_f32 v[152:153], v[62:63], v[152:153], v[14:15]
	v_addc_co_u32_e32 v77, vcc, 0, v73, vcc
	global_load_dwordx2 v[156:157], v[74:75], off offset:3072 nt
	global_load_dwordx2 v[154:155], v[74:75], off offset:3200 nt
	global_load_dwordx2 v[140:141], v[76:77], off offset:512 nt
	global_load_dwordx2 v[138:139], v[76:77], off offset:640 nt
	v_add_co_u32_e32 v74, vcc, s28, v72
	v_pk_mul_f32 v[34:35], v[34:35], s[44:45] op_sel_hi:[1,0]
	s_nop 0
	v_addc_co_u32_e32 v75, vcc, 0, v73, vcc
	v_add_co_u32_e32 v76, vcc, s29, v72
	v_pk_fma_f32 v[152:153], v[50:51], v[132:133], v[152:153]
	s_nop 0
	v_addc_co_u32_e32 v77, vcc, 0, v73, vcc
	global_load_dwordx2 v[104:105], v[74:75], off offset:2048 nt
	global_load_dwordx2 v[100:101], v[74:75], off offset:2176 nt
	global_load_dwordx2 v[96:97], v[76:77], off offset:3584 nt
	global_load_dwordx2 v[92:93], v[76:77], off offset:3712 nt
	v_add_co_u32_e32 v74, vcc, s30, v72
	v_pk_mul_f32 v[64:65], v[64:65], s[44:45] op_sel_hi:[1,0]
	s_nop 0
	v_addc_co_u32_e32 v75, vcc, 0, v73, vcc
	v_add_co_u32_e32 v76, vcc, s31, v72
	v_pk_mul_f32 v[52:53], v[52:53], s[44:45] op_sel_hi:[1,0]
	s_nop 0
	v_addc_co_u32_e32 v77, vcc, 0, v73, vcc
	global_load_dwordx2 v[88:89], v[74:75], off offset:1024 nt
	global_load_dwordx2 v[84:85], v[74:75], off offset:1152 nt
	global_load_dwordx2 v[80:81], v[76:77], off offset:2560 nt
	s_nop 0
	global_load_dwordx2 v[76:77], v[76:77], off offset:2688 nt
	v_add_co_u32_e32 v74, vcc, s33, v72
	v_pk_mul_f32 v[16:17], v[16:17], s[82:83] op_sel_hi:[1,0]
	s_nop 0
	v_pk_fma_f32 v[148:149], v[64:65], v[148:149], v[16:17]
	s_nop 0
	v_addc_co_u32_e32 v75, vcc, 0, v73, vcc
	v_add_co_u32_e32 v78, vcc, s34, v72
	v_pk_mul_f32 v[36:37], v[36:37], s[44:45] op_sel_hi:[1,0]
	s_nop 0
	v_addc_co_u32_e32 v79, vcc, 0, v73, vcc
	global_load_dwordx2 v[134:135], v[74:75], off nt
	global_load_dwordx2 v[130:131], v[74:75], off offset:128 nt
	global_load_dwordx2 v[126:127], v[78:79], off offset:1536 nt
	global_load_dwordx2 v[122:123], v[78:79], off offset:1664 nt
	v_add_co_u32_e32 v74, vcc, s35, v72
	v_pk_fma_f32 v[148:149], v[52:53], v[124:125], v[148:149]
	s_nop 0
	v_addc_co_u32_e32 v75, vcc, 0, v73, vcc
	v_add_co_u32_e32 v78, vcc, s36, v72
	v_pk_mul_f32 v[58:59], v[58:59], s[80:81] op_sel_hi:[1,0]
	s_nop 0
	v_addc_co_u32_e32 v79, vcc, 0, v73, vcc
	global_load_dwordx2 v[118:119], v[74:75], off offset:3072 nt
	global_load_dwordx2 v[114:115], v[74:75], off offset:3200 nt
	global_load_dwordx2 v[110:111], v[78:79], off offset:512 nt
	global_load_dwordx2 v[106:107], v[78:79], off offset:640 nt
	v_add_co_u32_e32 v74, vcc, s37, v72
	v_pk_mul_f32 v[42:43], v[42:43], s[80:81] op_sel_hi:[1,0]
	s_nop 0
	v_addc_co_u32_e32 v75, vcc, 0, v73, vcc
	v_add_co_u32_e32 v78, vcc, s38, v72
	s_waitcnt vmcnt(24)
	v_pk_mul_f32 v[10:11], v[10:11], s[94:95] op_sel_hi:[1,0]
	s_nop 0
	v_pk_fma_f32 v[158:159], v[58:59], v[158:159], v[10:11]
	v_addc_co_u32_e32 v79, vcc, 0, v73, vcc
	global_load_dwordx2 v[102:103], v[74:75], off offset:2048 nt
	global_load_dwordx2 v[98:99], v[74:75], off offset:2176 nt
	global_load_dwordx2 v[94:95], v[78:79], off offset:3584 nt
	global_load_dwordx2 v[90:91], v[78:79], off offset:3712 nt
	v_add_co_u32_e32 v74, vcc, s39, v72
	v_pk_mul_f32 v[26:27], v[26:27], s[80:81] op_sel_hi:[1,0]
	s_nop 0
	v_addc_co_u32_e32 v75, vcc, 0, v73, vcc
	v_add_co_u32_e32 v162, vcc, s40, v72
	v_pk_fma_f32 v[158:159], v[42:43], v[136:137], v[158:159]
	s_nop 0
	v_addc_co_u32_e32 v163, vcc, 0, v73, vcc
	s_waitcnt vmcnt(27)
	v_cvt_pk_f32_fp8_e32 v[178:179], v160
	v_cvt_pk_f32_fp8_sdwa v[168:169], v160 src0_sel:WORD_1
	s_waitcnt vmcnt(26)
; __device__ __forceinline__ float clamp448(float x) { return __builtin_amdgcn_fmed3f(x, -448.f, 448.f); }
; __device__ __forceinline__ unsigned pk4_fp8(float a, float b, float c, float d) {
;     int w = __builtin_amdgcn_cvt_pk_fp8_f32(clamp448(a), clamp448(b), 0, false);
;     w = __builtin_amdgcn_cvt_pk_fp8_f32(clamp448(c), clamp448(d), w, true);
;     return (unsigned)w;
; }
	v_cvt_pk_f32_fp8_e32 v[172:173], v176
	v_cvt_pk_f32_fp8_sdwa v[166:167], v176 src0_sel:WORD_1
	v_pk_fma_f32 v[180:181], v[34:35], v[178:179], v[152:153]
	global_load_dwordx2 v[86:87], v[74:75], off offset:1024 nt
	global_load_dwordx2 v[82:83], v[74:75], off offset:1152 nt
	global_load_dwordx2 v[78:79], v[162:163], off offset:2560 nt
	s_nop 0
	global_load_dwordx2 v[74:75], v[162:163], off offset:2688 nt
	v_exp_f32_e32 v175, v180
	v_exp_f32_e32 v184, v181
	v_cvt_pk_f32_fp8_e32 v[162:163], v177
	v_add_f32_e32 v175, 1.0, v175
	v_rcp_f32_e32 v176, v175
	v_add_f32_e32 v175, 1.0, v184
	v_cvt_pk_f32_fp8_sdwa v[152:153], v177 src0_sel:WORD_1
	v_rcp_f32_e32 v177, v175
	v_pk_fma_f32 v[148:149], v[36:37], v[168:169], v[148:149]
	v_pk_fma_f32 v[158:159], v[26:27], v[172:173], v[158:159]
	v_pk_mul_f32 v[176:177], v[180:181], v[176:177]
	v_exp_f32_e32 v175, v148
	v_exp_f32_e32 v180, v149
	v_add_f32_e32 v175, 1.0, v175
	v_cvt_pk_f32_fp8_e32 v[164:165], v161
	v_pk_mul_f32 v[158:159], v[158:159], v[176:177]
	v_rcp_f32_e32 v176, v175
	v_add_f32_e32 v175, 1.0, v180
	v_pk_mul_f32 v[54:55], v[54:55], s[44:45] op_sel_hi:[1,0]
	v_rcp_f32_e32 v177, v175
	v_pk_mul_f32 v[38:39], v[38:39], s[44:45] op_sel_hi:[1,0]
	v_pk_mul_f32 v[6:7], v[6:7], s[82:83] op_sel_hi:[1,0]
	s_nop 0
	v_pk_fma_f32 v[144:145], v[54:55], v[144:145], v[6:7]
	v_pk_mul_f32 v[22:23], v[22:23], s[44:45] op_sel_hi:[1,0]
	v_pk_fma_f32 v[144:145], v[38:39], v[116:117], v[144:145]
	v_pk_mul_f32 v[60:61], v[60:61], s[80:81] op_sel_hi:[1,0]
	v_pk_fma_f32 v[144:145], v[22:23], v[164:165], v[144:145]
	v_pk_mul_f32 v[148:149], v[148:149], v[176:177]
	v_pk_mul_f32 v[44:45], v[44:45], s[80:81] op_sel_hi:[1,0]
	v_pk_mul_f32 v[12:13], v[12:13], s[94:95] op_sel_hi:[1,0]
	s_nop 0
	v_pk_fma_f32 v[150:151], v[60:61], v[150:151], v[12:13]
	v_exp_f32_e32 v175, v144
	v_exp_f32_e32 v176, v145
	v_pk_mul_f32 v[28:29], v[28:29], s[80:81] op_sel_hi:[1,0]
	v_pk_fma_f32 v[150:151], v[44:45], v[128:129], v[150:151]
	v_cvt_pk_f32_fp8_sdwa v[160:161], v161 src0_sel:WORD_1
	v_pk_fma_f32 v[150:151], v[28:29], v[166:167], v[150:151]
	v_pk_mul_f32 v[56:57], v[56:57], s[44:45] op_sel_hi:[1,0]
	v_pk_mul_f32 v[40:41], v[40:41], s[44:45] op_sel_hi:[1,0]
	v_pk_mul_f32 v[148:149], v[150:151], v[148:149]
	v_add_f32_e32 v150, 1.0, v175
	v_add_f32_e32 v151, 1.0, v176
	v_rcp_f32_e32 v150, v150
	v_rcp_f32_e32 v151, v151
	v_pk_mul_f32 v[8:9], v[8:9], s[82:83] op_sel_hi:[1,0]
	s_nop 0
	v_pk_fma_f32 v[70:71], v[56:57], v[70:71], v[8:9]
	v_pk_mul_f32 v[24:25], v[24:25], s[44:45] op_sel_hi:[1,0]
	v_pk_fma_f32 v[70:71], v[40:41], v[108:109], v[70:71]
	v_pk_mul_f32 v[46:47], v[46:47], s[80:81] op_sel_hi:[1,0]
	v_pk_fma_f32 v[70:71], v[24:25], v[160:161], v[70:71]
	v_pk_mul_f32 v[144:145], v[144:145], v[150:151]
	v_pk_mul_f32 v[30:31], v[30:31], s[80:81] op_sel_hi:[1,0]
	v_pk_mul_f32 v[2:3], v[2:3], s[94:95] op_sel_hi:[1,0]
	s_nop 0
	v_pk_fma_f32 v[146:147], v[46:47], v[146:147], v[2:3]
	v_exp_f32_e32 v150, v70
	v_exp_f32_e32 v151, v71
	v_pk_mul_f32 v[18:19], v[18:19], s[80:81] op_sel_hi:[1,0]
	v_pk_fma_f32 v[146:147], v[30:31], v[120:121], v[146:147]
	v_pk_mul_f32 v[48:49], v[48:49], s[80:81] op_sel_hi:[1,0]
	v_pk_fma_f32 v[146:147], v[18:19], v[162:163], v[146:147]
	v_pk_mul_f32 v[32:33], v[32:33], s[80:81] op_sel_hi:[1,0]
	v_pk_mul_f32 v[4:5], v[4:5], s[94:95] op_sel_hi:[1,0]
	s_nop 0
	v_pk_fma_f32 v[142:143], v[48:49], v[142:143], v[4:5]
	v_pk_mul_f32 v[144:145], v[146:147], v[144:145]
	v_add_f32_e32 v146, 1.0, v150
	v_add_f32_e32 v147, 1.0, v151
	v_rcp_f32_e32 v146, v146
	v_rcp_f32_e32 v147, v147
	v_pk_mul_f32 v[20:21], v[20:21], s[80:81] op_sel_hi:[1,0]
	v_pk_fma_f32 v[142:143], v[32:33], v[112:113], v[142:143]
	v_med3_f32 v144, v144, s41, v1
	v_pk_fma_f32 v[142:143], v[20:21], v[152:153], v[142:143]
	v_pk_mul_f32 v[70:71], v[70:71], v[146:147]
	v_med3_f32 v146, v159, s41, v1
	v_pk_mul_f32 v[70:71], v[142:143], v[70:71]
	v_med3_f32 v143, v158, s41, v1
	v_cvt_pk_fp8_f32 v142, v143, v146
	v_med3_f32 v145, v145, s41, v1
	v_cvt_pk_fp8_f32 v143, v144, v145
	s_waitcnt vmcnt(29)
	v_cvt_pk_f32_fp8_e32 v[180:181], v182
	v_med3_f32 v70, v70, s41, v1
	v_med3_f32 v71, v71, s41, v1
	v_pk_fma_f32 v[132:133], v[62:63], v[132:133], v[14:15]
	v_cvt_pk_fp8_f32 v143, v70, v71 op_sel:[0,0,1]
	v_mul_u32_u24_e32 v70, 0x56000, v174
	v_mov_b32_e32 v71, v69
	v_pk_fma_f32 v[132:133], v[50:51], v[178:179], v[132:133]
	v_med3_f32 v146, v148, s41, v1
	v_med3_f32 v147, v149, s41, v1
	v_lshl_add_u64 v[70:71], s[4:5], 0, v[70:71]
	v_pk_fma_f32 v[148:149], v[34:35], v[180:181], v[132:133]
	v_lshl_add_u64 v[70:71], v[70:71], 0, v[68:69]
	v_exp_f32_e32 v68, v148
	v_exp_f32_e32 v176, v149
	v_cvt_pk_f32_fp8_sdwa v[158:159], v182 src0_sel:WORD_1
	v_add_f32_e32 v68, 1.0, v68
	s_waitcnt vmcnt(28)
; __device__ __forceinline__ float clamp448(float x) { return __builtin_amdgcn_fmed3f(x, -448.f, 448.f); }
; __device__ __forceinline__ unsigned pk4_fp8(float a, float b, float c, float d) {
;     int w = __builtin_amdgcn_cvt_pk_fp8_f32(clamp448(a), clamp448(b), 0, false);
;     w = __builtin_amdgcn_cvt_pk_fp8_f32(clamp448(c), clamp448(d), w, true);
;     return (unsigned)w;
; }
	v_cvt_pk_f32_fp8_e32 v[174:175], v170
	v_cvt_pk_f32_fp8_sdwa v[150:151], v170 src0_sel:WORD_1
	v_rcp_f32_e32 v170, v68
	v_add_f32_e32 v68, 1.0, v176
	v_cvt_pk_f32_fp8_e32 v[144:145], v171
	v_cvt_pk_f32_fp8_sdwa v[132:133], v171 src0_sel:WORD_1
	v_rcp_f32_e32 v171, v68
	v_pk_fma_f32 v[124:125], v[64:65], v[124:125], v[16:17]
	v_pk_fma_f32 v[136:137], v[58:59], v[136:137], v[10:11]
	v_pk_fma_f32 v[124:125], v[52:53], v[168:169], v[124:125]
	v_pk_mul_f32 v[148:149], v[148:149], v[170:171]
	v_pk_fma_f32 v[124:125], v[36:37], v[158:159], v[124:125]
	v_pk_fma_f32 v[136:137], v[42:43], v[172:173], v[136:137]
	v_exp_f32_e32 v68, v124
	v_exp_f32_e32 v170, v125
	v_pk_fma_f32 v[136:137], v[26:27], v[174:175], v[136:137]
	v_cvt_pk_fp8_f32 v142, v146, v147 op_sel:[0,0,1]
	v_cvt_pk_f32_fp8_e32 v[146:147], v183
	v_add_f32_e32 v68, 1.0, v68
	v_pk_mul_f32 v[136:137], v[136:137], v[148:149]
	v_rcp_f32_e32 v148, v68
	v_add_f32_e32 v68, 1.0, v170
	v_rcp_f32_e32 v149, v68
	v_pk_fma_f32 v[116:117], v[54:55], v[116:117], v[6:7]
	v_pk_fma_f32 v[128:129], v[60:61], v[128:129], v[12:13]
	v_pk_fma_f32 v[116:117], v[38:39], v[164:165], v[116:117]
	v_pk_mul_f32 v[124:125], v[124:125], v[148:149]
	v_pk_fma_f32 v[116:117], v[22:23], v[146:147], v[116:117]
	v_pk_fma_f32 v[128:129], v[44:45], v[166:167], v[128:129]
	v_exp_f32_e32 v68, v116
	v_exp_f32_e32 v148, v117
	v_pk_fma_f32 v[128:129], v[28:29], v[150:151], v[128:129]
	global_store_dwordx2 v[70:71], v[142:143], off
	v_cvt_pk_f32_fp8_sdwa v[142:143], v183 src0_sel:WORD_1
	v_add_f32_e32 v68, 1.0, v68
	v_pk_mul_f32 v[124:125], v[128:129], v[124:125]
	v_rcp_f32_e32 v128, v68
	v_add_f32_e32 v68, 1.0, v148
	v_rcp_f32_e32 v129, v68
	v_pk_fma_f32 v[108:109], v[56:57], v[108:109], v[8:9]
	v_pk_fma_f32 v[120:121], v[46:47], v[120:121], v[2:3]
	v_pk_fma_f32 v[108:109], v[40:41], v[160:161], v[108:109]
	v_pk_mul_f32 v[116:117], v[116:117], v[128:129]
	v_pk_fma_f32 v[108:109], v[24:25], v[142:143], v[108:109]
	v_pk_fma_f32 v[120:121], v[30:31], v[162:163], v[120:121]
	v_exp_f32_e32 v68, v108
	v_exp_f32_e32 v128, v109
	v_pk_fma_f32 v[120:121], v[18:19], v[144:145], v[120:121]
	v_add_f32_e32 v68, 1.0, v68
	v_pk_fma_f32 v[112:113], v[48:49], v[112:113], v[4:5]
	v_pk_mul_f32 v[116:117], v[120:121], v[116:117]
	v_rcp_f32_e32 v120, v68
	v_add_f32_e32 v68, 1.0, v128
	v_rcp_f32_e32 v121, v68
	v_pk_fma_f32 v[112:113], v[32:33], v[152:153], v[112:113]
	v_med3_f32 v68, v136, s41, v1
	v_pk_fma_f32 v[112:113], v[20:21], v[132:133], v[112:113]
	v_pk_mul_f32 v[108:109], v[108:109], v[120:121]
	v_med3_f32 v116, v116, s41, v1
	v_pk_mul_f32 v[108:109], v[112:113], v[108:109]
	v_med3_f32 v113, v137, s41, v1
	v_cvt_pk_fp8_f32 v112, v68, v113
	v_med3_f32 v117, v117, s41, v1
	v_cvt_pk_fp8_f32 v113, v116, v117
	v_med3_f32 v68, v124, s41, v1
	v_med3_f32 v120, v125, s41, v1
	v_cvt_pk_fp8_f32 v112, v68, v120 op_sel:[0,0,1]
	v_med3_f32 v68, v108, s41, v1
	v_med3_f32 v108, v109, s41, v1
	v_cvt_pk_fp8_f32 v113, v68, v108 op_sel:[0,0,1]
	v_add_co_u32_e32 v108, vcc, s43, v70
	s_waitcnt vmcnt(28)
	v_cvt_pk_f32_fp8_e32 v[182:183], v156
	v_addc_co_u32_e32 v109, vcc, 0, v71, vcc
	global_store_dwordx2 v[108:109], v[112:113], off offset:2816
	v_pk_fma_f32 v[112:113], v[62:63], v[178:179], v[14:15]
	s_waitcnt vmcnt(28)
	v_cvt_pk_f32_fp8_e32 v[176:177], v154
	v_pk_fma_f32 v[112:113], v[50:51], v[180:181], v[112:113]
	v_pk_fma_f32 v[128:129], v[58:59], v[172:173], v[10:11]
	v_pk_fma_f32 v[112:113], v[34:35], v[182:183], v[112:113]
	v_cvt_pk_f32_fp8_sdwa v[170:171], v156 src0_sel:WORD_1
	v_exp_f32_e32 v68, v112
	v_exp_f32_e32 v121, v113
	v_pk_fma_f32 v[128:129], v[42:43], v[174:175], v[128:129]
	v_add_f32_e32 v68, 1.0, v68
	v_rcp_f32_e32 v120, v68
	v_add_f32_e32 v68, 1.0, v121
	v_rcp_f32_e32 v121, v68
	v_pk_fma_f32 v[128:129], v[26:27], v[176:177], v[128:129]
	v_cvt_pk_f32_fp8_e32 v[136:137], v157
	v_cvt_pk_f32_fp8_sdwa v[108:109], v157 src0_sel:WORD_1
	v_pk_mul_f32 v[112:113], v[112:113], v[120:121]
	s_nop 0
	v_pk_mul_f32 v[112:113], v[128:129], v[112:113]
	v_pk_fma_f32 v[128:129], v[64:65], v[168:169], v[16:17]
	v_cvt_pk_f32_fp8_sdwa v[156:157], v154 src0_sel:WORD_1
	v_pk_fma_f32 v[128:129], v[52:53], v[158:159], v[128:129]
	s_nop 0
	v_pk_fma_f32 v[128:129], v[36:37], v[170:171], v[128:129]
	v_cvt_pk_f32_fp8_e32 v[124:125], v155
	v_exp_f32_e32 v68, v128
	v_exp_f32_e32 v148, v129
	v_cvt_pk_f32_fp8_sdwa v[116:117], v155 src0_sel:WORD_1
	v_add_f32_e32 v68, 1.0, v68
	v_rcp_f32_e32 v120, v68
	v_add_f32_e32 v68, 1.0, v148
	v_rcp_f32_e32 v121, v68
	v_pk_fma_f32 v[148:149], v[60:61], v[166:167], v[12:13]
	v_pk_fma_f32 v[152:153], v[48:49], v[152:153], v[4:5]
	v_pk_fma_f32 v[148:149], v[44:45], v[150:151], v[148:149]
	v_pk_mul_f32 v[120:121], v[128:129], v[120:121]
	v_pk_fma_f32 v[148:149], v[28:29], v[156:157], v[148:149]
	v_med3_f32 v113, v113, s41, v1
	v_pk_mul_f32 v[120:121], v[148:149], v[120:121]
	v_pk_fma_f32 v[148:149], v[54:55], v[164:165], v[6:7]
	s_nop 0
	v_pk_fma_f32 v[148:149], v[38:39], v[146:147], v[148:149]
	v_pk_fma_f32 v[152:153], v[32:33], v[132:133], v[152:153]
	v_pk_fma_f32 v[148:149], v[22:23], v[136:137], v[148:149]
	v_pk_fma_f32 v[152:153], v[20:21], v[116:117], v[152:153]
	v_exp_f32_e32 v68, v148
	v_exp_f32_e32 v154, v149
	v_add_f32_e32 v68, 1.0, v68
	v_rcp_f32_e32 v128, v68
	v_add_f32_e32 v68, 1.0, v154
	v_rcp_f32_e32 v129, v68
	v_pk_fma_f32 v[154:155], v[46:47], v[162:163], v[2:3]
	s_waitcnt vmcnt(27)
	v_cvt_pk_f32_fp8_e32 v[168:169], v140
	v_pk_fma_f32 v[154:155], v[30:31], v[144:145], v[154:155]
	v_pk_mul_f32 v[128:129], v[148:149], v[128:129]
	v_pk_fma_f32 v[154:155], v[18:19], v[124:125], v[154:155]
	s_waitcnt vmcnt(26)
; __device__ __forceinline__ float clamp448(float x) { return __builtin_amdgcn_fmed3f(x, -448.f, 448.f); }
; __device__ __forceinline__ unsigned pk4_fp8(float a, float b, float c, float d) {
;     int w = __builtin_amdgcn_cvt_pk_fp8_f32(clamp448(a), clamp448(b), 0, false);
;     w = __builtin_amdgcn_cvt_pk_fp8_f32(clamp448(c), clamp448(d), w, true);
;     return (unsigned)w;
; }
	v_cvt_pk_f32_fp8_e32 v[162:163], v138
	v_pk_mul_f32 v[128:129], v[154:155], v[128:129]
	v_pk_fma_f32 v[154:155], v[56:57], v[160:161], v[8:9]
	s_nop 0
	v_pk_fma_f32 v[154:155], v[40:41], v[142:143], v[154:155]
	v_pk_fma_f32 v[158:159], v[64:65], v[158:159], v[16:17]
	v_pk_fma_f32 v[154:155], v[24:25], v[108:109], v[154:155]
	v_pk_fma_f32 v[158:159], v[52:53], v[170:171], v[158:159]
	v_exp_f32_e32 v68, v154
	v_exp_f32_e32 v160, v155
	v_pk_fma_f32 v[146:147], v[54:55], v[146:147], v[6:7]
	v_add_f32_e32 v68, 1.0, v68
	v_rcp_f32_e32 v148, v68
	v_add_f32_e32 v68, 1.0, v160
	v_rcp_f32_e32 v149, v68
	v_med3_f32 v68, v112, s41, v1
	v_cvt_pk_fp8_f32 v112, v68, v113
	v_med3_f32 v68, v120, s41, v1
	v_med3_f32 v120, v121, s41, v1
	v_med3_f32 v121, v128, s41, v1
	v_med3_f32 v128, v129, s41, v1
	v_cvt_pk_fp8_f32 v113, v121, v128
	v_pk_mul_f32 v[148:149], v[154:155], v[148:149]
	v_cvt_pk_fp8_f32 v112, v68, v120 op_sel:[0,0,1]
	v_pk_mul_f32 v[148:149], v[152:153], v[148:149]
	v_cvt_pk_f32_fp8_sdwa v[154:155], v140 src0_sel:WORD_1
	v_med3_f32 v68, v148, s41, v1
	v_med3_f32 v120, v149, s41, v1
	v_cvt_pk_fp8_f32 v113, v68, v120 op_sel:[0,0,1]
	v_add_co_u32_e32 v120, vcc, s25, v70
	v_cvt_pk_f32_fp8_e32 v[148:149], v141
	s_nop 0
	v_addc_co_u32_e32 v121, vcc, 0, v71, vcc
	global_store_dwordx2 v[120:121], v[112:113], off offset:1536
	v_pk_fma_f32 v[120:121], v[62:63], v[180:181], v[14:15]
	v_cvt_pk_f32_fp8_sdwa v[112:113], v141 src0_sel:WORD_1
	v_pk_fma_f32 v[120:121], v[50:51], v[182:183], v[120:121]
	v_cvt_pk_f32_fp8_sdwa v[152:153], v138 src0_sel:WORD_1
	v_pk_fma_f32 v[140:141], v[34:35], v[168:169], v[120:121]
	v_cvt_pk_f32_fp8_e32 v[128:129], v139
	v_exp_f32_e32 v68, v140
	v_exp_f32_e32 v160, v141
	v_cvt_pk_f32_fp8_sdwa v[120:121], v139 src0_sel:WORD_1
	v_add_f32_e32 v68, 1.0, v68
	v_rcp_f32_e32 v138, v68
	v_add_f32_e32 v68, 1.0, v160
	v_rcp_f32_e32 v139, v68
	v_pk_fma_f32 v[160:161], v[58:59], v[174:175], v[10:11]
	v_pk_fma_f32 v[158:159], v[36:37], v[154:155], v[158:159]
	v_pk_fma_f32 v[160:161], v[42:43], v[176:177], v[160:161]
	s_nop 0
	v_pk_fma_f32 v[160:161], v[26:27], v[162:163], v[160:161]
	v_pk_mul_f32 v[138:139], v[140:141], v[138:139]
	s_nop 0
	v_pk_mul_f32 v[138:139], v[160:161], v[138:139]
	v_exp_f32_e32 v68, v158
	v_exp_f32_e32 v160, v159
	v_add_f32_e32 v68, 1.0, v68
	v_rcp_f32_e32 v140, v68
	v_add_f32_e32 v68, 1.0, v160
	v_rcp_f32_e32 v141, v68
	v_pk_fma_f32 v[146:147], v[38:39], v[136:137], v[146:147]
	v_pk_fma_f32 v[150:151], v[60:61], v[150:151], v[12:13]
	v_pk_fma_f32 v[146:147], v[22:23], v[148:149], v[146:147]
	v_pk_mul_f32 v[140:141], v[158:159], v[140:141]
	v_exp_f32_e32 v68, v146
	v_exp_f32_e32 v158, v147
	v_pk_fma_f32 v[150:151], v[44:45], v[156:157], v[150:151]
	v_add_f32_e32 v68, 1.0, v68
	v_pk_fma_f32 v[150:151], v[28:29], v[152:153], v[150:151]
	v_pk_fma_f32 v[142:143], v[56:57], v[142:143], v[8:9]
	s_nop 0
	v_pk_fma_f32 v[142:143], v[40:41], v[108:109], v[142:143]
	v_pk_mul_f32 v[140:141], v[150:151], v[140:141]
	v_rcp_f32_e32 v150, v68
	v_add_f32_e32 v68, 1.0, v158
	v_rcp_f32_e32 v151, v68
	v_pk_fma_f32 v[142:143], v[24:25], v[112:113], v[142:143]
	v_pk_fma_f32 v[144:145], v[46:47], v[144:145], v[2:3]
	v_pk_mul_f32 v[146:147], v[146:147], v[150:151]
	v_exp_f32_e32 v68, v142
	v_exp_f32_e32 v150, v143
	v_pk_fma_f32 v[144:145], v[30:31], v[124:125], v[144:145]
	v_add_f32_e32 v68, 1.0, v68
	v_pk_fma_f32 v[144:145], v[18:19], v[128:129], v[144:145]
	v_pk_fma_f32 v[132:133], v[48:49], v[132:133], v[4:5]
	s_nop 0
	v_pk_fma_f32 v[132:133], v[32:33], v[116:117], v[132:133]
	v_pk_mul_f32 v[144:145], v[144:145], v[146:147]
	v_rcp_f32_e32 v146, v68
	v_add_f32_e32 v68, 1.0, v150
	v_rcp_f32_e32 v147, v68
	v_pk_fma_f32 v[132:133], v[20:21], v[120:121], v[132:133]
	v_med3_f32 v68, v138, s41, v1
	v_pk_mul_f32 v[142:143], v[142:143], v[146:147]
	v_med3_f32 v139, v139, s41, v1
	v_pk_mul_f32 v[132:133], v[132:133], v[142:143]
	v_cvt_pk_fp8_f32 v138, v68, v139
	v_med3_f32 v68, v140, s41, v1
	v_med3_f32 v140, v141, s41, v1
	v_med3_f32 v141, v144, s41, v1
	v_med3_f32 v142, v145, s41, v1
	v_cvt_pk_fp8_f32 v139, v141, v142
	v_cvt_pk_fp8_f32 v138, v68, v140 op_sel:[0,0,1]
	v_med3_f32 v68, v132, s41, v1
	v_med3_f32 v132, v133, s41, v1
	v_cvt_pk_fp8_f32 v139, v68, v132 op_sel:[0,0,1]
	v_add_co_u32_e32 v132, vcc, s46, v70
	s_waitcnt vmcnt(26)
	v_cvt_pk_f32_fp8_e32 v[142:143], v104
	v_addc_co_u32_e32 v133, vcc, 0, v71, vcc
	global_store_dwordx2 v[132:133], v[138:139], off offset:256
	v_pk_fma_f32 v[138:139], v[62:63], v[182:183], v[14:15]
	s_waitcnt vmcnt(26)
; __device__ __forceinline__ float clamp448(float x) { return __builtin_amdgcn_fmed3f(x, -448.f, 448.f); }
; __device__ __forceinline__ unsigned pk4_fp8(float a, float b, float c, float d) {
;     int w = __builtin_amdgcn_cvt_pk_fp8_f32(clamp448(a), clamp448(b), 0, false);
;     w = __builtin_amdgcn_cvt_pk_fp8_f32(clamp448(c), clamp448(d), w, true);
;     return (unsigned)w;
; }
	v_cvt_pk_f32_fp8_e32 v[164:165], v100
	v_pk_fma_f32 v[138:139], v[50:51], v[168:169], v[138:139]
	v_cvt_pk_f32_fp8_sdwa v[144:145], v100 src0_sel:WORD_1
	v_pk_fma_f32 v[138:139], v[34:35], v[142:143], v[138:139]
	v_pk_fma_f32 v[150:151], v[58:59], v[176:177], v[10:11]
	v_exp_f32_e32 v68, v138
	v_exp_f32_e32 v147, v139
	v_cvt_pk_f32_fp8_sdwa v[160:161], v104 src0_sel:WORD_1
	v_add_f32_e32 v68, 1.0, v68
	v_rcp_f32_e32 v146, v68
	v_add_f32_e32 v68, 1.0, v147
	v_rcp_f32_e32 v147, v68
	v_pk_fma_f32 v[150:151], v[42:43], v[162:163], v[150:151]
	v_cvt_pk_f32_fp8_e32 v[140:141], v105
	v_pk_fma_f32 v[150:151], v[26:27], v[164:165], v[150:151]
	v_pk_mul_f32 v[138:139], v[138:139], v[146:147]
	s_nop 0
	v_pk_mul_f32 v[138:139], v[150:151], v[138:139]
	v_pk_fma_f32 v[150:151], v[64:65], v[170:171], v[16:17]
	s_nop 0
	v_pk_fma_f32 v[150:151], v[52:53], v[154:155], v[150:151]
	v_pk_fma_f32 v[136:137], v[54:55], v[136:137], v[6:7]
	v_pk_fma_f32 v[150:151], v[36:37], v[160:161], v[150:151]
	v_pk_fma_f32 v[156:157], v[60:61], v[156:157], v[12:13]
	v_exp_f32_e32 v68, v150
	v_exp_f32_e32 v158, v151
	v_pk_fma_f32 v[136:137], v[38:39], v[148:149], v[136:137]
	v_add_f32_e32 v68, 1.0, v68
	v_rcp_f32_e32 v146, v68
	v_add_f32_e32 v68, 1.0, v158
	v_rcp_f32_e32 v147, v68
	v_pk_fma_f32 v[156:157], v[44:45], v[152:153], v[156:157]
	v_pk_fma_f32 v[136:137], v[22:23], v[140:141], v[136:137]
	v_pk_fma_f32 v[156:157], v[28:29], v[144:145], v[156:157]
	v_pk_mul_f32 v[146:147], v[150:151], v[146:147]
	s_nop 0
	v_pk_mul_f32 v[146:147], v[156:157], v[146:147]
	v_exp_f32_e32 v68, v136
	v_exp_f32_e32 v156, v137
	v_cvt_pk_f32_fp8_sdwa v[104:105], v105 src0_sel:WORD_1
	v_add_f32_e32 v68, 1.0, v68
	v_rcp_f32_e32 v150, v68
	v_add_f32_e32 v68, 1.0, v156
	v_rcp_f32_e32 v151, v68
	v_pk_fma_f32 v[108:109], v[56:57], v[108:109], v[8:9]
	v_cvt_pk_f32_fp8_e32 v[132:133], v101
	v_pk_fma_f32 v[108:109], v[40:41], v[112:113], v[108:109]
	v_pk_mul_f32 v[136:137], v[136:137], v[150:151]
	v_pk_fma_f32 v[108:109], v[24:25], v[104:105], v[108:109]
	v_pk_fma_f32 v[124:125], v[46:47], v[124:125], v[2:3]
	v_exp_f32_e32 v68, v108
	v_exp_f32_e32 v150, v109
	v_pk_fma_f32 v[124:125], v[30:31], v[128:129], v[124:125]
	v_add_f32_e32 v68, 1.0, v68
	v_pk_fma_f32 v[124:125], v[18:19], v[132:133], v[124:125]
	v_cvt_pk_f32_fp8_sdwa v[100:101], v101 src0_sel:WORD_1
	v_pk_fma_f32 v[116:117], v[48:49], v[116:117], v[4:5]
	v_pk_mul_f32 v[124:125], v[124:125], v[136:137]
	v_rcp_f32_e32 v136, v68
	v_add_f32_e32 v68, 1.0, v150
	v_rcp_f32_e32 v137, v68
	v_pk_fma_f32 v[116:117], v[32:33], v[120:121], v[116:117]
	v_med3_f32 v68, v138, s41, v1
	v_pk_fma_f32 v[116:117], v[20:21], v[100:101], v[116:117]
	v_pk_mul_f32 v[108:109], v[108:109], v[136:137]
	v_med3_f32 v124, v124, s41, v1
	v_pk_mul_f32 v[108:109], v[116:117], v[108:109]
	v_med3_f32 v117, v139, s41, v1
	v_cvt_pk_fp8_f32 v116, v68, v117
	v_med3_f32 v125, v125, s41, v1
	s_waitcnt vmcnt(25)
	v_cvt_pk_f32_fp8_e32 v[172:173], v96
	v_cvt_pk_fp8_f32 v117, v124, v125
	v_pk_fma_f32 v[138:139], v[62:63], v[168:169], v[14:15]
	v_med3_f32 v68, v146, s41, v1
	v_med3_f32 v136, v147, s41, v1
	v_pk_fma_f32 v[138:139], v[50:51], v[142:143], v[138:139]
	v_cvt_pk_fp8_f32 v116, v68, v136 op_sel:[0,0,1]
	v_med3_f32 v68, v108, s41, v1
	v_med3_f32 v108, v109, s41, v1
	v_pk_fma_f32 v[138:139], v[34:35], v[172:173], v[138:139]
	v_cvt_pk_fp8_f32 v117, v68, v108 op_sel:[0,0,1]
	s_waitcnt vmcnt(24)
	v_cvt_pk_f32_fp8_e32 v[166:167], v92
	v_cvt_pk_f32_fp8_sdwa v[124:125], v92 src0_sel:WORD_1
	v_exp_f32_e32 v68, v138
	v_exp_f32_e32 v147, v139
	v_pk_fma_f32 v[150:151], v[58:59], v[162:163], v[10:11]
	v_add_f32_e32 v68, 1.0, v68
	v_rcp_f32_e32 v146, v68
	v_add_f32_e32 v68, 1.0, v147
	v_rcp_f32_e32 v147, v68
	v_cvt_pk_f32_fp8_sdwa v[136:137], v96 src0_sel:WORD_1
	v_pk_fma_f32 v[150:151], v[42:43], v[164:165], v[150:151]
	v_add_co_u32_e32 v108, vcc, s26, v70
	v_pk_fma_f32 v[150:151], v[26:27], v[166:167], v[150:151]
	v_pk_mul_f32 v[138:139], v[138:139], v[146:147]
	s_nop 0
	v_pk_mul_f32 v[138:139], v[150:151], v[138:139]
	v_pk_fma_f32 v[150:151], v[64:65], v[154:155], v[16:17]
	v_addc_co_u32_e32 v109, vcc, 0, v71, vcc
	v_pk_fma_f32 v[150:151], v[52:53], v[160:161], v[150:151]
	global_store_dwordx2 v[108:109], v[116:117], off offset:3072
	v_pk_fma_f32 v[150:151], v[36:37], v[136:137], v[150:151]
	v_cvt_pk_f32_fp8_e32 v[116:117], v97
	v_exp_f32_e32 v68, v150
	v_exp_f32_e32 v154, v151
	v_add_f32_e32 v68, 1.0, v68
	v_rcp_f32_e32 v146, v68
	v_add_f32_e32 v68, 1.0, v154
	v_rcp_f32_e32 v147, v68
	v_pk_fma_f32 v[148:149], v[54:55], v[148:149], v[6:7]
	v_pk_fma_f32 v[152:153], v[60:61], v[152:153], v[12:13]
	v_pk_fma_f32 v[148:149], v[38:39], v[140:141], v[148:149]
	v_pk_fma_f32 v[152:153], v[44:45], v[144:145], v[152:153]
	v_pk_fma_f32 v[148:149], v[22:23], v[116:117], v[148:149]
	v_pk_fma_f32 v[152:153], v[28:29], v[124:125], v[152:153]
	v_pk_mul_f32 v[146:147], v[150:151], v[146:147]
	s_nop 0
	v_pk_mul_f32 v[146:147], v[152:153], v[146:147]
	v_exp_f32_e32 v68, v148
	v_exp_f32_e32 v152, v149
	v_cvt_pk_f32_fp8_sdwa v[96:97], v97 src0_sel:WORD_1
	v_add_f32_e32 v68, 1.0, v68
	v_rcp_f32_e32 v150, v68
	v_add_f32_e32 v68, 1.0, v152
	v_rcp_f32_e32 v151, v68
	v_pk_fma_f32 v[112:113], v[56:57], v[112:113], v[8:9]
	v_cvt_pk_f32_fp8_e32 v[108:109], v93
	v_pk_fma_f32 v[112:113], v[40:41], v[104:105], v[112:113]
	v_pk_mul_f32 v[148:149], v[148:149], v[150:151]
	v_pk_fma_f32 v[112:113], v[24:25], v[96:97], v[112:113]
	v_pk_fma_f32 v[128:129], v[46:47], v[128:129], v[2:3]
	v_exp_f32_e32 v68, v112
	v_exp_f32_e32 v150, v113
	v_pk_fma_f32 v[128:129], v[30:31], v[132:133], v[128:129]
	v_add_f32_e32 v68, 1.0, v68
	v_pk_fma_f32 v[128:129], v[18:19], v[108:109], v[128:129]
	v_cvt_pk_f32_fp8_sdwa v[92:93], v93 src0_sel:WORD_1
	v_pk_fma_f32 v[120:121], v[48:49], v[120:121], v[4:5]
	v_pk_mul_f32 v[128:129], v[128:129], v[148:149]
	v_rcp_f32_e32 v148, v68
	v_add_f32_e32 v68, 1.0, v150
	v_rcp_f32_e32 v149, v68
	v_pk_fma_f32 v[120:121], v[32:33], v[100:101], v[120:121]
	v_med3_f32 v68, v138, s41, v1
	v_pk_fma_f32 v[120:121], v[20:21], v[92:93], v[120:121]
	v_pk_mul_f32 v[112:113], v[112:113], v[148:149]
	v_med3_f32 v128, v128, s41, v1
	v_pk_mul_f32 v[112:113], v[120:121], v[112:113]
	v_med3_f32 v121, v139, s41, v1
	v_cvt_pk_fp8_f32 v120, v68, v121
	v_med3_f32 v129, v129, s41, v1
	v_cvt_pk_fp8_f32 v121, v128, v129
	s_waitcnt vmcnt(24)
; __device__ __forceinline__ float clamp448(float x) { return __builtin_amdgcn_fmed3f(x, -448.f, 448.f); }
; __device__ __forceinline__ unsigned pk4_fp8(float a, float b, float c, float d) {
;     int w = __builtin_amdgcn_cvt_pk_fp8_f32(clamp448(a), clamp448(b), 0, false);
;     w = __builtin_amdgcn_cvt_pk_fp8_f32(clamp448(c), clamp448(d), w, true);
;     return (unsigned)w;
; }
	v_cvt_pk_f32_fp8_e32 v[168:169], v88
	v_med3_f32 v68, v146, s41, v1
	v_med3_f32 v138, v147, s41, v1
	v_cvt_pk_fp8_f32 v120, v68, v138 op_sel:[0,0,1]
	v_med3_f32 v68, v112, s41, v1
	v_med3_f32 v112, v113, s41, v1
	v_cvt_pk_f32_fp8_sdwa v[158:159], v88 src0_sel:WORD_1
	v_cvt_pk_f32_fp8_e32 v[150:151], v89
	v_cvt_pk_f32_fp8_sdwa v[138:139], v89 src0_sel:WORD_1
	v_pk_fma_f32 v[88:89], v[62:63], v[142:143], v[14:15]
	v_cvt_pk_fp8_f32 v121, v68, v112 op_sel:[0,0,1]
	v_pk_fma_f32 v[88:89], v[50:51], v[172:173], v[88:89]
	v_add_co_u32_e32 v112, vcc, s47, v70
	v_pk_fma_f32 v[88:89], v[34:35], v[168:169], v[88:89]
	s_nop 0
	v_addc_co_u32_e32 v113, vcc, 0, v71, vcc
	s_waitcnt vmcnt(23)
	v_cvt_pk_f32_fp8_e32 v[162:163], v84
	v_cvt_pk_f32_fp8_sdwa v[154:155], v84 src0_sel:WORD_1
	v_exp_f32_e32 v68, v88
	global_store_dwordx2 v[112:113], v[120:121], off offset:1792
	v_exp_f32_e32 v112, v89
	v_add_f32_e32 v68, 1.0, v68
	v_rcp_f32_e32 v84, v68
	v_cvt_pk_f32_fp8_e32 v[146:147], v85
	v_add_f32_e32 v68, 1.0, v112
	v_cvt_pk_f32_fp8_sdwa v[142:143], v85 src0_sel:WORD_1
	v_rcp_f32_e32 v85, v68
	v_pk_fma_f32 v[112:113], v[58:59], v[164:165], v[10:11]
	v_pk_fma_f32 v[104:105], v[56:57], v[104:105], v[8:9]
	v_pk_fma_f32 v[112:113], v[42:43], v[166:167], v[112:113]
	v_pk_mul_f32 v[84:85], v[88:89], v[84:85]
	v_pk_fma_f32 v[112:113], v[26:27], v[162:163], v[112:113]
	v_pk_fma_f32 v[104:105], v[40:41], v[96:97], v[104:105]
	v_pk_mul_f32 v[84:85], v[112:113], v[84:85]
	v_pk_fma_f32 v[112:113], v[64:65], v[160:161], v[16:17]
	s_nop 0
	v_pk_fma_f32 v[112:113], v[52:53], v[136:137], v[112:113]
	v_pk_fma_f32 v[104:105], v[24:25], v[138:139], v[104:105]
	v_pk_fma_f32 v[112:113], v[36:37], v[158:159], v[112:113]
	v_pk_fma_f32 v[100:101], v[48:49], v[100:101], v[4:5]
	v_exp_f32_e32 v68, v112
	v_exp_f32_e32 v120, v113
	v_pk_fma_f32 v[100:101], v[32:33], v[92:93], v[100:101]
	v_add_f32_e32 v68, 1.0, v68
	v_rcp_f32_e32 v88, v68
	v_add_f32_e32 v68, 1.0, v120
	v_rcp_f32_e32 v89, v68
	v_pk_fma_f32 v[120:121], v[60:61], v[144:145], v[12:13]
	v_pk_fma_f32 v[100:101], v[20:21], v[142:143], v[100:101]
	v_pk_fma_f32 v[120:121], v[44:45], v[124:125], v[120:121]
	v_pk_mul_f32 v[88:89], v[112:113], v[88:89]
	v_pk_fma_f32 v[120:121], v[28:29], v[154:155], v[120:121]
	s_nop 0
	v_pk_mul_f32 v[88:89], v[120:121], v[88:89]
	v_pk_fma_f32 v[120:121], v[54:55], v[140:141], v[6:7]
	s_nop 0
	v_pk_fma_f32 v[120:121], v[38:39], v[116:117], v[120:121]
	v_med3_f32 v85, v85, s41, v1
	v_pk_fma_f32 v[120:121], v[22:23], v[150:151], v[120:121]
	s_waitcnt vmcnt(23)
	v_cvt_pk_f32_fp8_e32 v[170:171], v80
	v_exp_f32_e32 v68, v120
	v_exp_f32_e32 v128, v121
	v_cvt_pk_f32_fp8_sdwa v[160:161], v80 src0_sel:WORD_1
	v_add_f32_e32 v68, 1.0, v68
	v_rcp_f32_e32 v112, v68
	v_add_f32_e32 v68, 1.0, v128
	v_rcp_f32_e32 v113, v68
	v_pk_fma_f32 v[128:129], v[46:47], v[132:133], v[2:3]
	s_nop 0
	v_pk_fma_f32 v[128:129], v[30:31], v[108:109], v[128:129]
	v_pk_mul_f32 v[112:113], v[120:121], v[112:113]
	v_pk_fma_f32 v[128:129], v[18:19], v[146:147], v[128:129]
	v_exp_f32_e32 v68, v104
	v_pk_mul_f32 v[112:113], v[128:129], v[112:113]
	v_exp_f32_e32 v128, v105
	v_add_f32_e32 v68, 1.0, v68
	v_rcp_f32_e32 v120, v68
	v_add_f32_e32 v68, 1.0, v128
	v_rcp_f32_e32 v121, v68
	v_med3_f32 v68, v84, s41, v1
	v_cvt_pk_fp8_f32 v84, v68, v85
	v_pk_mul_f32 v[104:105], v[104:105], v[120:121]
	v_med3_f32 v68, v88, s41, v1
	v_pk_mul_f32 v[100:101], v[100:101], v[104:105]
	v_med3_f32 v88, v89, s41, v1
	v_med3_f32 v89, v112, s41, v1
	v_med3_f32 v104, v113, s41, v1
	v_cvt_pk_fp8_f32 v85, v89, v104
	v_cvt_pk_fp8_f32 v84, v68, v88 op_sel:[0,0,1]
	v_med3_f32 v68, v100, s41, v1
	v_med3_f32 v88, v101, s41, v1
	v_cvt_pk_f32_fp8_e32 v[152:153], v81
	v_cvt_pk_f32_fp8_sdwa v[140:141], v81 src0_sel:WORD_1
	v_pk_fma_f32 v[80:81], v[62:63], v[172:173], v[14:15]
	v_cvt_pk_fp8_f32 v85, v68, v88 op_sel:[0,0,1]
	v_pk_fma_f32 v[80:81], v[50:51], v[168:169], v[80:81]
	v_add_co_u32_e32 v88, vcc, s27, v70
	v_pk_fma_f32 v[80:81], v[34:35], v[170:171], v[80:81]
	s_nop 0
	v_addc_co_u32_e32 v89, vcc, 0, v71, vcc
	s_waitcnt vmcnt(22)
	v_cvt_pk_f32_fp8_e32 v[164:165], v76
	v_cvt_pk_f32_fp8_sdwa v[156:157], v76 src0_sel:WORD_1
	v_exp_f32_e32 v68, v80
	global_store_dwordx2 v[88:89], v[84:85], off offset:512
	v_exp_f32_e32 v84, v81
	v_add_f32_e32 v68, 1.0, v68
	v_rcp_f32_e32 v76, v68
	v_cvt_pk_f32_fp8_e32 v[148:149], v77
	v_add_f32_e32 v68, 1.0, v84
	v_cvt_pk_f32_fp8_sdwa v[144:145], v77 src0_sel:WORD_1
	v_rcp_f32_e32 v77, v68
	v_pk_fma_f32 v[84:85], v[58:59], v[166:167], v[10:11]
	v_pk_fma_f32 v[96:97], v[56:57], v[96:97], v[8:9]
	v_pk_fma_f32 v[84:85], v[42:43], v[162:163], v[84:85]
	v_pk_mul_f32 v[76:77], v[80:81], v[76:77]
	v_pk_fma_f32 v[84:85], v[26:27], v[164:165], v[84:85]
	v_pk_fma_f32 v[96:97], v[40:41], v[138:139], v[96:97]
	v_pk_mul_f32 v[76:77], v[84:85], v[76:77]
	v_pk_fma_f32 v[84:85], v[64:65], v[136:137], v[16:17]
	s_nop 0
	v_pk_fma_f32 v[84:85], v[52:53], v[158:159], v[84:85]
	v_pk_fma_f32 v[96:97], v[24:25], v[140:141], v[96:97]
	v_pk_fma_f32 v[84:85], v[36:37], v[160:161], v[84:85]
	v_pk_fma_f32 v[92:93], v[48:49], v[92:93], v[4:5]
	v_exp_f32_e32 v68, v84
	v_exp_f32_e32 v88, v85
	v_med3_f32 v77, v77, s41, v1
	v_add_f32_e32 v68, 1.0, v68
	v_rcp_f32_e32 v80, v68
	v_add_f32_e32 v68, 1.0, v88
	v_rcp_f32_e32 v81, v68
	v_pk_fma_f32 v[88:89], v[60:61], v[124:125], v[12:13]
	v_pk_fma_f32 v[92:93], v[32:33], v[142:143], v[92:93]
	v_pk_fma_f32 v[88:89], v[44:45], v[154:155], v[88:89]
	v_pk_mul_f32 v[80:81], v[84:85], v[80:81]
	v_pk_fma_f32 v[88:89], v[28:29], v[156:157], v[88:89]
	s_waitcnt vmcnt(22)
; #define CV_LOAD(G_, V_, r0_) do { _Pragma("unroll") for (int i_ = 0; i_ < 8; ++i_) { G_[i_] = *(const GAS v2u*)(ap + (size_t)((r0_) + i_) * F2); V_[i_] = *(const GAS v2u*)(ap + (size_t)((r0_) + i_) * F2 + 128); } } while (0)
; __device__ __forceinline__ void conv_phase(Frame& F) {
;     ...
;         CV_LOAD(GA, VA, 0); CV_LOAD(GB, VB, 8); CV_COMP(GA, VA, 0); CV_LOAD(GA, VA, 16); CV_COMP(GB, VB, 8); CV_LOAD(GB, VB, 24); CV_COMP(GA, VA, 16); CV_COMP(GB, VB, 24);
	v_cvt_pk_f32_fp8_e32 v[180:181], v134
	v_pk_mul_f32 v[80:81], v[88:89], v[80:81]
	v_pk_fma_f32 v[88:89], v[54:55], v[116:117], v[6:7]
	s_nop 0
	v_pk_fma_f32 v[88:89], v[38:39], v[150:151], v[88:89]
	v_pk_fma_f32 v[92:93], v[20:21], v[144:145], v[92:93]
	v_pk_fma_f32 v[88:89], v[22:23], v[152:153], v[88:89]
	s_nop 0
	v_exp_f32_e32 v68, v88
	v_exp_f32_e32 v100, v89
	v_pk_fma_f32 v[168:169], v[62:63], v[168:169], v[14:15]
	v_add_f32_e32 v68, 1.0, v68
	v_rcp_f32_e32 v84, v68
	v_add_f32_e32 v68, 1.0, v100
	v_rcp_f32_e32 v85, v68
	v_pk_fma_f32 v[100:101], v[46:47], v[108:109], v[2:3]
	s_nop 0
	v_pk_fma_f32 v[100:101], v[30:31], v[146:147], v[100:101]
	v_pk_mul_f32 v[84:85], v[88:89], v[84:85]
	v_pk_fma_f32 v[100:101], v[18:19], v[148:149], v[100:101]
	v_exp_f32_e32 v68, v96
	v_pk_mul_f32 v[84:85], v[100:101], v[84:85]
	v_exp_f32_e32 v100, v97
	v_add_f32_e32 v68, 1.0, v68
	v_rcp_f32_e32 v88, v68
	v_add_f32_e32 v68, 1.0, v100
	v_rcp_f32_e32 v89, v68
	v_med3_f32 v68, v76, s41, v1
	v_cvt_pk_fp8_f32 v76, v68, v77
	v_med3_f32 v68, v80, s41, v1
	v_med3_f32 v80, v81, s41, v1
	v_med3_f32 v81, v84, s41, v1
	v_med3_f32 v84, v85, s41, v1
	v_cvt_pk_fp8_f32 v77, v81, v84
	v_pk_mul_f32 v[88:89], v[96:97], v[88:89]
	v_pk_fma_f32 v[168:169], v[50:51], v[170:171], v[168:169]
	v_pk_mul_f32 v[88:89], v[92:93], v[88:89]
	v_cvt_pk_fp8_f32 v76, v68, v80 op_sel:[0,0,1]
	v_med3_f32 v68, v88, s41, v1
	v_med3_f32 v80, v89, s41, v1
	v_pk_fma_f32 v[168:169], v[34:35], v[180:181], v[168:169]
	v_cvt_pk_fp8_f32 v77, v68, v80 op_sel:[0,0,1]
	s_waitcnt vmcnt(21)
	v_cvt_pk_f32_fp8_e32 v[178:179], v130
	v_cvt_pk_f32_fp8_sdwa v[174:175], v130 src0_sel:WORD_1
	v_exp_f32_e32 v68, v168
	v_exp_f32_e32 v183, v169
	v_cvt_pk_f32_fp8_sdwa v[176:177], v134 src0_sel:WORD_1
	v_add_f32_e32 v68, 1.0, v68
	v_rcp_f32_e32 v182, v68
	v_add_f32_e32 v68, 1.0, v183
	v_rcp_f32_e32 v183, v68
	v_pk_fma_f32 v[158:159], v[64:65], v[158:159], v[16:17]
	v_add_co_u32_e32 v80, vcc, s48, v70
	v_pk_fma_f32 v[158:159], v[52:53], v[160:161], v[158:159]
	v_pk_mul_f32 v[168:169], v[168:169], v[182:183]
	v_pk_fma_f32 v[158:159], v[36:37], v[176:177], v[158:159]
	v_pk_fma_f32 v[162:163], v[58:59], v[162:163], v[10:11]
	v_exp_f32_e32 v68, v158
	v_exp_f32_e32 v182, v159
	v_addc_co_u32_e32 v81, vcc, 0, v71, vcc
	v_pk_fma_f32 v[162:163], v[42:43], v[164:165], v[162:163]
	global_store_dwordx2 v[80:81], v[76:77], off offset:3328
	v_add_co_u32_e32 v76, vcc, s42, v72
	v_pk_fma_f32 v[162:163], v[26:27], v[178:179], v[162:163]
	s_nop 0
	v_addc_co_u32_e32 v77, vcc, 0, v73, vcc
	v_cvt_pk_f32_fp8_e32 v[172:173], v135
	v_add_f32_e32 v68, 1.0, v68
	v_add_co_u32_e32 v80, vcc, s49, v72
	v_pk_mul_f32 v[162:163], v[162:163], v[168:169]
	v_rcp_f32_e32 v168, v68
	v_add_f32_e32 v68, 1.0, v182
	v_addc_co_u32_e32 v81, vcc, 0, v73, vcc
	v_rcp_f32_e32 v169, v68
	v_pk_fma_f32 v[150:151], v[54:55], v[150:151], v[6:7]
	global_load_dwordx2 v[136:137], v[76:77], off nt
	global_load_dwordx2 v[132:133], v[76:77], off offset:128 nt
	global_load_dwordx2 v[128:129], v[80:81], off offset:1536 nt
	global_load_dwordx2 v[124:125], v[80:81], off offset:1664 nt
	v_add_co_u32_e32 v76, vcc, s50, v72
	v_pk_fma_f32 v[150:151], v[38:39], v[152:153], v[150:151]
	s_nop 0
	v_addc_co_u32_e32 v77, vcc, 0, v73, vcc
	v_pk_fma_f32 v[150:151], v[22:23], v[172:173], v[150:151]
	v_add_co_u32_e32 v80, vcc, s51, v72
	s_nop 0
	s_nop 0
	v_addc_co_u32_e32 v81, vcc, 0, v73, vcc
	v_pk_mul_f32 v[158:159], v[158:159], v[168:169]
	v_exp_f32_e32 v68, v150
	global_load_dwordx2 v[120:121], v[76:77], off offset:3072 nt
	global_load_dwordx2 v[116:117], v[76:77], off offset:3200 nt
	global_load_dwordx2 v[112:113], v[80:81], off offset:512 nt
	global_load_dwordx2 v[108:109], v[80:81], off offset:640 nt
	v_add_co_u32_e32 v76, vcc, s52, v72
	v_pk_fma_f32 v[154:155], v[60:61], v[154:155], v[12:13]
	v_exp_f32_e32 v168, v151
	v_addc_co_u32_e32 v77, vcc, 0, v73, vcc
	v_pk_fma_f32 v[154:155], v[44:45], v[156:157], v[154:155]
	v_add_co_u32_e32 v80, vcc, s53, v72
	v_pk_fma_f32 v[154:155], v[28:29], v[174:175], v[154:155]
	s_nop 0
	v_addc_co_u32_e32 v81, vcc, 0, v73, vcc
	v_cvt_pk_f32_fp8_sdwa v[134:135], v135 src0_sel:WORD_1
	v_add_f32_e32 v68, 1.0, v68
	global_load_dwordx2 v[104:105], v[76:77], off offset:2048 nt
	global_load_dwordx2 v[100:101], v[76:77], off offset:2176 nt
	global_load_dwordx2 v[96:97], v[80:81], off offset:3584 nt
	global_load_dwordx2 v[92:93], v[80:81], off offset:3712 nt
	v_add_co_u32_e32 v76, vcc, s54, v72
	v_pk_mul_f32 v[154:155], v[154:155], v[158:159]
	v_rcp_f32_e32 v158, v68
	v_add_f32_e32 v68, 1.0, v168
	v_addc_co_u32_e32 v77, vcc, 0, v73, vcc
	v_rcp_f32_e32 v159, v68
	v_pk_fma_f32 v[138:139], v[56:57], v[138:139], v[8:9]
	v_add_co_u32_e32 v166, vcc, s55, v72
	v_pk_fma_f32 v[138:139], v[40:41], v[140:141], v[138:139]
	s_nop 0
	v_addc_co_u32_e32 v167, vcc, 0, v73, vcc
	v_pk_fma_f32 v[138:139], v[24:25], v[134:135], v[138:139]
	global_load_dwordx2 v[88:89], v[76:77], off offset:1024 nt
	global_load_dwordx2 v[84:85], v[76:77], off offset:1152 nt
	global_load_dwordx2 v[80:81], v[166:167], off offset:2560 nt
	s_nop 0
	global_load_dwordx2 v[76:77], v[166:167], off offset:2688 nt
	v_cvt_pk_f32_fp8_e32 v[166:167], v131
	v_pk_mul_f32 v[150:151], v[150:151], v[158:159]
	v_exp_f32_e32 v68, v138
	v_pk_fma_f32 v[146:147], v[46:47], v[146:147], v[2:3]
	v_exp_f32_e32 v158, v139
	v_pk_fma_f32 v[146:147], v[30:31], v[148:149], v[146:147]
	v_add_f32_e32 v68, 1.0, v68
	v_pk_fma_f32 v[146:147], v[18:19], v[166:167], v[146:147]
	v_cvt_pk_f32_fp8_sdwa v[130:131], v131 src0_sel:WORD_1
	v_pk_fma_f32 v[142:143], v[48:49], v[142:143], v[4:5]
	v_pk_mul_f32 v[146:147], v[146:147], v[150:151]
	v_rcp_f32_e32 v150, v68
	v_add_f32_e32 v68, 1.0, v158
	v_rcp_f32_e32 v151, v68
	v_pk_fma_f32 v[142:143], v[32:33], v[144:145], v[142:143]
	v_med3_f32 v68, v162, s41, v1
	v_pk_fma_f32 v[142:143], v[20:21], v[130:131], v[142:143]
	v_pk_mul_f32 v[138:139], v[138:139], v[150:151]
	v_med3_f32 v146, v146, s41, v1
	v_pk_mul_f32 v[138:139], v[142:143], v[138:139]
	v_med3_f32 v143, v163, s41, v1
	v_cvt_pk_fp8_f32 v142, v68, v143
	v_med3_f32 v147, v147, s41, v1
	s_waitcnt vmcnt(37)
; __device__ __forceinline__ float clamp448(float x) { return __builtin_amdgcn_fmed3f(x, -448.f, 448.f); }
; __device__ __forceinline__ unsigned pk4_fp8(float a, float b, float c, float d) {
;     int w = __builtin_amdgcn_cvt_pk_fp8_f32(clamp448(a), clamp448(b), 0, false);
;     w = __builtin_amdgcn_cvt_pk_fp8_f32(clamp448(c), clamp448(d), w, true);
;     return (unsigned)w;
; }
	v_cvt_pk_f32_fp8_e32 v[168:169], v126
	v_med3_f32 v68, v154, s41, v1
	v_med3_f32 v150, v155, s41, v1
	v_cvt_pk_fp8_f32 v143, v146, v147
	v_cvt_pk_fp8_f32 v142, v68, v150 op_sel:[0,0,1]
	v_pk_fma_f32 v[150:151], v[62:63], v[170:171], v[14:15]
	v_med3_f32 v68, v138, s41, v1
	v_pk_fma_f32 v[150:151], v[50:51], v[180:181], v[150:151]
	v_med3_f32 v138, v139, s41, v1
	v_pk_fma_f32 v[150:151], v[34:35], v[168:169], v[150:151]
	v_cvt_pk_fp8_f32 v143, v68, v138 op_sel:[0,0,1]
	s_waitcnt vmcnt(36)
	v_cvt_pk_f32_fp8_e32 v[158:159], v122
	v_cvt_pk_f32_fp8_sdwa v[146:147], v122 src0_sel:WORD_1
	v_exp_f32_e32 v68, v150
	v_exp_f32_e32 v163, v151
	v_cvt_pk_f32_fp8_sdwa v[154:155], v126 src0_sel:WORD_1
	v_add_f32_e32 v68, 1.0, v68
	v_rcp_f32_e32 v162, v68
	v_add_f32_e32 v68, 1.0, v163
	v_rcp_f32_e32 v163, v68
	v_pk_fma_f32 v[160:161], v[64:65], v[160:161], v[16:17]
	v_pk_fma_f32 v[164:165], v[58:59], v[164:165], v[10:11]
	v_pk_fma_f32 v[160:161], v[52:53], v[176:177], v[160:161]
	v_pk_fma_f32 v[164:165], v[42:43], v[178:179], v[164:165]
	v_pk_fma_f32 v[160:161], v[36:37], v[154:155], v[160:161]
	v_pk_fma_f32 v[164:165], v[26:27], v[158:159], v[164:165]
	v_pk_mul_f32 v[150:151], v[150:151], v[162:163]
	s_nop 0
	v_pk_mul_f32 v[150:151], v[164:165], v[150:151]
	v_exp_f32_e32 v68, v160
	v_exp_f32_e32 v164, v161
	v_add_co_u32_e32 v138, vcc, s28, v70
	v_add_f32_e32 v68, 1.0, v68
	s_nop 0
	v_addc_co_u32_e32 v139, vcc, 0, v71, vcc
	global_store_dwordx2 v[138:139], v[142:143], off offset:2048
	v_cvt_pk_f32_fp8_e32 v[142:143], v127
	v_rcp_f32_e32 v162, v68
	v_add_f32_e32 v68, 1.0, v164
	v_rcp_f32_e32 v163, v68
	v_pk_fma_f32 v[152:153], v[54:55], v[152:153], v[6:7]
	v_pk_fma_f32 v[156:157], v[60:61], v[156:157], v[12:13]
	v_pk_fma_f32 v[152:153], v[38:39], v[172:173], v[152:153]
	v_pk_mul_f32 v[160:161], v[160:161], v[162:163]
	v_pk_fma_f32 v[152:153], v[22:23], v[142:143], v[152:153]
	v_pk_fma_f32 v[156:157], v[44:45], v[174:175], v[156:157]
	v_exp_f32_e32 v68, v152
	v_exp_f32_e32 v162, v153
	v_pk_fma_f32 v[156:157], v[28:29], v[146:147], v[156:157]
	v_cvt_pk_f32_fp8_sdwa v[126:127], v127 src0_sel:WORD_1
	v_add_f32_e32 v68, 1.0, v68
	v_pk_mul_f32 v[156:157], v[156:157], v[160:161]
	v_rcp_f32_e32 v160, v68
	v_add_f32_e32 v68, 1.0, v162
	v_rcp_f32_e32 v161, v68
	v_pk_fma_f32 v[140:141], v[56:57], v[140:141], v[8:9]
	v_cvt_pk_f32_fp8_e32 v[138:139], v123
	v_pk_fma_f32 v[140:141], v[40:41], v[134:135], v[140:141]
	v_pk_mul_f32 v[152:153], v[152:153], v[160:161]
	v_pk_fma_f32 v[140:141], v[24:25], v[126:127], v[140:141]
	v_pk_fma_f32 v[148:149], v[46:47], v[148:149], v[2:3]
	v_exp_f32_e32 v68, v140
	v_exp_f32_e32 v160, v141
	v_pk_fma_f32 v[148:149], v[30:31], v[166:167], v[148:149]
	v_add_f32_e32 v68, 1.0, v68
	v_pk_fma_f32 v[148:149], v[18:19], v[138:139], v[148:149]
	v_cvt_pk_f32_fp8_sdwa v[122:123], v123 src0_sel:WORD_1
	v_pk_fma_f32 v[144:145], v[48:49], v[144:145], v[4:5]
	v_pk_mul_f32 v[148:149], v[148:149], v[152:153]
	v_rcp_f32_e32 v152, v68
	v_add_f32_e32 v68, 1.0, v160
	v_rcp_f32_e32 v153, v68
	v_pk_fma_f32 v[144:145], v[32:33], v[130:131], v[144:145]
	v_med3_f32 v68, v150, s41, v1
	v_pk_fma_f32 v[144:145], v[20:21], v[122:123], v[144:145]
	v_pk_mul_f32 v[140:141], v[140:141], v[152:153]
	v_med3_f32 v148, v148, s41, v1
	v_pk_mul_f32 v[140:141], v[144:145], v[140:141]
	v_med3_f32 v145, v151, s41, v1
	v_cvt_pk_fp8_f32 v144, v68, v145
	v_med3_f32 v149, v149, s41, v1
	s_waitcnt vmcnt(36)
	v_cvt_pk_f32_fp8_e32 v[164:165], v118
	v_med3_f32 v68, v156, s41, v1
	v_med3_f32 v150, v157, s41, v1
	v_cvt_pk_fp8_f32 v145, v148, v149
	v_cvt_pk_fp8_f32 v144, v68, v150 op_sel:[0,0,1]
	v_pk_fma_f32 v[150:151], v[62:63], v[180:181], v[14:15]
	v_med3_f32 v68, v140, s41, v1
	v_pk_fma_f32 v[150:151], v[50:51], v[168:169], v[150:151]
	v_med3_f32 v140, v141, s41, v1
	v_pk_fma_f32 v[150:151], v[34:35], v[164:165], v[150:151]
	v_cvt_pk_fp8_f32 v145, v68, v140 op_sel:[0,0,1]
	s_waitcnt vmcnt(35)
	v_cvt_pk_f32_fp8_e32 v[160:161], v114
	v_cvt_pk_f32_fp8_sdwa v[148:149], v114 src0_sel:WORD_1
	v_exp_f32_e32 v68, v150
	v_exp_f32_e32 v157, v151
	v_pk_fma_f32 v[162:163], v[58:59], v[178:179], v[10:11]
	v_add_f32_e32 v68, 1.0, v68
	v_rcp_f32_e32 v156, v68
	v_add_f32_e32 v68, 1.0, v157
	v_rcp_f32_e32 v157, v68
	v_cvt_pk_f32_fp8_sdwa v[152:153], v118 src0_sel:WORD_1
	v_pk_fma_f32 v[162:163], v[42:43], v[158:159], v[162:163]
	v_add_co_u32_e32 v140, vcc, s56, v70
	v_pk_fma_f32 v[162:163], v[26:27], v[160:161], v[162:163]
	v_pk_mul_f32 v[150:151], v[150:151], v[156:157]
	s_nop 0
	v_pk_mul_f32 v[150:151], v[162:163], v[150:151]
	v_pk_fma_f32 v[162:163], v[64:65], v[176:177], v[16:17]
	s_nop 0
	v_pk_fma_f32 v[162:163], v[52:53], v[154:155], v[162:163]
	v_addc_co_u32_e32 v141, vcc, 0, v71, vcc
	v_pk_fma_f32 v[162:163], v[36:37], v[152:153], v[162:163]
	global_store_dwordx2 v[140:141], v[144:145], off offset:768
	v_exp_f32_e32 v68, v162
	v_exp_f32_e32 v170, v163
	v_cvt_pk_f32_fp8_e32 v[144:145], v119
	v_add_f32_e32 v68, 1.0, v68
	v_rcp_f32_e32 v156, v68
	v_add_f32_e32 v68, 1.0, v170
	v_rcp_f32_e32 v157, v68
	v_pk_fma_f32 v[170:171], v[60:61], v[174:175], v[12:13]
	v_cvt_pk_f32_fp8_sdwa v[118:119], v119 src0_sel:WORD_1
	v_pk_fma_f32 v[170:171], v[44:45], v[146:147], v[170:171]
	v_pk_mul_f32 v[156:157], v[162:163], v[156:157]
	v_pk_fma_f32 v[170:171], v[28:29], v[148:149], v[170:171]
	v_pk_fma_f32 v[134:135], v[56:57], v[134:135], v[8:9]
	v_pk_mul_f32 v[156:157], v[170:171], v[156:157]
	v_pk_fma_f32 v[170:171], v[54:55], v[172:173], v[6:7]
	s_nop 0
	v_pk_fma_f32 v[170:171], v[38:39], v[142:143], v[170:171]
	v_pk_fma_f32 v[134:135], v[40:41], v[126:127], v[134:135]
	v_pk_fma_f32 v[170:171], v[22:23], v[144:145], v[170:171]
	v_pk_fma_f32 v[134:135], v[24:25], v[118:119], v[134:135]
	v_exp_f32_e32 v68, v170
	v_exp_f32_e32 v172, v171
	v_cvt_pk_f32_fp8_e32 v[140:141], v115
	v_add_f32_e32 v68, 1.0, v68
	v_rcp_f32_e32 v162, v68
	v_add_f32_e32 v68, 1.0, v172
	v_rcp_f32_e32 v163, v68
	v_exp_f32_e32 v68, v134
	v_pk_fma_f32 v[166:167], v[46:47], v[166:167], v[2:3]
	v_pk_mul_f32 v[162:163], v[170:171], v[162:163]
	v_exp_f32_e32 v170, v135
	v_pk_fma_f32 v[166:167], v[30:31], v[138:139], v[166:167]
	v_add_f32_e32 v68, 1.0, v68
	v_pk_fma_f32 v[166:167], v[18:19], v[140:141], v[166:167]
	v_cvt_pk_f32_fp8_sdwa v[114:115], v115 src0_sel:WORD_1
	v_pk_fma_f32 v[130:131], v[48:49], v[130:131], v[4:5]
	v_pk_mul_f32 v[162:163], v[166:167], v[162:163]
	v_rcp_f32_e32 v166, v68
	v_add_f32_e32 v68, 1.0, v170
	v_rcp_f32_e32 v167, v68
	v_pk_fma_f32 v[130:131], v[32:33], v[122:123], v[130:131]
	v_med3_f32 v68, v150, s41, v1
	v_pk_fma_f32 v[130:131], v[20:21], v[114:115], v[130:131]
	v_pk_mul_f32 v[134:135], v[134:135], v[166:167]
	s_waitcnt vmcnt(35)
; __device__ __forceinline__ float clamp448(float x) { return __builtin_amdgcn_fmed3f(x, -448.f, 448.f); }
; __device__ __forceinline__ unsigned pk4_fp8(float a, float b, float c, float d) {
;     int w = __builtin_amdgcn_cvt_pk_fp8_f32(clamp448(a), clamp448(b), 0, false);
;     w = __builtin_amdgcn_cvt_pk_fp8_f32(clamp448(c), clamp448(d), w, true);
;     return (unsigned)w;
; }
	v_cvt_pk_f32_fp8_e32 v[166:167], v110
	v_pk_mul_f32 v[130:131], v[130:131], v[134:135]
	v_med3_f32 v135, v151, s41, v1
	v_cvt_pk_fp8_f32 v134, v68, v135
	v_med3_f32 v68, v156, s41, v1
	v_med3_f32 v151, v162, s41, v1
	v_med3_f32 v156, v163, s41, v1
	v_cvt_pk_fp8_f32 v135, v151, v156
	v_pk_fma_f32 v[168:169], v[62:63], v[168:169], v[14:15]
	v_med3_f32 v150, v157, s41, v1
	v_pk_fma_f32 v[168:169], v[50:51], v[164:165], v[168:169]
	v_cvt_pk_fp8_f32 v134, v68, v150 op_sel:[0,0,1]
	v_med3_f32 v68, v130, s41, v1
	v_med3_f32 v130, v131, s41, v1
	v_pk_fma_f32 v[168:169], v[34:35], v[166:167], v[168:169]
	v_cvt_pk_fp8_f32 v135, v68, v130 op_sel:[0,0,1]
	s_waitcnt vmcnt(34)
	v_cvt_pk_f32_fp8_e32 v[162:163], v106
	v_cvt_pk_f32_fp8_sdwa v[150:151], v106 src0_sel:WORD_1
	v_exp_f32_e32 v68, v168
	v_exp_f32_e32 v171, v169
	v_cvt_pk_f32_fp8_sdwa v[156:157], v110 src0_sel:WORD_1
	v_add_f32_e32 v68, 1.0, v68
	v_rcp_f32_e32 v170, v68
	v_add_f32_e32 v68, 1.0, v171
	v_rcp_f32_e32 v171, v68
	v_pk_fma_f32 v[154:155], v[64:65], v[154:155], v[16:17]
	v_pk_fma_f32 v[158:159], v[58:59], v[158:159], v[10:11]
	v_pk_fma_f32 v[154:155], v[52:53], v[152:153], v[154:155]
	v_pk_mul_f32 v[168:169], v[168:169], v[170:171]
	v_pk_fma_f32 v[154:155], v[36:37], v[156:157], v[154:155]
	v_add_co_u32_e32 v130, vcc, s29, v70
	v_exp_f32_e32 v68, v154
	v_exp_f32_e32 v170, v155
	v_pk_fma_f32 v[158:159], v[42:43], v[160:161], v[158:159]
	v_addc_co_u32_e32 v131, vcc, 0, v71, vcc
	v_pk_fma_f32 v[158:159], v[26:27], v[162:163], v[158:159]
	global_store_dwordx2 v[130:131], v[134:135], off offset:3584
	v_cvt_pk_f32_fp8_e32 v[134:135], v111
	v_add_f32_e32 v68, 1.0, v68
	v_pk_mul_f32 v[158:159], v[158:159], v[168:169]
	v_rcp_f32_e32 v168, v68
	v_add_f32_e32 v68, 1.0, v170
	v_rcp_f32_e32 v169, v68
	v_pk_fma_f32 v[142:143], v[54:55], v[142:143], v[6:7]
	v_pk_fma_f32 v[146:147], v[60:61], v[146:147], v[12:13]
	v_pk_fma_f32 v[142:143], v[38:39], v[144:145], v[142:143]
	v_pk_mul_f32 v[154:155], v[154:155], v[168:169]
	v_pk_fma_f32 v[142:143], v[22:23], v[134:135], v[142:143]
	v_pk_fma_f32 v[146:147], v[44:45], v[148:149], v[146:147]
	v_exp_f32_e32 v68, v142
	v_exp_f32_e32 v168, v143
	v_pk_fma_f32 v[146:147], v[28:29], v[150:151], v[146:147]
	v_cvt_pk_f32_fp8_sdwa v[110:111], v111 src0_sel:WORD_1
	v_add_f32_e32 v68, 1.0, v68
	v_pk_mul_f32 v[146:147], v[146:147], v[154:155]
	v_rcp_f32_e32 v154, v68
	v_add_f32_e32 v68, 1.0, v168
	v_rcp_f32_e32 v155, v68
	v_pk_fma_f32 v[126:127], v[56:57], v[126:127], v[8:9]
	v_cvt_pk_f32_fp8_e32 v[130:131], v107
	v_pk_fma_f32 v[126:127], v[40:41], v[118:119], v[126:127]
	v_pk_mul_f32 v[142:143], v[142:143], v[154:155]
	v_pk_fma_f32 v[126:127], v[24:25], v[110:111], v[126:127]
	v_pk_fma_f32 v[138:139], v[46:47], v[138:139], v[2:3]
	v_exp_f32_e32 v68, v126
	v_exp_f32_e32 v154, v127
	v_pk_fma_f32 v[138:139], v[30:31], v[140:141], v[138:139]
	v_add_f32_e32 v68, 1.0, v68
	v_pk_fma_f32 v[138:139], v[18:19], v[130:131], v[138:139]
	v_cvt_pk_f32_fp8_sdwa v[106:107], v107 src0_sel:WORD_1
	v_pk_fma_f32 v[122:123], v[48:49], v[122:123], v[4:5]
	v_pk_mul_f32 v[138:139], v[138:139], v[142:143]
	v_rcp_f32_e32 v142, v68
	v_add_f32_e32 v68, 1.0, v154
	v_rcp_f32_e32 v143, v68
	v_pk_fma_f32 v[122:123], v[32:33], v[114:115], v[122:123]
	v_med3_f32 v68, v158, s41, v1
	v_pk_fma_f32 v[122:123], v[20:21], v[106:107], v[122:123]
	v_pk_mul_f32 v[126:127], v[126:127], v[142:143]
	v_med3_f32 v138, v138, s41, v1
	v_pk_mul_f32 v[122:123], v[122:123], v[126:127]
	v_med3_f32 v127, v159, s41, v1
	v_cvt_pk_fp8_f32 v126, v68, v127
	v_med3_f32 v139, v139, s41, v1
	s_waitcnt vmcnt(34)
	v_cvt_pk_f32_fp8_e32 v[154:155], v102
	v_cvt_pk_fp8_f32 v127, v138, v139
	v_pk_fma_f32 v[158:159], v[62:63], v[164:165], v[14:15]
	v_med3_f32 v68, v146, s41, v1
	v_med3_f32 v142, v147, s41, v1
	v_pk_fma_f32 v[158:159], v[50:51], v[166:167], v[158:159]
	v_cvt_pk_fp8_f32 v126, v68, v142 op_sel:[0,0,1]
	v_med3_f32 v68, v122, s41, v1
	v_med3_f32 v122, v123, s41, v1
	v_pk_fma_f32 v[158:159], v[34:35], v[154:155], v[158:159]
	v_cvt_pk_fp8_f32 v127, v68, v122 op_sel:[0,0,1]
	s_waitcnt vmcnt(33)
	v_cvt_pk_f32_fp8_e32 v[146:147], v98
	v_cvt_pk_f32_fp8_sdwa v[138:139], v98 src0_sel:WORD_1
	v_exp_f32_e32 v68, v158
	v_exp_f32_e32 v165, v159
	v_cvt_pk_f32_fp8_sdwa v[142:143], v102 src0_sel:WORD_1
	v_add_f32_e32 v68, 1.0, v68
	v_rcp_f32_e32 v164, v68
	v_add_f32_e32 v68, 1.0, v165
	v_rcp_f32_e32 v165, v68
	v_pk_fma_f32 v[152:153], v[64:65], v[152:153], v[16:17]
	v_pk_fma_f32 v[160:161], v[58:59], v[160:161], v[10:11]
	v_pk_fma_f32 v[152:153], v[52:53], v[156:157], v[152:153]
	v_pk_mul_f32 v[158:159], v[158:159], v[164:165]
	v_pk_fma_f32 v[152:153], v[36:37], v[142:143], v[152:153]
	v_add_co_u32_e32 v122, vcc, s57, v70
	v_exp_f32_e32 v68, v152
	v_exp_f32_e32 v164, v153
	v_pk_fma_f32 v[160:161], v[42:43], v[162:163], v[160:161]
	v_addc_co_u32_e32 v123, vcc, 0, v71, vcc
	v_pk_fma_f32 v[160:161], v[26:27], v[146:147], v[160:161]
	global_store_dwordx2 v[122:123], v[126:127], off offset:2304
	v_cvt_pk_f32_fp8_e32 v[126:127], v103
	v_add_f32_e32 v68, 1.0, v68
	v_pk_mul_f32 v[158:159], v[160:161], v[158:159]
	v_rcp_f32_e32 v160, v68
	v_add_f32_e32 v68, 1.0, v164
	v_rcp_f32_e32 v161, v68
	v_pk_fma_f32 v[144:145], v[54:55], v[144:145], v[6:7]
	v_pk_fma_f32 v[148:149], v[60:61], v[148:149], v[12:13]
	v_pk_fma_f32 v[144:145], v[38:39], v[134:135], v[144:145]
	v_pk_mul_f32 v[152:153], v[152:153], v[160:161]
	v_pk_fma_f32 v[144:145], v[22:23], v[126:127], v[144:145]
	v_pk_fma_f32 v[148:149], v[44:45], v[150:151], v[148:149]
	v_exp_f32_e32 v68, v144
	v_exp_f32_e32 v160, v145
	v_pk_fma_f32 v[148:149], v[28:29], v[138:139], v[148:149]
	v_cvt_pk_f32_fp8_sdwa v[102:103], v103 src0_sel:WORD_1
	v_add_f32_e32 v68, 1.0, v68
	v_pk_mul_f32 v[148:149], v[148:149], v[152:153]
	v_rcp_f32_e32 v152, v68
	v_add_f32_e32 v68, 1.0, v160
	v_rcp_f32_e32 v153, v68
	v_pk_fma_f32 v[118:119], v[56:57], v[118:119], v[8:9]
	v_cvt_pk_f32_fp8_e32 v[122:123], v99
	v_pk_fma_f32 v[118:119], v[40:41], v[110:111], v[118:119]
	v_pk_mul_f32 v[144:145], v[144:145], v[152:153]
	v_pk_fma_f32 v[118:119], v[24:25], v[102:103], v[118:119]
	v_pk_fma_f32 v[140:141], v[46:47], v[140:141], v[2:3]
	v_exp_f32_e32 v68, v118
	v_exp_f32_e32 v152, v119
	v_pk_fma_f32 v[140:141], v[30:31], v[130:131], v[140:141]
	v_add_f32_e32 v68, 1.0, v68
	v_pk_fma_f32 v[140:141], v[18:19], v[122:123], v[140:141]
	v_cvt_pk_f32_fp8_sdwa v[98:99], v99 src0_sel:WORD_1
	v_pk_fma_f32 v[114:115], v[48:49], v[114:115], v[4:5]
	v_pk_mul_f32 v[140:141], v[140:141], v[144:145]
	v_rcp_f32_e32 v144, v68
	v_add_f32_e32 v68, 1.0, v152
	v_rcp_f32_e32 v145, v68
	v_pk_fma_f32 v[114:115], v[32:33], v[106:107], v[114:115]
	v_med3_f32 v68, v158, s41, v1
	v_pk_fma_f32 v[114:115], v[20:21], v[98:99], v[114:115]
	v_pk_mul_f32 v[118:119], v[118:119], v[144:145]
	v_med3_f32 v140, v140, s41, v1
	v_pk_mul_f32 v[114:115], v[114:115], v[118:119]
	v_med3_f32 v119, v159, s41, v1
	v_cvt_pk_fp8_f32 v118, v68, v119
	v_med3_f32 v141, v141, s41, v1
	s_waitcnt vmcnt(33)
; __device__ __forceinline__ float clamp448(float x) { return __builtin_amdgcn_fmed3f(x, -448.f, 448.f); }
; __device__ __forceinline__ unsigned pk4_fp8(float a, float b, float c, float d) {
;     int w = __builtin_amdgcn_cvt_pk_fp8_f32(clamp448(a), clamp448(b), 0, false);
;     w = __builtin_amdgcn_cvt_pk_fp8_f32(clamp448(c), clamp448(d), w, true);
;     return (unsigned)w;
; }
	v_cvt_pk_f32_fp8_e32 v[174:175], v94
	v_cvt_pk_fp8_f32 v119, v140, v141
	v_pk_fma_f32 v[140:141], v[62:63], v[166:167], v[14:15]
	v_med3_f32 v68, v148, s41, v1
	v_med3_f32 v144, v149, s41, v1
	v_pk_fma_f32 v[140:141], v[50:51], v[154:155], v[140:141]
	v_cvt_pk_fp8_f32 v118, v68, v144 op_sel:[0,0,1]
	v_med3_f32 v68, v114, s41, v1
	v_med3_f32 v114, v115, s41, v1
	v_pk_fma_f32 v[140:141], v[34:35], v[174:175], v[140:141]
	v_cvt_pk_fp8_f32 v119, v68, v114 op_sel:[0,0,1]
	s_waitcnt vmcnt(32)
	v_cvt_pk_f32_fp8_e32 v[172:173], v90
	v_cvt_pk_f32_fp8_sdwa v[164:165], v90 src0_sel:WORD_1
	v_exp_f32_e32 v68, v140
	v_exp_f32_e32 v145, v141
	v_pk_fma_f32 v[148:149], v[58:59], v[162:163], v[10:11]
	v_add_f32_e32 v68, 1.0, v68
	v_rcp_f32_e32 v144, v68
	v_add_f32_e32 v68, 1.0, v145
	v_rcp_f32_e32 v145, v68
	v_cvt_pk_f32_fp8_sdwa v[170:171], v94 src0_sel:WORD_1
	v_pk_fma_f32 v[148:149], v[42:43], v[146:147], v[148:149]
	v_add_co_u32_e32 v114, vcc, s30, v70
	v_pk_fma_f32 v[148:149], v[26:27], v[172:173], v[148:149]
	v_pk_mul_f32 v[140:141], v[140:141], v[144:145]
	s_nop 0
	v_pk_mul_f32 v[140:141], v[148:149], v[140:141]
	v_pk_fma_f32 v[148:149], v[64:65], v[156:157], v[16:17]
	v_addc_co_u32_e32 v115, vcc, 0, v71, vcc
	v_pk_fma_f32 v[148:149], v[52:53], v[142:143], v[148:149]
	global_store_dwordx2 v[114:115], v[118:119], off offset:1024
	v_pk_fma_f32 v[148:149], v[36:37], v[170:171], v[148:149]
	v_cvt_pk_f32_fp8_e32 v[118:119], v95
	v_exp_f32_e32 v68, v148
	v_exp_f32_e32 v152, v149
	v_add_f32_e32 v68, 1.0, v68
	v_rcp_f32_e32 v144, v68
	v_add_f32_e32 v68, 1.0, v152
	v_rcp_f32_e32 v145, v68
	v_pk_fma_f32 v[134:135], v[54:55], v[134:135], v[6:7]
	v_pk_fma_f32 v[150:151], v[60:61], v[150:151], v[12:13]
	v_pk_fma_f32 v[134:135], v[38:39], v[126:127], v[134:135]
	v_pk_fma_f32 v[150:151], v[44:45], v[138:139], v[150:151]
	v_pk_fma_f32 v[134:135], v[22:23], v[118:119], v[134:135]
	v_pk_fma_f32 v[150:151], v[28:29], v[164:165], v[150:151]
	v_pk_mul_f32 v[144:145], v[148:149], v[144:145]
	s_nop 0
	v_pk_mul_f32 v[144:145], v[150:151], v[144:145]
	v_exp_f32_e32 v68, v134
	v_exp_f32_e32 v150, v135
	v_cvt_pk_f32_fp8_sdwa v[94:95], v95 src0_sel:WORD_1
	v_add_f32_e32 v68, 1.0, v68
	v_rcp_f32_e32 v148, v68
	v_add_f32_e32 v68, 1.0, v150
	v_rcp_f32_e32 v149, v68
	v_pk_fma_f32 v[110:111], v[56:57], v[110:111], v[8:9]
	v_cvt_pk_f32_fp8_e32 v[114:115], v91
	v_pk_fma_f32 v[110:111], v[40:41], v[102:103], v[110:111]
	v_pk_mul_f32 v[134:135], v[134:135], v[148:149]
	v_pk_fma_f32 v[110:111], v[24:25], v[94:95], v[110:111]
	v_pk_fma_f32 v[130:131], v[46:47], v[130:131], v[2:3]
	v_exp_f32_e32 v68, v110
	v_exp_f32_e32 v148, v111
	v_pk_fma_f32 v[130:131], v[30:31], v[122:123], v[130:131]
	v_add_f32_e32 v68, 1.0, v68
	v_pk_fma_f32 v[130:131], v[18:19], v[114:115], v[130:131]
	v_cvt_pk_f32_fp8_sdwa v[90:91], v91 src0_sel:WORD_1
	v_pk_fma_f32 v[106:107], v[48:49], v[106:107], v[4:5]
	v_pk_mul_f32 v[130:131], v[130:131], v[134:135]
	v_rcp_f32_e32 v134, v68
	v_add_f32_e32 v68, 1.0, v148
	v_rcp_f32_e32 v135, v68
	v_pk_fma_f32 v[106:107], v[32:33], v[98:99], v[106:107]
	v_med3_f32 v68, v140, s41, v1
	v_pk_fma_f32 v[106:107], v[20:21], v[90:91], v[106:107]
	v_pk_mul_f32 v[110:111], v[110:111], v[134:135]
	v_med3_f32 v130, v130, s41, v1
	v_pk_mul_f32 v[106:107], v[106:107], v[110:111]
	v_med3_f32 v111, v141, s41, v1
	v_cvt_pk_fp8_f32 v110, v68, v111
	v_med3_f32 v131, v131, s41, v1
	v_cvt_pk_fp8_f32 v111, v130, v131
	s_waitcnt vmcnt(32)
	v_cvt_pk_f32_fp8_e32 v[166:167], v86
	v_med3_f32 v68, v144, s41, v1
	v_med3_f32 v134, v145, s41, v1
	v_cvt_pk_fp8_f32 v110, v68, v134 op_sel:[0,0,1]
	v_med3_f32 v68, v106, s41, v1
	v_med3_f32 v106, v107, s41, v1
	v_cvt_pk_f32_fp8_sdwa v[156:157], v86 src0_sel:WORD_1
	v_cvt_pk_f32_fp8_e32 v[148:149], v87
	v_cvt_pk_f32_fp8_sdwa v[134:135], v87 src0_sel:WORD_1
	v_pk_fma_f32 v[86:87], v[62:63], v[154:155], v[14:15]
	v_cvt_pk_fp8_f32 v111, v68, v106 op_sel:[0,0,1]
	v_pk_fma_f32 v[86:87], v[50:51], v[174:175], v[86:87]
	v_add_co_u32_e32 v106, vcc, s58, v70
	v_pk_fma_f32 v[86:87], v[34:35], v[166:167], v[86:87]
	s_nop 0
	v_addc_co_u32_e32 v107, vcc, 0, v71, vcc
	s_waitcnt vmcnt(31)
	v_cvt_pk_f32_fp8_e32 v[160:161], v82
	v_cvt_pk_f32_fp8_sdwa v[152:153], v82 src0_sel:WORD_1
	v_exp_f32_e32 v68, v86
	global_store_dwordx2 v[106:107], v[110:111], off offset:3840
	v_exp_f32_e32 v106, v87
	v_add_f32_e32 v68, 1.0, v68
	v_rcp_f32_e32 v82, v68
	v_cvt_pk_f32_fp8_e32 v[144:145], v83
	v_add_f32_e32 v68, 1.0, v106
	v_cvt_pk_f32_fp8_sdwa v[140:141], v83 src0_sel:WORD_1
	v_rcp_f32_e32 v83, v68
	v_pk_fma_f32 v[106:107], v[58:59], v[146:147], v[10:11]
	v_pk_fma_f32 v[102:103], v[56:57], v[102:103], v[8:9]
	v_pk_fma_f32 v[106:107], v[42:43], v[172:173], v[106:107]
	v_pk_mul_f32 v[82:83], v[86:87], v[82:83]
	v_pk_fma_f32 v[106:107], v[26:27], v[160:161], v[106:107]
	v_pk_fma_f32 v[122:123], v[46:47], v[122:123], v[2:3]
	v_pk_mul_f32 v[82:83], v[106:107], v[82:83]
	v_pk_fma_f32 v[106:107], v[64:65], v[142:143], v[16:17]
	s_nop 0
	v_pk_fma_f32 v[106:107], v[52:53], v[170:171], v[106:107]
	v_pk_fma_f32 v[102:103], v[40:41], v[94:95], v[102:103]
	v_pk_fma_f32 v[106:107], v[36:37], v[156:157], v[106:107]
	v_pk_fma_f32 v[122:123], v[30:31], v[114:115], v[122:123]
	v_exp_f32_e32 v68, v106
	v_exp_f32_e32 v110, v107
	v_pk_fma_f32 v[102:103], v[24:25], v[134:135], v[102:103]
	v_add_f32_e32 v68, 1.0, v68
	v_rcp_f32_e32 v86, v68
	v_add_f32_e32 v68, 1.0, v110
	v_rcp_f32_e32 v87, v68
	v_pk_fma_f32 v[110:111], v[60:61], v[138:139], v[12:13]
	v_pk_fma_f32 v[122:123], v[18:19], v[144:145], v[122:123]
	v_pk_fma_f32 v[110:111], v[44:45], v[164:165], v[110:111]
	v_pk_mul_f32 v[86:87], v[106:107], v[86:87]
	v_pk_fma_f32 v[110:111], v[28:29], v[152:153], v[110:111]
	v_pk_fma_f32 v[98:99], v[48:49], v[98:99], v[4:5]
	v_pk_mul_f32 v[86:87], v[110:111], v[86:87]
	v_pk_fma_f32 v[110:111], v[54:55], v[126:127], v[6:7]
	s_nop 0
	v_pk_fma_f32 v[110:111], v[38:39], v[118:119], v[110:111]
	v_pk_fma_f32 v[98:99], v[32:33], v[90:91], v[98:99]
	v_pk_fma_f32 v[110:111], v[22:23], v[148:149], v[110:111]
	v_pk_fma_f32 v[98:99], v[20:21], v[140:141], v[98:99]
	v_exp_f32_e32 v68, v110
	v_exp_f32_e32 v126, v111
	v_add_f32_e32 v68, 1.0, v68
	v_rcp_f32_e32 v106, v68
	v_add_f32_e32 v68, 1.0, v126
	v_rcp_f32_e32 v107, v68
	v_exp_f32_e32 v68, v102
	v_med3_f32 v83, v83, s41, v1
	v_pk_mul_f32 v[106:107], v[110:111], v[106:107]
	s_nop 0
	v_pk_mul_f32 v[106:107], v[122:123], v[106:107]
	v_exp_f32_e32 v122, v103
	v_add_f32_e32 v68, 1.0, v68
	v_rcp_f32_e32 v110, v68
	v_add_f32_e32 v68, 1.0, v122
	v_rcp_f32_e32 v111, v68
	v_med3_f32 v68, v82, s41, v1
	v_cvt_pk_fp8_f32 v82, v68, v83
	v_pk_mul_f32 v[102:103], v[102:103], v[110:111]
	v_med3_f32 v68, v86, s41, v1
	v_pk_mul_f32 v[98:99], v[98:99], v[102:103]
	v_med3_f32 v86, v87, s41, v1
	v_med3_f32 v87, v106, s41, v1
	v_med3_f32 v102, v107, s41, v1
	v_cvt_pk_fp8_f32 v83, v87, v102
	s_waitcnt vmcnt(31)
; __device__ __forceinline__ float clamp448(float x) { return __builtin_amdgcn_fmed3f(x, -448.f, 448.f); }
; __device__ __forceinline__ unsigned pk4_fp8(float a, float b, float c, float d) {
;     int w = __builtin_amdgcn_cvt_pk_fp8_f32(clamp448(a), clamp448(b), 0, false);
;     w = __builtin_amdgcn_cvt_pk_fp8_f32(clamp448(c), clamp448(d), w, true);
;     return (unsigned)w;
; }
	v_cvt_pk_f32_fp8_e32 v[168:169], v78
	v_cvt_pk_fp8_f32 v82, v68, v86 op_sel:[0,0,1]
	v_med3_f32 v68, v98, s41, v1
	v_med3_f32 v86, v99, s41, v1
	v_cvt_pk_f32_fp8_sdwa v[158:159], v78 src0_sel:WORD_1
	v_cvt_pk_f32_fp8_e32 v[150:151], v79
	v_cvt_pk_f32_fp8_sdwa v[138:139], v79 src0_sel:WORD_1
	v_pk_fma_f32 v[78:79], v[62:63], v[174:175], v[14:15]
	v_cvt_pk_fp8_f32 v83, v68, v86 op_sel:[0,0,1]
	v_pk_fma_f32 v[78:79], v[50:51], v[166:167], v[78:79]
	v_add_co_u32_e32 v86, vcc, s31, v70
	v_pk_fma_f32 v[78:79], v[34:35], v[168:169], v[78:79]
	s_nop 0
	v_addc_co_u32_e32 v87, vcc, 0, v71, vcc
	s_waitcnt vmcnt(30)
	v_cvt_pk_f32_fp8_e32 v[162:163], v74
	v_cvt_pk_f32_fp8_sdwa v[154:155], v74 src0_sel:WORD_1
	v_exp_f32_e32 v68, v78
	global_store_dwordx2 v[86:87], v[82:83], off offset:2560
	v_exp_f32_e32 v82, v79
	v_add_f32_e32 v68, 1.0, v68
	v_rcp_f32_e32 v74, v68
	v_cvt_pk_f32_fp8_e32 v[146:147], v75
	v_add_f32_e32 v68, 1.0, v82
	v_cvt_pk_f32_fp8_sdwa v[142:143], v75 src0_sel:WORD_1
	v_rcp_f32_e32 v75, v68
	v_pk_fma_f32 v[82:83], v[58:59], v[172:173], v[10:11]
	v_pk_fma_f32 v[94:95], v[56:57], v[94:95], v[8:9]
	v_pk_fma_f32 v[82:83], v[42:43], v[160:161], v[82:83]
	v_pk_mul_f32 v[74:75], v[78:79], v[74:75]
	v_pk_fma_f32 v[82:83], v[26:27], v[162:163], v[82:83]
	v_pk_fma_f32 v[94:95], v[40:41], v[134:135], v[94:95]
	v_pk_mul_f32 v[74:75], v[82:83], v[74:75]
	v_pk_fma_f32 v[82:83], v[64:65], v[170:171], v[16:17]
	s_nop 0
	v_pk_fma_f32 v[82:83], v[52:53], v[156:157], v[82:83]
	v_pk_fma_f32 v[94:95], v[24:25], v[138:139], v[94:95]
	v_pk_fma_f32 v[82:83], v[36:37], v[158:159], v[82:83]
	v_pk_fma_f32 v[90:91], v[48:49], v[90:91], v[4:5]
	v_exp_f32_e32 v68, v82
	v_exp_f32_e32 v86, v83
	v_med3_f32 v75, v75, s41, v1
	v_add_f32_e32 v68, 1.0, v68
	v_rcp_f32_e32 v78, v68
	v_add_f32_e32 v68, 1.0, v86
	v_rcp_f32_e32 v79, v68
	v_pk_fma_f32 v[86:87], v[60:61], v[164:165], v[12:13]
	v_pk_fma_f32 v[90:91], v[32:33], v[140:141], v[90:91]
	v_pk_fma_f32 v[86:87], v[44:45], v[152:153], v[86:87]
	v_pk_mul_f32 v[78:79], v[82:83], v[78:79]
	v_pk_fma_f32 v[86:87], v[28:29], v[154:155], v[86:87]
	s_waitcnt vmcnt(22)
	v_cvt_pk_f32_fp8_e32 v[178:179], v136
	v_pk_mul_f32 v[78:79], v[86:87], v[78:79]
	v_pk_fma_f32 v[86:87], v[54:55], v[118:119], v[6:7]
	s_nop 0
	v_pk_fma_f32 v[86:87], v[38:39], v[148:149], v[86:87]
	v_pk_fma_f32 v[90:91], v[20:21], v[142:143], v[90:91]
	v_pk_fma_f32 v[86:87], v[22:23], v[150:151], v[86:87]
	s_nop 0
	v_exp_f32_e32 v68, v86
	v_exp_f32_e32 v98, v87
	v_pk_fma_f32 v[166:167], v[62:63], v[166:167], v[14:15]
	v_add_f32_e32 v68, 1.0, v68
	v_rcp_f32_e32 v82, v68
	v_add_f32_e32 v68, 1.0, v98
	v_rcp_f32_e32 v83, v68
	v_pk_fma_f32 v[98:99], v[46:47], v[114:115], v[2:3]
	s_nop 0
	v_pk_fma_f32 v[98:99], v[30:31], v[144:145], v[98:99]
	v_pk_mul_f32 v[82:83], v[86:87], v[82:83]
	v_pk_fma_f32 v[98:99], v[18:19], v[146:147], v[98:99]
	v_exp_f32_e32 v68, v94
	v_pk_mul_f32 v[82:83], v[98:99], v[82:83]
	v_exp_f32_e32 v98, v95
	v_add_f32_e32 v68, 1.0, v68
	v_rcp_f32_e32 v86, v68
	v_add_f32_e32 v68, 1.0, v98
	v_rcp_f32_e32 v87, v68
	v_med3_f32 v68, v74, s41, v1
	v_cvt_pk_fp8_f32 v74, v68, v75
	v_med3_f32 v68, v78, s41, v1
	v_med3_f32 v78, v79, s41, v1
	v_med3_f32 v79, v82, s41, v1
	v_med3_f32 v82, v83, s41, v1
	v_cvt_pk_fp8_f32 v75, v79, v82
	v_pk_mul_f32 v[86:87], v[94:95], v[86:87]
	v_pk_fma_f32 v[166:167], v[50:51], v[168:169], v[166:167]
	v_pk_mul_f32 v[86:87], v[90:91], v[86:87]
	v_cvt_pk_fp8_f32 v74, v68, v78 op_sel:[0,0,1]
	v_med3_f32 v68, v86, s41, v1
	v_med3_f32 v78, v87, s41, v1
	v_pk_fma_f32 v[166:167], v[34:35], v[178:179], v[166:167]
	v_cvt_pk_fp8_f32 v75, v68, v78 op_sel:[0,0,1]
	s_waitcnt vmcnt(21)
	v_cvt_pk_f32_fp8_e32 v[176:177], v132
	v_cvt_pk_f32_fp8_sdwa v[172:173], v132 src0_sel:WORD_1
	v_exp_f32_e32 v68, v166
	v_exp_f32_e32 v181, v167
	v_cvt_pk_f32_fp8_sdwa v[174:175], v136 src0_sel:WORD_1
	v_add_f32_e32 v68, 1.0, v68
	v_rcp_f32_e32 v180, v68
	v_add_f32_e32 v68, 1.0, v181
	v_rcp_f32_e32 v181, v68
	v_pk_fma_f32 v[156:157], v[64:65], v[156:157], v[16:17]
	v_pk_fma_f32 v[160:161], v[58:59], v[160:161], v[10:11]
	v_pk_fma_f32 v[156:157], v[52:53], v[158:159], v[156:157]
	v_pk_mul_f32 v[166:167], v[166:167], v[180:181]
	v_pk_fma_f32 v[156:157], v[36:37], v[174:175], v[156:157]
	v_pk_fma_f32 v[160:161], v[42:43], v[162:163], v[160:161]
	v_exp_f32_e32 v68, v156
	v_exp_f32_e32 v180, v157
	v_pk_fma_f32 v[160:161], v[26:27], v[176:177], v[160:161]
	v_cvt_pk_f32_fp8_e32 v[170:171], v137
	v_add_f32_e32 v68, 1.0, v68
	v_pk_mul_f32 v[160:161], v[160:161], v[166:167]
	v_rcp_f32_e32 v166, v68
	v_add_f32_e32 v68, 1.0, v180
	v_rcp_f32_e32 v167, v68
	v_pk_fma_f32 v[148:149], v[54:55], v[148:149], v[6:7]
	v_pk_fma_f32 v[152:153], v[60:61], v[152:153], v[12:13]
	v_pk_fma_f32 v[148:149], v[38:39], v[150:151], v[148:149]
	v_pk_mul_f32 v[156:157], v[156:157], v[166:167]
	v_pk_fma_f32 v[148:149], v[22:23], v[170:171], v[148:149]
	v_pk_fma_f32 v[152:153], v[44:45], v[154:155], v[152:153]
	v_exp_f32_e32 v68, v148
	v_exp_f32_e32 v166, v149
	v_pk_fma_f32 v[152:153], v[28:29], v[172:173], v[152:153]
	v_cvt_pk_f32_fp8_sdwa v[136:137], v137 src0_sel:WORD_1
	v_add_f32_e32 v68, 1.0, v68
	v_pk_mul_f32 v[152:153], v[152:153], v[156:157]
	v_rcp_f32_e32 v156, v68
	v_add_f32_e32 v68, 1.0, v166
	v_rcp_f32_e32 v157, v68
	v_pk_fma_f32 v[134:135], v[56:57], v[134:135], v[8:9]
	v_cvt_pk_f32_fp8_e32 v[164:165], v133
	v_pk_fma_f32 v[134:135], v[40:41], v[138:139], v[134:135]
	v_pk_mul_f32 v[148:149], v[148:149], v[156:157]
	v_pk_fma_f32 v[134:135], v[24:25], v[136:137], v[134:135]
	v_pk_fma_f32 v[144:145], v[46:47], v[144:145], v[2:3]
	v_exp_f32_e32 v68, v134
	v_exp_f32_e32 v156, v135
	v_pk_fma_f32 v[144:145], v[30:31], v[146:147], v[144:145]
	v_add_f32_e32 v68, 1.0, v68
	v_pk_fma_f32 v[144:145], v[18:19], v[164:165], v[144:145]
	v_cvt_pk_f32_fp8_sdwa v[132:133], v133 src0_sel:WORD_1
	v_pk_fma_f32 v[140:141], v[48:49], v[140:141], v[4:5]
	v_pk_mul_f32 v[144:145], v[144:145], v[148:149]
	v_rcp_f32_e32 v148, v68
	v_add_f32_e32 v68, 1.0, v156
	v_rcp_f32_e32 v149, v68
	v_pk_fma_f32 v[140:141], v[32:33], v[142:143], v[140:141]
	v_med3_f32 v68, v160, s41, v1
	v_pk_fma_f32 v[140:141], v[20:21], v[132:133], v[140:141]
	v_pk_mul_f32 v[134:135], v[134:135], v[148:149]
	v_add_co_u32_e32 v78, vcc, s59, v70
	v_pk_mul_f32 v[134:135], v[140:141], v[134:135]
	v_med3_f32 v141, v161, s41, v1
	v_cvt_pk_fp8_f32 v140, v68, v141
	v_med3_f32 v144, v144, s41, v1
	v_med3_f32 v145, v145, s41, v1
	s_waitcnt vmcnt(20)
; #define CV_LOAD(G_, V_, r0_) do { _Pragma("unroll") for (int i_ = 0; i_ < 8; ++i_) { G_[i_] = *(const GAS v2u*)(ap + (size_t)((r0_) + i_) * F2); V_[i_] = *(const GAS v2u*)(ap + (size_t)((r0_) + i_) * F2 + 128); } } while (0)
; __device__ __forceinline__ void conv_phase(Frame& F) {
;     ...
;         CV_LOAD(GA, VA, 0); CV_LOAD(GB, VB, 8); CV_COMP(GA, VA, 0); CV_LOAD(GA, VA, 16); CV_COMP(GB, VB, 8); CV_LOAD(GB, VB, 24); CV_COMP(GA, VA, 16); CV_COMP(GB, VB, 24);
	v_cvt_pk_f32_fp8_e32 v[166:167], v128
	v_addc_co_u32_e32 v79, vcc, 0, v71, vcc
	v_med3_f32 v68, v152, s41, v1
	v_med3_f32 v148, v153, s41, v1
	v_cvt_pk_fp8_f32 v141, v144, v145
	global_store_dwordx2 v[78:79], v[74:75], off offset:1280
	v_add_co_u32_e32 v74, vcc, s60, v72
	v_cvt_pk_fp8_f32 v140, v68, v148 op_sel:[0,0,1]
	v_pk_fma_f32 v[148:149], v[62:63], v[168:169], v[14:15]
	v_addc_co_u32_e32 v75, vcc, 0, v73, vcc
	v_pk_fma_f32 v[148:149], v[50:51], v[178:179], v[148:149]
	v_add_co_u32_e32 v78, vcc, s61, v72
	v_med3_f32 v68, v134, s41, v1
	v_med3_f32 v134, v135, s41, v1
	v_pk_fma_f32 v[148:149], v[34:35], v[166:167], v[148:149]
	v_addc_co_u32_e32 v79, vcc, 0, v73, vcc
	v_cvt_pk_fp8_f32 v141, v68, v134 op_sel:[0,0,1]
	global_load_dwordx2 v[130:131], v[74:75], off nt
	global_load_dwordx2 v[126:127], v[74:75], off offset:128 nt
	global_load_dwordx2 v[122:123], v[78:79], off offset:1536 nt
	global_load_dwordx2 v[118:119], v[78:79], off offset:1664 nt
	v_add_co_u32_e32 v74, vcc, s62, v72
	s_waitcnt vmcnt(24)
	v_cvt_pk_f32_fp8_e32 v[156:157], v124
	v_cvt_pk_f32_fp8_sdwa v[144:145], v124 src0_sel:WORD_1
	v_exp_f32_e32 v68, v148
	v_addc_co_u32_e32 v75, vcc, 0, v73, vcc
	v_exp_f32_e32 v161, v149
	v_add_co_u32_e32 v78, vcc, s63, v72
	v_cvt_pk_f32_fp8_sdwa v[152:153], v128 src0_sel:WORD_1
	s_nop 0
	v_addc_co_u32_e32 v79, vcc, 0, v73, vcc
	global_load_dwordx2 v[114:115], v[74:75], off offset:3072 nt
	global_load_dwordx2 v[110:111], v[74:75], off offset:3200 nt
	global_load_dwordx2 v[106:107], v[78:79], off offset:512 nt
	global_load_dwordx2 v[102:103], v[78:79], off offset:640 nt
	v_add_co_u32_e32 v74, vcc, s64, v72
	v_add_f32_e32 v68, 1.0, v68
	s_nop 0
	v_addc_co_u32_e32 v75, vcc, 0, v73, vcc
	v_rcp_f32_e32 v160, v68
	v_add_f32_e32 v68, 1.0, v161
	v_add_co_u32_e32 v78, vcc, s65, v72
	v_rcp_f32_e32 v161, v68
	v_pk_fma_f32 v[158:159], v[64:65], v[158:159], v[16:17]
	v_addc_co_u32_e32 v79, vcc, 0, v73, vcc
	v_pk_fma_f32 v[162:163], v[58:59], v[162:163], v[10:11]
	v_pk_fma_f32 v[158:159], v[52:53], v[174:175], v[158:159]
	global_load_dwordx2 v[98:99], v[74:75], off offset:2048 nt
	global_load_dwordx2 v[94:95], v[74:75], off offset:2176 nt
	global_load_dwordx2 v[90:91], v[78:79], off offset:3584 nt
	global_load_dwordx2 v[86:87], v[78:79], off offset:3712 nt
	v_add_co_u32_e32 v74, vcc, s66, v72
	v_pk_fma_f32 v[162:163], v[42:43], v[176:177], v[162:163]
	v_pk_fma_f32 v[158:159], v[36:37], v[152:153], v[158:159]
	v_addc_co_u32_e32 v75, vcc, 0, v73, vcc
	v_pk_fma_f32 v[162:163], v[26:27], v[156:157], v[162:163]
	v_add_co_u32_e32 v72, vcc, s67, v72
	v_pk_mul_f32 v[148:149], v[148:149], v[160:161]
	s_nop 0
	v_pk_mul_f32 v[148:149], v[162:163], v[148:149]
	v_exp_f32_e32 v68, v158
	v_addc_co_u32_e32 v73, vcc, 0, v73, vcc
	v_exp_f32_e32 v162, v159
	v_add_co_u32_e32 v134, vcc, s33, v70
	global_load_dwordx2 v[82:83], v[74:75], off offset:1024 nt
	global_load_dwordx2 v[78:79], v[74:75], off offset:1152 nt
	s_nop 0
	global_load_dwordx2 v[74:75], v[72:73], off offset:2560 nt
	s_nop 0
	global_load_dwordx2 v[72:73], v[72:73], off offset:2688 nt
	v_addc_co_u32_e32 v135, vcc, 0, v71, vcc
	global_store_dwordx2 v[134:135], v[140:141], off
	v_cvt_pk_f32_fp8_e32 v[140:141], v129
	v_add_f32_e32 v68, 1.0, v68
	v_rcp_f32_e32 v160, v68
	v_add_f32_e32 v68, 1.0, v162
	v_rcp_f32_e32 v161, v68
	v_pk_fma_f32 v[150:151], v[54:55], v[150:151], v[6:7]
	v_pk_fma_f32 v[154:155], v[60:61], v[154:155], v[12:13]
	v_pk_fma_f32 v[150:151], v[38:39], v[170:171], v[150:151]
	v_pk_mul_f32 v[158:159], v[158:159], v[160:161]
	v_pk_fma_f32 v[150:151], v[22:23], v[140:141], v[150:151]
	v_pk_fma_f32 v[154:155], v[44:45], v[172:173], v[154:155]
	v_exp_f32_e32 v68, v150
	v_exp_f32_e32 v160, v151
	v_pk_fma_f32 v[154:155], v[28:29], v[144:145], v[154:155]
	v_cvt_pk_f32_fp8_sdwa v[128:129], v129 src0_sel:WORD_1
	v_add_f32_e32 v68, 1.0, v68
	v_pk_mul_f32 v[154:155], v[154:155], v[158:159]
	v_rcp_f32_e32 v158, v68
	v_add_f32_e32 v68, 1.0, v160
	v_rcp_f32_e32 v159, v68
	v_pk_fma_f32 v[138:139], v[56:57], v[138:139], v[8:9]
	v_cvt_pk_f32_fp8_e32 v[134:135], v125
	v_pk_fma_f32 v[138:139], v[40:41], v[136:137], v[138:139]
	v_pk_mul_f32 v[150:151], v[150:151], v[158:159]
	v_pk_fma_f32 v[138:139], v[24:25], v[128:129], v[138:139]
	v_pk_fma_f32 v[146:147], v[46:47], v[146:147], v[2:3]
	v_exp_f32_e32 v68, v138
	v_exp_f32_e32 v158, v139
	v_pk_fma_f32 v[146:147], v[30:31], v[164:165], v[146:147]
	v_add_f32_e32 v68, 1.0, v68
	v_pk_fma_f32 v[146:147], v[18:19], v[134:135], v[146:147]
	v_cvt_pk_f32_fp8_sdwa v[124:125], v125 src0_sel:WORD_1
	v_pk_fma_f32 v[142:143], v[48:49], v[142:143], v[4:5]
	v_pk_mul_f32 v[146:147], v[146:147], v[150:151]
	v_rcp_f32_e32 v150, v68
	v_add_f32_e32 v68, 1.0, v158
	v_rcp_f32_e32 v151, v68
	v_pk_fma_f32 v[142:143], v[32:33], v[132:133], v[142:143]
	v_med3_f32 v68, v148, s41, v1
	v_pk_fma_f32 v[142:143], v[20:21], v[124:125], v[142:143]
	v_pk_mul_f32 v[138:139], v[138:139], v[150:151]
	v_med3_f32 v146, v146, s41, v1
	v_pk_mul_f32 v[138:139], v[142:143], v[138:139]
	v_med3_f32 v143, v149, s41, v1
	v_cvt_pk_fp8_f32 v142, v68, v143
	v_med3_f32 v147, v147, s41, v1
	s_waitcnt vmcnt(36)
	v_cvt_pk_f32_fp8_e32 v[162:163], v120
	v_med3_f32 v68, v154, s41, v1
	v_med3_f32 v148, v155, s41, v1
	v_cvt_pk_fp8_f32 v143, v146, v147
	v_cvt_pk_fp8_f32 v142, v68, v148 op_sel:[0,0,1]
	v_pk_fma_f32 v[148:149], v[62:63], v[178:179], v[14:15]
	v_med3_f32 v68, v138, s41, v1
	v_pk_fma_f32 v[148:149], v[50:51], v[166:167], v[148:149]
	v_med3_f32 v138, v139, s41, v1
	v_pk_fma_f32 v[148:149], v[34:35], v[162:163], v[148:149]
	v_cvt_pk_fp8_f32 v143, v68, v138 op_sel:[0,0,1]
	s_waitcnt vmcnt(35)
; __device__ __forceinline__ float clamp448(float x) { return __builtin_amdgcn_fmed3f(x, -448.f, 448.f); }
; __device__ __forceinline__ unsigned pk4_fp8(float a, float b, float c, float d) {
;     int w = __builtin_amdgcn_cvt_pk_fp8_f32(clamp448(a), clamp448(b), 0, false);
;     w = __builtin_amdgcn_cvt_pk_fp8_f32(clamp448(c), clamp448(d), w, true);
;     return (unsigned)w;
; }
	v_cvt_pk_f32_fp8_e32 v[158:159], v116
	v_cvt_pk_f32_fp8_sdwa v[146:147], v116 src0_sel:WORD_1
	v_exp_f32_e32 v68, v148
	v_exp_f32_e32 v155, v149
	v_pk_fma_f32 v[160:161], v[58:59], v[176:177], v[10:11]
	v_add_f32_e32 v68, 1.0, v68
	v_rcp_f32_e32 v154, v68
	v_add_f32_e32 v68, 1.0, v155
	v_rcp_f32_e32 v155, v68
	v_cvt_pk_f32_fp8_sdwa v[150:151], v120 src0_sel:WORD_1
	v_pk_fma_f32 v[160:161], v[42:43], v[156:157], v[160:161]
	v_add_co_u32_e32 v138, vcc, s68, v70
	v_pk_fma_f32 v[160:161], v[26:27], v[158:159], v[160:161]
	v_pk_mul_f32 v[148:149], v[148:149], v[154:155]
	s_nop 0
	v_pk_mul_f32 v[148:149], v[160:161], v[148:149]
	v_pk_fma_f32 v[160:161], v[64:65], v[174:175], v[16:17]
	s_nop 0
	v_pk_fma_f32 v[160:161], v[52:53], v[152:153], v[160:161]
	v_addc_co_u32_e32 v139, vcc, 0, v71, vcc
	v_pk_fma_f32 v[160:161], v[36:37], v[150:151], v[160:161]
	global_store_dwordx2 v[138:139], v[142:143], off offset:2816
	v_exp_f32_e32 v68, v160
	v_exp_f32_e32 v168, v161
	v_cvt_pk_f32_fp8_e32 v[142:143], v121
	v_add_f32_e32 v68, 1.0, v68
	v_rcp_f32_e32 v154, v68
	v_add_f32_e32 v68, 1.0, v168
	v_rcp_f32_e32 v155, v68
	v_pk_fma_f32 v[168:169], v[60:61], v[172:173], v[12:13]
	v_cvt_pk_f32_fp8_sdwa v[120:121], v121 src0_sel:WORD_1
	v_pk_fma_f32 v[168:169], v[44:45], v[144:145], v[168:169]
	v_pk_mul_f32 v[154:155], v[160:161], v[154:155]
	v_pk_fma_f32 v[168:169], v[28:29], v[146:147], v[168:169]
	v_pk_fma_f32 v[136:137], v[56:57], v[136:137], v[8:9]
	v_pk_mul_f32 v[154:155], v[168:169], v[154:155]
	v_pk_fma_f32 v[168:169], v[54:55], v[170:171], v[6:7]
	s_nop 0
	v_pk_fma_f32 v[168:169], v[38:39], v[140:141], v[168:169]
	v_pk_fma_f32 v[136:137], v[40:41], v[128:129], v[136:137]
	v_pk_fma_f32 v[168:169], v[22:23], v[142:143], v[168:169]
	v_pk_fma_f32 v[136:137], v[24:25], v[120:121], v[136:137]
	v_exp_f32_e32 v68, v168
	v_exp_f32_e32 v170, v169
	v_cvt_pk_f32_fp8_e32 v[138:139], v117
	v_add_f32_e32 v68, 1.0, v68
	v_rcp_f32_e32 v160, v68
	v_add_f32_e32 v68, 1.0, v170
	v_rcp_f32_e32 v161, v68
	v_exp_f32_e32 v68, v136
	v_pk_fma_f32 v[164:165], v[46:47], v[164:165], v[2:3]
	v_pk_mul_f32 v[160:161], v[168:169], v[160:161]
	v_exp_f32_e32 v168, v137
	v_pk_fma_f32 v[164:165], v[30:31], v[134:135], v[164:165]
	v_add_f32_e32 v68, 1.0, v68
	v_pk_fma_f32 v[164:165], v[18:19], v[138:139], v[164:165]
	v_cvt_pk_f32_fp8_sdwa v[116:117], v117 src0_sel:WORD_1
	v_pk_fma_f32 v[132:133], v[48:49], v[132:133], v[4:5]
	v_pk_mul_f32 v[160:161], v[164:165], v[160:161]
	v_rcp_f32_e32 v164, v68
	v_add_f32_e32 v68, 1.0, v168
	v_rcp_f32_e32 v165, v68
	v_pk_fma_f32 v[132:133], v[32:33], v[124:125], v[132:133]
	v_med3_f32 v68, v148, s41, v1
	v_pk_fma_f32 v[132:133], v[20:21], v[116:117], v[132:133]
	v_pk_mul_f32 v[136:137], v[136:137], v[164:165]
	s_waitcnt vmcnt(35)
	v_cvt_pk_f32_fp8_e32 v[164:165], v112
	v_pk_mul_f32 v[132:133], v[132:133], v[136:137]
	v_med3_f32 v137, v149, s41, v1
	v_cvt_pk_fp8_f32 v136, v68, v137
	v_med3_f32 v68, v154, s41, v1
	v_med3_f32 v149, v160, s41, v1
	v_med3_f32 v154, v161, s41, v1
	v_cvt_pk_fp8_f32 v137, v149, v154
	v_pk_fma_f32 v[166:167], v[62:63], v[166:167], v[14:15]
	v_med3_f32 v148, v155, s41, v1
	v_pk_fma_f32 v[166:167], v[50:51], v[162:163], v[166:167]
	v_cvt_pk_fp8_f32 v136, v68, v148 op_sel:[0,0,1]
	v_med3_f32 v68, v132, s41, v1
	v_med3_f32 v132, v133, s41, v1
	v_pk_fma_f32 v[166:167], v[34:35], v[164:165], v[166:167]
	v_cvt_pk_fp8_f32 v137, v68, v132 op_sel:[0,0,1]
	s_waitcnt vmcnt(34)
	v_cvt_pk_f32_fp8_e32 v[160:161], v108
	v_cvt_pk_f32_fp8_sdwa v[148:149], v108 src0_sel:WORD_1
	v_exp_f32_e32 v68, v166
	v_exp_f32_e32 v169, v167
	v_cvt_pk_f32_fp8_sdwa v[154:155], v112 src0_sel:WORD_1
	v_add_f32_e32 v68, 1.0, v68
	v_rcp_f32_e32 v168, v68
	v_add_f32_e32 v68, 1.0, v169
	v_rcp_f32_e32 v169, v68
	v_pk_fma_f32 v[152:153], v[64:65], v[152:153], v[16:17]
	v_pk_fma_f32 v[156:157], v[58:59], v[156:157], v[10:11]
	v_pk_fma_f32 v[152:153], v[52:53], v[150:151], v[152:153]
	v_pk_mul_f32 v[166:167], v[166:167], v[168:169]
	v_pk_fma_f32 v[152:153], v[36:37], v[154:155], v[152:153]
	v_add_co_u32_e32 v132, vcc, s34, v70
	v_exp_f32_e32 v68, v152
	v_exp_f32_e32 v168, v153
	v_pk_fma_f32 v[156:157], v[42:43], v[158:159], v[156:157]
	v_addc_co_u32_e32 v133, vcc, 0, v71, vcc
	v_pk_fma_f32 v[156:157], v[26:27], v[160:161], v[156:157]
	global_store_dwordx2 v[132:133], v[136:137], off offset:1536
	v_cvt_pk_f32_fp8_e32 v[136:137], v113
	v_add_f32_e32 v68, 1.0, v68
	v_pk_mul_f32 v[156:157], v[156:157], v[166:167]
	v_rcp_f32_e32 v166, v68
	v_add_f32_e32 v68, 1.0, v168
	v_rcp_f32_e32 v167, v68
	v_pk_fma_f32 v[140:141], v[54:55], v[140:141], v[6:7]
	v_pk_fma_f32 v[144:145], v[60:61], v[144:145], v[12:13]
	v_pk_fma_f32 v[140:141], v[38:39], v[142:143], v[140:141]
	v_pk_mul_f32 v[152:153], v[152:153], v[166:167]
	v_pk_fma_f32 v[140:141], v[22:23], v[136:137], v[140:141]
	v_pk_fma_f32 v[144:145], v[44:45], v[146:147], v[144:145]
	v_exp_f32_e32 v68, v140
	v_exp_f32_e32 v166, v141
	v_pk_fma_f32 v[144:145], v[28:29], v[148:149], v[144:145]
	v_cvt_pk_f32_fp8_sdwa v[112:113], v113 src0_sel:WORD_1
	v_add_f32_e32 v68, 1.0, v68
	v_pk_mul_f32 v[144:145], v[144:145], v[152:153]
	v_rcp_f32_e32 v152, v68
	v_add_f32_e32 v68, 1.0, v166
	v_rcp_f32_e32 v153, v68
	v_pk_fma_f32 v[128:129], v[56:57], v[128:129], v[8:9]
	v_cvt_pk_f32_fp8_e32 v[132:133], v109
	v_pk_fma_f32 v[128:129], v[40:41], v[120:121], v[128:129]
	v_pk_mul_f32 v[140:141], v[140:141], v[152:153]
	v_pk_fma_f32 v[128:129], v[24:25], v[112:113], v[128:129]
	v_pk_fma_f32 v[134:135], v[46:47], v[134:135], v[2:3]
	v_exp_f32_e32 v68, v128
	v_exp_f32_e32 v152, v129
	v_pk_fma_f32 v[134:135], v[30:31], v[138:139], v[134:135]
	v_add_f32_e32 v68, 1.0, v68
	v_pk_fma_f32 v[134:135], v[18:19], v[132:133], v[134:135]
	v_cvt_pk_f32_fp8_sdwa v[108:109], v109 src0_sel:WORD_1
	v_pk_fma_f32 v[124:125], v[48:49], v[124:125], v[4:5]
	v_pk_mul_f32 v[134:135], v[134:135], v[140:141]
	v_rcp_f32_e32 v140, v68
	v_add_f32_e32 v68, 1.0, v152
	v_rcp_f32_e32 v141, v68
	v_pk_fma_f32 v[124:125], v[32:33], v[116:117], v[124:125]
	v_med3_f32 v68, v156, s41, v1
	v_pk_fma_f32 v[124:125], v[20:21], v[108:109], v[124:125]
	v_pk_mul_f32 v[128:129], v[128:129], v[140:141]
	v_med3_f32 v134, v134, s41, v1
	v_pk_mul_f32 v[124:125], v[124:125], v[128:129]
	v_med3_f32 v129, v157, s41, v1
	v_cvt_pk_fp8_f32 v128, v68, v129
	v_med3_f32 v135, v135, s41, v1
	s_waitcnt vmcnt(34)
; __device__ __forceinline__ float clamp448(float x) { return __builtin_amdgcn_fmed3f(x, -448.f, 448.f); }
; __device__ __forceinline__ unsigned pk4_fp8(float a, float b, float c, float d) {
;     int w = __builtin_amdgcn_cvt_pk_fp8_f32(clamp448(a), clamp448(b), 0, false);
;     w = __builtin_amdgcn_cvt_pk_fp8_f32(clamp448(c), clamp448(d), w, true);
;     return (unsigned)w;
; }
	v_cvt_pk_f32_fp8_e32 v[156:157], v104
	v_cvt_pk_fp8_f32 v129, v134, v135
	v_pk_fma_f32 v[134:135], v[62:63], v[162:163], v[14:15]
	v_med3_f32 v68, v144, s41, v1
	v_med3_f32 v140, v145, s41, v1
	v_pk_fma_f32 v[134:135], v[50:51], v[164:165], v[134:135]
	v_cvt_pk_fp8_f32 v128, v68, v140 op_sel:[0,0,1]
	v_med3_f32 v68, v124, s41, v1
	v_med3_f32 v124, v125, s41, v1
	v_pk_fma_f32 v[134:135], v[34:35], v[156:157], v[134:135]
	v_cvt_pk_fp8_f32 v129, v68, v124 op_sel:[0,0,1]
	s_waitcnt vmcnt(33)
	v_cvt_pk_f32_fp8_e32 v[152:153], v100
	v_cvt_pk_f32_fp8_sdwa v[140:141], v100 src0_sel:WORD_1
	v_exp_f32_e32 v68, v134
	v_exp_f32_e32 v163, v135
	v_cvt_pk_f32_fp8_sdwa v[144:145], v104 src0_sel:WORD_1
	v_add_f32_e32 v68, 1.0, v68
	v_rcp_f32_e32 v162, v68
	v_add_f32_e32 v68, 1.0, v163
	v_rcp_f32_e32 v163, v68
	v_pk_fma_f32 v[150:151], v[64:65], v[150:151], v[16:17]
	v_pk_fma_f32 v[158:159], v[58:59], v[158:159], v[10:11]
	v_pk_fma_f32 v[150:151], v[52:53], v[154:155], v[150:151]
	v_pk_mul_f32 v[134:135], v[134:135], v[162:163]
	v_pk_fma_f32 v[150:151], v[36:37], v[144:145], v[150:151]
	v_add_co_u32_e32 v124, vcc, s69, v70
	v_exp_f32_e32 v68, v150
	v_exp_f32_e32 v162, v151
	v_pk_fma_f32 v[158:159], v[42:43], v[160:161], v[158:159]
	v_addc_co_u32_e32 v125, vcc, 0, v71, vcc
	v_pk_fma_f32 v[158:159], v[26:27], v[152:153], v[158:159]
	global_store_dwordx2 v[124:125], v[128:129], off offset:256
	v_cvt_pk_f32_fp8_e32 v[128:129], v105
	v_add_f32_e32 v68, 1.0, v68
	v_pk_mul_f32 v[134:135], v[158:159], v[134:135]
	v_rcp_f32_e32 v158, v68
	v_add_f32_e32 v68, 1.0, v162
	v_rcp_f32_e32 v159, v68
	v_pk_fma_f32 v[142:143], v[54:55], v[142:143], v[6:7]
	v_pk_fma_f32 v[146:147], v[60:61], v[146:147], v[12:13]
	v_pk_fma_f32 v[142:143], v[38:39], v[136:137], v[142:143]
	v_pk_mul_f32 v[150:151], v[150:151], v[158:159]
	v_pk_fma_f32 v[142:143], v[22:23], v[128:129], v[142:143]
	v_pk_fma_f32 v[146:147], v[44:45], v[148:149], v[146:147]
	v_exp_f32_e32 v68, v142
	v_exp_f32_e32 v158, v143
	v_pk_fma_f32 v[146:147], v[28:29], v[140:141], v[146:147]
	v_cvt_pk_f32_fp8_sdwa v[104:105], v105 src0_sel:WORD_1
	v_add_f32_e32 v68, 1.0, v68
	v_pk_mul_f32 v[146:147], v[146:147], v[150:151]
	v_rcp_f32_e32 v150, v68
	v_add_f32_e32 v68, 1.0, v158
	v_rcp_f32_e32 v151, v68
	v_pk_fma_f32 v[120:121], v[56:57], v[120:121], v[8:9]
	v_cvt_pk_f32_fp8_e32 v[124:125], v101
	v_pk_fma_f32 v[120:121], v[40:41], v[112:113], v[120:121]
	v_pk_mul_f32 v[142:143], v[142:143], v[150:151]
	v_pk_fma_f32 v[120:121], v[24:25], v[104:105], v[120:121]
	v_pk_fma_f32 v[138:139], v[46:47], v[138:139], v[2:3]
	v_exp_f32_e32 v68, v120
	v_exp_f32_e32 v150, v121
	v_pk_fma_f32 v[138:139], v[30:31], v[132:133], v[138:139]
	v_add_f32_e32 v68, 1.0, v68
	v_pk_fma_f32 v[138:139], v[18:19], v[124:125], v[138:139]
	v_cvt_pk_f32_fp8_sdwa v[100:101], v101 src0_sel:WORD_1
	v_pk_fma_f32 v[116:117], v[48:49], v[116:117], v[4:5]
	v_pk_mul_f32 v[138:139], v[138:139], v[142:143]
	v_rcp_f32_e32 v142, v68
	v_add_f32_e32 v68, 1.0, v150
	v_rcp_f32_e32 v143, v68
	v_pk_fma_f32 v[116:117], v[32:33], v[108:109], v[116:117]
	v_med3_f32 v68, v134, s41, v1
	v_pk_fma_f32 v[116:117], v[20:21], v[100:101], v[116:117]
	v_pk_mul_f32 v[120:121], v[120:121], v[142:143]
	v_med3_f32 v134, v147, s41, v1
	v_pk_mul_f32 v[116:117], v[116:117], v[120:121]
	v_med3_f32 v121, v135, s41, v1
	v_cvt_pk_fp8_f32 v120, v68, v121
	v_med3_f32 v135, v138, s41, v1
	v_med3_f32 v138, v139, s41, v1
	v_cvt_pk_fp8_f32 v121, v135, v138
	v_med3_f32 v68, v146, s41, v1
	v_cvt_pk_fp8_f32 v120, v68, v134 op_sel:[0,0,1]
	v_med3_f32 v68, v116, s41, v1
	v_med3_f32 v116, v117, s41, v1
	v_cvt_pk_fp8_f32 v121, v68, v116 op_sel:[0,0,1]
	v_add_co_u32_e32 v116, vcc, s35, v70
	s_waitcnt vmcnt(33)
	v_cvt_pk_f32_fp8_e32 v[158:159], v96
	v_addc_co_u32_e32 v117, vcc, 0, v71, vcc
	global_store_dwordx2 v[116:117], v[120:121], off offset:3072
	v_pk_fma_f32 v[116:117], v[62:63], v[164:165], v[14:15]
	s_waitcnt vmcnt(33)
	v_cvt_pk_f32_fp8_e32 v[150:151], v92
	v_pk_fma_f32 v[116:117], v[50:51], v[156:157], v[116:117]
	v_cvt_pk_f32_fp8_sdwa v[138:139], v92 src0_sel:WORD_1
	v_pk_fma_f32 v[146:147], v[34:35], v[158:159], v[116:117]
	v_cvt_pk_f32_fp8_sdwa v[142:143], v96 src0_sel:WORD_1
	v_exp_f32_e32 v68, v146
	v_exp_f32_e32 v162, v147
	v_cvt_pk_f32_fp8_e32 v[120:121], v93
	v_add_f32_e32 v68, 1.0, v68
	v_rcp_f32_e32 v92, v68
	v_add_f32_e32 v68, 1.0, v162
	v_cvt_pk_f32_fp8_sdwa v[116:117], v93 src0_sel:WORD_1
	v_rcp_f32_e32 v93, v68
	v_pk_fma_f32 v[154:155], v[64:65], v[154:155], v[16:17]
	v_pk_fma_f32 v[160:161], v[58:59], v[160:161], v[10:11]
	v_pk_fma_f32 v[154:155], v[52:53], v[144:145], v[154:155]
	v_pk_fma_f32 v[160:161], v[42:43], v[152:153], v[160:161]
	v_pk_fma_f32 v[154:155], v[36:37], v[142:143], v[154:155]
	v_pk_fma_f32 v[160:161], v[26:27], v[150:151], v[160:161]
	v_pk_mul_f32 v[92:93], v[146:147], v[92:93]
	s_nop 0
	v_pk_mul_f32 v[92:93], v[160:161], v[92:93]
	v_exp_f32_e32 v68, v154
	v_exp_f32_e32 v160, v155
	v_cvt_pk_f32_fp8_e32 v[134:135], v97
	v_add_f32_e32 v68, 1.0, v68
	v_rcp_f32_e32 v146, v68
	v_add_f32_e32 v68, 1.0, v160
	v_rcp_f32_e32 v147, v68
	v_pk_fma_f32 v[136:137], v[54:55], v[136:137], v[6:7]
	v_pk_fma_f32 v[148:149], v[60:61], v[148:149], v[12:13]
	v_pk_fma_f32 v[136:137], v[38:39], v[128:129], v[136:137]
	v_pk_mul_f32 v[146:147], v[154:155], v[146:147]
	v_pk_fma_f32 v[136:137], v[22:23], v[134:135], v[136:137]
	v_pk_fma_f32 v[148:149], v[44:45], v[140:141], v[148:149]
	v_exp_f32_e32 v68, v136
	v_exp_f32_e32 v154, v137
	v_pk_fma_f32 v[148:149], v[28:29], v[138:139], v[148:149]
	v_cvt_pk_f32_fp8_sdwa v[96:97], v97 src0_sel:WORD_1
	v_add_f32_e32 v68, 1.0, v68
; __device__ __forceinline__ float clamp448(float x) { return __builtin_amdgcn_fmed3f(x, -448.f, 448.f); }
; __device__ __forceinline__ unsigned pk4_fp8(float a, float b, float c, float d) {
;     int w = __builtin_amdgcn_cvt_pk_fp8_f32(clamp448(a), clamp448(b), 0, false);
;     w = __builtin_amdgcn_cvt_pk_fp8_f32(clamp448(c), clamp448(d), w, true);
;     return (unsigned)w;
; }
	v_pk_mul_f32 v[146:147], v[148:149], v[146:147]
	v_rcp_f32_e32 v148, v68
	v_add_f32_e32 v68, 1.0, v154
	v_rcp_f32_e32 v149, v68
	v_pk_fma_f32 v[112:113], v[56:57], v[112:113], v[8:9]
	v_pk_fma_f32 v[132:133], v[46:47], v[132:133], v[2:3]
	v_pk_fma_f32 v[112:113], v[40:41], v[104:105], v[112:113]
	v_pk_mul_f32 v[136:137], v[136:137], v[148:149]
	v_pk_fma_f32 v[112:113], v[24:25], v[96:97], v[112:113]
	v_pk_fma_f32 v[132:133], v[30:31], v[124:125], v[132:133]
	v_exp_f32_e32 v68, v112
	v_exp_f32_e32 v148, v113
	v_pk_fma_f32 v[132:133], v[18:19], v[120:121], v[132:133]
	v_add_f32_e32 v68, 1.0, v68
	v_pk_fma_f32 v[108:109], v[48:49], v[108:109], v[4:5]
	v_pk_mul_f32 v[132:133], v[132:133], v[136:137]
	v_rcp_f32_e32 v136, v68
	v_add_f32_e32 v68, 1.0, v148
	v_rcp_f32_e32 v137, v68
	v_pk_fma_f32 v[108:109], v[32:33], v[100:101], v[108:109]
	v_med3_f32 v68, v92, s41, v1
	v_pk_fma_f32 v[108:109], v[20:21], v[116:117], v[108:109]
	v_pk_mul_f32 v[112:113], v[112:113], v[136:137]
	v_med3_f32 v93, v93, s41, v1
	v_pk_mul_f32 v[108:109], v[108:109], v[112:113]
	v_cvt_pk_fp8_f32 v92, v68, v93
	v_med3_f32 v113, v132, s41, v1
	v_med3_f32 v132, v133, s41, v1
	v_cvt_pk_fp8_f32 v93, v113, v132
	v_med3_f32 v68, v146, s41, v1
	v_med3_f32 v112, v147, s41, v1
	v_cvt_pk_fp8_f32 v92, v68, v112 op_sel:[0,0,1]
	v_med3_f32 v68, v108, s41, v1
	v_med3_f32 v108, v109, s41, v1
	v_cvt_pk_fp8_f32 v93, v68, v108 op_sel:[0,0,1]
	v_add_co_u32_e32 v108, vcc, s70, v70
	s_waitcnt vmcnt(32)
	v_cvt_pk_f32_fp8_e32 v[148:149], v88
	v_addc_co_u32_e32 v109, vcc, 0, v71, vcc
	global_store_dwordx2 v[108:109], v[92:93], off offset:1792
	v_pk_fma_f32 v[92:93], v[62:63], v[156:157], v[14:15]
	s_waitcnt vmcnt(32)
	v_cvt_pk_f32_fp8_e32 v[146:147], v84
	v_pk_fma_f32 v[92:93], v[50:51], v[158:159], v[92:93]
	v_cvt_pk_f32_fp8_sdwa v[132:133], v84 src0_sel:WORD_1
	v_pk_fma_f32 v[92:93], v[34:35], v[148:149], v[92:93]
	v_cvt_pk_f32_fp8_sdwa v[136:137], v88 src0_sel:WORD_1
	v_exp_f32_e32 v68, v92
	v_exp_f32_e32 v155, v93
	v_pk_fma_f32 v[144:145], v[64:65], v[144:145], v[16:17]
	v_add_f32_e32 v68, 1.0, v68
	v_rcp_f32_e32 v154, v68
	v_add_f32_e32 v68, 1.0, v155
	v_rcp_f32_e32 v155, v68
	v_pk_fma_f32 v[144:145], v[52:53], v[142:143], v[144:145]
	v_pk_fma_f32 v[152:153], v[58:59], v[152:153], v[10:11]
	v_pk_fma_f32 v[144:145], v[36:37], v[136:137], v[144:145]
	v_pk_mul_f32 v[92:93], v[92:93], v[154:155]
	v_exp_f32_e32 v68, v144
	v_exp_f32_e32 v154, v145
	v_pk_fma_f32 v[152:153], v[42:43], v[150:151], v[152:153]
	v_cvt_pk_f32_fp8_e32 v[112:113], v89
	v_pk_fma_f32 v[152:153], v[26:27], v[146:147], v[152:153]
	v_add_f32_e32 v68, 1.0, v68
	v_pk_fma_f32 v[128:129], v[54:55], v[128:129], v[6:7]
	v_pk_mul_f32 v[92:93], v[152:153], v[92:93]
	v_rcp_f32_e32 v152, v68
	v_add_f32_e32 v68, 1.0, v154
	v_rcp_f32_e32 v153, v68
	v_pk_fma_f32 v[128:129], v[38:39], v[134:135], v[128:129]
	v_pk_fma_f32 v[140:141], v[60:61], v[140:141], v[12:13]
	v_pk_fma_f32 v[128:129], v[22:23], v[112:113], v[128:129]
	v_pk_mul_f32 v[144:145], v[144:145], v[152:153]
	v_exp_f32_e32 v68, v128
	v_exp_f32_e32 v152, v129
	v_pk_fma_f32 v[140:141], v[44:45], v[138:139], v[140:141]
	v_cvt_pk_f32_fp8_sdwa v[88:89], v89 src0_sel:WORD_1
	v_pk_fma_f32 v[140:141], v[28:29], v[132:133], v[140:141]
	v_add_f32_e32 v68, 1.0, v68
	v_pk_fma_f32 v[104:105], v[56:57], v[104:105], v[8:9]
	v_pk_mul_f32 v[140:141], v[140:141], v[144:145]
	v_rcp_f32_e32 v144, v68
	v_add_f32_e32 v68, 1.0, v152
	v_rcp_f32_e32 v145, v68
	v_pk_fma_f32 v[104:105], v[40:41], v[96:97], v[104:105]
	v_cvt_pk_f32_fp8_e32 v[108:109], v85
	v_pk_fma_f32 v[104:105], v[24:25], v[88:89], v[104:105]
	v_pk_mul_f32 v[128:129], v[128:129], v[144:145]
	v_exp_f32_e32 v68, v104
	v_pk_fma_f32 v[124:125], v[46:47], v[124:125], v[2:3]
	v_exp_f32_e32 v144, v105
	v_pk_fma_f32 v[124:125], v[30:31], v[120:121], v[124:125]
	v_add_f32_e32 v68, 1.0, v68
	v_pk_fma_f32 v[124:125], v[18:19], v[108:109], v[124:125]
	v_cvt_pk_f32_fp8_sdwa v[84:85], v85 src0_sel:WORD_1
	v_pk_fma_f32 v[100:101], v[48:49], v[100:101], v[4:5]
	v_pk_mul_f32 v[124:125], v[124:125], v[128:129]
	v_rcp_f32_e32 v128, v68
	v_add_f32_e32 v68, 1.0, v144
	v_rcp_f32_e32 v129, v68
	v_pk_fma_f32 v[100:101], v[32:33], v[116:117], v[100:101]
	v_med3_f32 v68, v92, s41, v1
	v_pk_fma_f32 v[100:101], v[20:21], v[84:85], v[100:101]
	v_pk_mul_f32 v[104:105], v[104:105], v[128:129]
	v_med3_f32 v93, v93, s41, v1
	v_pk_mul_f32 v[100:101], v[100:101], v[104:105]
	v_cvt_pk_fp8_f32 v92, v68, v93
	v_med3_f32 v105, v124, s41, v1
	v_med3_f32 v124, v125, s41, v1
	v_cvt_pk_fp8_f32 v93, v105, v124
	v_med3_f32 v68, v140, s41, v1
	v_med3_f32 v104, v141, s41, v1
	v_cvt_pk_fp8_f32 v92, v68, v104 op_sel:[0,0,1]
	v_med3_f32 v68, v100, s41, v1
	v_med3_f32 v100, v101, s41, v1
	v_cvt_pk_fp8_f32 v93, v68, v100 op_sel:[0,0,1]
	v_add_co_u32_e32 v100, vcc, s36, v70
	s_waitcnt vmcnt(31)
	v_cvt_pk_f32_fp8_e32 v[152:153], v80
	v_addc_co_u32_e32 v101, vcc, 0, v71, vcc
	global_store_dwordx2 v[100:101], v[92:93], off offset:512
	v_pk_fma_f32 v[92:93], v[62:63], v[158:159], v[14:15]
	s_waitcnt vmcnt(31)
; __device__ __forceinline__ float clamp448(float x) { return __builtin_amdgcn_fmed3f(x, -448.f, 448.f); }
; __device__ __forceinline__ unsigned pk4_fp8(float a, float b, float c, float d) {
;     int w = __builtin_amdgcn_cvt_pk_fp8_f32(clamp448(a), clamp448(b), 0, false);
;     w = __builtin_amdgcn_cvt_pk_fp8_f32(clamp448(c), clamp448(d), w, true);
;     return (unsigned)w;
; }
	v_cvt_pk_f32_fp8_e32 v[144:145], v76
	v_pk_fma_f32 v[92:93], v[50:51], v[148:149], v[92:93]
	v_cvt_pk_f32_fp8_sdwa v[128:129], v76 src0_sel:WORD_1
	v_pk_fma_f32 v[104:105], v[34:35], v[152:153], v[92:93]
	v_cvt_pk_f32_fp8_sdwa v[140:141], v80 src0_sel:WORD_1
	v_exp_f32_e32 v68, v104
	v_exp_f32_e32 v154, v105
	v_cvt_pk_f32_fp8_e32 v[100:101], v77
	v_add_f32_e32 v68, 1.0, v68
	v_rcp_f32_e32 v76, v68
	v_add_f32_e32 v68, 1.0, v154
	v_cvt_pk_f32_fp8_sdwa v[92:93], v77 src0_sel:WORD_1
	v_rcp_f32_e32 v77, v68
	v_pk_fma_f32 v[142:143], v[64:65], v[142:143], v[16:17]
	v_pk_fma_f32 v[150:151], v[58:59], v[150:151], v[10:11]
	v_pk_fma_f32 v[142:143], v[52:53], v[136:137], v[142:143]
	v_pk_fma_f32 v[150:151], v[42:43], v[146:147], v[150:151]
	v_pk_fma_f32 v[142:143], v[36:37], v[140:141], v[142:143]
	v_pk_fma_f32 v[150:151], v[26:27], v[144:145], v[150:151]
	v_pk_mul_f32 v[76:77], v[104:105], v[76:77]
	s_nop 0
	v_pk_mul_f32 v[76:77], v[150:151], v[76:77]
	v_exp_f32_e32 v68, v142
	v_exp_f32_e32 v150, v143
	v_cvt_pk_f32_fp8_e32 v[124:125], v81
	v_add_f32_e32 v68, 1.0, v68
	v_rcp_f32_e32 v104, v68
	v_add_f32_e32 v68, 1.0, v150
	v_rcp_f32_e32 v105, v68
	v_pk_fma_f32 v[134:135], v[54:55], v[134:135], v[6:7]
	v_pk_fma_f32 v[138:139], v[60:61], v[138:139], v[12:13]
	v_pk_fma_f32 v[134:135], v[38:39], v[112:113], v[134:135]
	v_pk_mul_f32 v[104:105], v[142:143], v[104:105]
	v_pk_fma_f32 v[134:135], v[22:23], v[124:125], v[134:135]
	v_pk_fma_f32 v[138:139], v[44:45], v[132:133], v[138:139]
	v_exp_f32_e32 v68, v134
	v_exp_f32_e32 v142, v135
	v_pk_fma_f32 v[138:139], v[28:29], v[128:129], v[138:139]
	v_cvt_pk_f32_fp8_sdwa v[80:81], v81 src0_sel:WORD_1
	v_add_f32_e32 v68, 1.0, v68
	v_pk_mul_f32 v[104:105], v[138:139], v[104:105]
	v_rcp_f32_e32 v138, v68
	v_add_f32_e32 v68, 1.0, v142
	v_rcp_f32_e32 v139, v68
	v_pk_fma_f32 v[96:97], v[56:57], v[96:97], v[8:9]
	v_pk_fma_f32 v[120:121], v[46:47], v[120:121], v[2:3]
	v_pk_fma_f32 v[96:97], v[40:41], v[88:89], v[96:97]
	v_pk_mul_f32 v[134:135], v[134:135], v[138:139]
	v_pk_fma_f32 v[96:97], v[24:25], v[80:81], v[96:97]
	v_pk_fma_f32 v[120:121], v[30:31], v[108:109], v[120:121]
	v_exp_f32_e32 v68, v96
	v_exp_f32_e32 v138, v97
	v_pk_fma_f32 v[120:121], v[18:19], v[100:101], v[120:121]
	v_add_f32_e32 v68, 1.0, v68
	v_pk_fma_f32 v[116:117], v[48:49], v[116:117], v[4:5]
	v_pk_mul_f32 v[120:121], v[120:121], v[134:135]
	v_rcp_f32_e32 v134, v68
	v_add_f32_e32 v68, 1.0, v138
	v_rcp_f32_e32 v135, v68
	v_pk_fma_f32 v[116:117], v[32:33], v[84:85], v[116:117]
	v_med3_f32 v68, v76, s41, v1
	v_pk_fma_f32 v[116:117], v[20:21], v[92:93], v[116:117]
	v_pk_mul_f32 v[96:97], v[96:97], v[134:135]
	v_med3_f32 v77, v77, s41, v1
	v_pk_mul_f32 v[96:97], v[116:117], v[96:97]
	v_cvt_pk_fp8_f32 v76, v68, v77
	v_med3_f32 v68, v104, s41, v1
	v_med3_f32 v104, v105, s41, v1
	v_med3_f32 v105, v120, s41, v1
	v_med3_f32 v116, v121, s41, v1
	v_cvt_pk_fp8_f32 v77, v105, v116
	v_cvt_pk_fp8_f32 v76, v68, v104 op_sel:[0,0,1]
	v_med3_f32 v68, v96, s41, v1
	v_med3_f32 v96, v97, s41, v1
	v_cvt_pk_fp8_f32 v77, v68, v96 op_sel:[0,0,1]
	v_add_co_u32_e32 v96, vcc, s71, v70
	s_waitcnt vmcnt(22)
	v_cvt_pk_f32_fp8_e32 v[138:139], v130
	v_addc_co_u32_e32 v97, vcc, 0, v71, vcc
	global_store_dwordx2 v[96:97], v[76:77], off offset:3328
	v_pk_fma_f32 v[96:97], v[62:63], v[148:149], v[14:15]
	v_cvt_pk_f32_fp8_sdwa v[134:135], v130 src0_sel:WORD_1
	v_pk_fma_f32 v[96:97], v[50:51], v[152:153], v[96:97]
	v_cvt_pk_f32_fp8_e32 v[116:117], v131
	v_pk_fma_f32 v[142:143], v[34:35], v[138:139], v[96:97]
	v_cvt_pk_f32_fp8_sdwa v[76:77], v131 src0_sel:WORD_1
	v_exp_f32_e32 v68, v142
	v_exp_f32_e32 v148, v143
	s_waitcnt vmcnt(22)
	v_cvt_pk_f32_fp8_e32 v[130:131], v126
	v_add_f32_e32 v68, 1.0, v68
	v_cvt_pk_f32_fp8_sdwa v[120:121], v126 src0_sel:WORD_1
	v_rcp_f32_e32 v126, v68
	v_add_f32_e32 v68, 1.0, v148
	v_cvt_pk_f32_fp8_e32 v[104:105], v127
	v_cvt_pk_f32_fp8_sdwa v[96:97], v127 src0_sel:WORD_1
	v_rcp_f32_e32 v127, v68
	v_pk_fma_f32 v[136:137], v[64:65], v[136:137], v[16:17]
	v_pk_fma_f32 v[146:147], v[58:59], v[146:147], v[10:11]
	v_pk_fma_f32 v[136:137], v[52:53], v[140:141], v[136:137]
	v_pk_fma_f32 v[146:147], v[42:43], v[144:145], v[146:147]
	v_pk_fma_f32 v[136:137], v[36:37], v[134:135], v[136:137]
	v_pk_fma_f32 v[146:147], v[26:27], v[130:131], v[146:147]
	v_pk_mul_f32 v[126:127], v[142:143], v[126:127]
	s_nop 0
	v_pk_mul_f32 v[126:127], v[146:147], v[126:127]
	v_exp_f32_e32 v68, v136
	v_exp_f32_e32 v146, v137
	v_add_f32_e32 v68, 1.0, v68
	v_rcp_f32_e32 v142, v68
	v_add_f32_e32 v68, 1.0, v146
	v_rcp_f32_e32 v143, v68
	v_pk_fma_f32 v[112:113], v[54:55], v[112:113], v[6:7]
	v_pk_fma_f32 v[132:133], v[60:61], v[132:133], v[12:13]
	v_pk_fma_f32 v[112:113], v[38:39], v[124:125], v[112:113]
	v_pk_mul_f32 v[136:137], v[136:137], v[142:143]
	v_pk_fma_f32 v[112:113], v[22:23], v[116:117], v[112:113]
	v_pk_fma_f32 v[132:133], v[44:45], v[128:129], v[132:133]
	v_exp_f32_e32 v68, v112
	v_exp_f32_e32 v142, v113
	v_pk_fma_f32 v[132:133], v[28:29], v[120:121], v[132:133]
	v_add_f32_e32 v68, 1.0, v68
	v_pk_fma_f32 v[88:89], v[56:57], v[88:89], v[8:9]
	v_pk_mul_f32 v[132:133], v[132:133], v[136:137]
	v_rcp_f32_e32 v136, v68
	v_add_f32_e32 v68, 1.0, v142
	v_rcp_f32_e32 v137, v68
	v_pk_fma_f32 v[88:89], v[40:41], v[80:81], v[88:89]
	v_pk_fma_f32 v[108:109], v[46:47], v[108:109], v[2:3]
	v_pk_fma_f32 v[88:89], v[24:25], v[76:77], v[88:89]
	v_pk_mul_f32 v[112:113], v[112:113], v[136:137]
	v_exp_f32_e32 v68, v88
	v_exp_f32_e32 v136, v89
	v_pk_fma_f32 v[108:109], v[30:31], v[100:101], v[108:109]
	v_add_f32_e32 v68, 1.0, v68
	v_pk_fma_f32 v[108:109], v[18:19], v[104:105], v[108:109]
	v_pk_fma_f32 v[84:85], v[48:49], v[84:85], v[4:5]
	s_nop 0
	v_pk_fma_f32 v[84:85], v[32:33], v[92:93], v[84:85]
	v_pk_mul_f32 v[108:109], v[108:109], v[112:113]
	v_rcp_f32_e32 v112, v68
	v_add_f32_e32 v68, 1.0, v136
	v_rcp_f32_e32 v113, v68
	v_pk_fma_f32 v[84:85], v[20:21], v[96:97], v[84:85]
	v_med3_f32 v68, v126, s41, v1
	v_pk_mul_f32 v[88:89], v[88:89], v[112:113]
	v_med3_f32 v108, v108, s41, v1
	v_pk_mul_f32 v[84:85], v[84:85], v[88:89]
	v_med3_f32 v89, v127, s41, v1
	v_cvt_pk_fp8_f32 v88, v68, v89
	v_med3_f32 v109, v109, s41, v1
	v_cvt_pk_fp8_f32 v89, v108, v109
	v_med3_f32 v68, v132, s41, v1
	v_med3_f32 v112, v133, s41, v1
	v_cvt_pk_fp8_f32 v88, v68, v112 op_sel:[0,0,1]
	v_med3_f32 v68, v84, s41, v1
	v_med3_f32 v84, v85, s41, v1
	v_cvt_pk_fp8_f32 v89, v68, v84 op_sel:[0,0,1]
	v_add_co_u32_e32 v84, vcc, s37, v70
	s_waitcnt vmcnt(21)
; __device__ __forceinline__ float clamp448(float x) { return __builtin_amdgcn_fmed3f(x, -448.f, 448.f); }
; __device__ __forceinline__ unsigned pk4_fp8(float a, float b, float c, float d) {
;     int w = __builtin_amdgcn_cvt_pk_fp8_f32(clamp448(a), clamp448(b), 0, false);
;     w = __builtin_amdgcn_cvt_pk_fp8_f32(clamp448(c), clamp448(d), w, true);
;     return (unsigned)w;
; }
	v_cvt_pk_f32_fp8_e32 v[136:137], v122
	v_addc_co_u32_e32 v85, vcc, 0, v71, vcc
	global_store_dwordx2 v[84:85], v[88:89], off offset:2048
	v_pk_fma_f32 v[88:89], v[62:63], v[152:153], v[14:15]
	v_cvt_pk_f32_fp8_sdwa v[126:127], v122 src0_sel:WORD_1
	v_pk_fma_f32 v[88:89], v[50:51], v[138:139], v[88:89]
	v_cvt_pk_f32_fp8_e32 v[112:113], v123
	v_pk_fma_f32 v[142:143], v[34:35], v[136:137], v[88:89]
	v_cvt_pk_f32_fp8_sdwa v[84:85], v123 src0_sel:WORD_1
	v_exp_f32_e32 v68, v142
	v_exp_f32_e32 v146, v143
	s_waitcnt vmcnt(21)
	v_cvt_pk_f32_fp8_e32 v[132:133], v118
	v_add_f32_e32 v68, 1.0, v68
	v_cvt_pk_f32_fp8_sdwa v[122:123], v118 src0_sel:WORD_1
	v_rcp_f32_e32 v118, v68
	v_add_f32_e32 v68, 1.0, v146
	v_cvt_pk_f32_fp8_e32 v[108:109], v119
	v_cvt_pk_f32_fp8_sdwa v[88:89], v119 src0_sel:WORD_1
	v_rcp_f32_e32 v119, v68
	v_pk_fma_f32 v[140:141], v[64:65], v[140:141], v[16:17]
	v_pk_fma_f32 v[144:145], v[58:59], v[144:145], v[10:11]
	v_pk_fma_f32 v[140:141], v[52:53], v[134:135], v[140:141]
	v_pk_fma_f32 v[144:145], v[42:43], v[130:131], v[144:145]
	v_pk_fma_f32 v[140:141], v[36:37], v[126:127], v[140:141]
	v_pk_fma_f32 v[144:145], v[26:27], v[132:133], v[144:145]
	v_pk_mul_f32 v[118:119], v[142:143], v[118:119]
	s_nop 0
	v_pk_mul_f32 v[118:119], v[144:145], v[118:119]
	v_exp_f32_e32 v68, v140
	v_exp_f32_e32 v144, v141
	v_add_f32_e32 v68, 1.0, v68
	v_rcp_f32_e32 v142, v68
	v_add_f32_e32 v68, 1.0, v144
	v_rcp_f32_e32 v143, v68
	v_pk_fma_f32 v[124:125], v[54:55], v[124:125], v[6:7]
	v_pk_fma_f32 v[128:129], v[60:61], v[128:129], v[12:13]
	v_pk_fma_f32 v[124:125], v[38:39], v[116:117], v[124:125]
	v_pk_mul_f32 v[140:141], v[140:141], v[142:143]
	v_pk_fma_f32 v[124:125], v[22:23], v[112:113], v[124:125]
	v_pk_fma_f32 v[128:129], v[44:45], v[120:121], v[128:129]
	v_exp_f32_e32 v68, v124
	v_exp_f32_e32 v142, v125
	v_pk_fma_f32 v[128:129], v[28:29], v[122:123], v[128:129]
	v_add_f32_e32 v68, 1.0, v68
	v_pk_fma_f32 v[80:81], v[56:57], v[80:81], v[8:9]
	v_pk_mul_f32 v[128:129], v[128:129], v[140:141]
	v_rcp_f32_e32 v140, v68
	v_add_f32_e32 v68, 1.0, v142
	v_rcp_f32_e32 v141, v68
	v_pk_fma_f32 v[80:81], v[40:41], v[76:77], v[80:81]
	v_pk_fma_f32 v[100:101], v[46:47], v[100:101], v[2:3]
	v_pk_fma_f32 v[80:81], v[24:25], v[84:85], v[80:81]
	v_pk_mul_f32 v[124:125], v[124:125], v[140:141]
	v_exp_f32_e32 v68, v80
	v_exp_f32_e32 v140, v81
	v_pk_fma_f32 v[100:101], v[30:31], v[104:105], v[100:101]
	v_add_f32_e32 v68, 1.0, v68
	v_pk_fma_f32 v[100:101], v[18:19], v[108:109], v[100:101]
	v_pk_fma_f32 v[92:93], v[48:49], v[92:93], v[4:5]
	s_nop 0
	v_pk_fma_f32 v[92:93], v[32:33], v[96:97], v[92:93]
	v_pk_mul_f32 v[100:101], v[100:101], v[124:125]
	v_rcp_f32_e32 v124, v68
	v_add_f32_e32 v68, 1.0, v140
	v_rcp_f32_e32 v125, v68
	v_pk_fma_f32 v[92:93], v[20:21], v[88:89], v[92:93]
	v_med3_f32 v68, v118, s41, v1
	v_pk_mul_f32 v[80:81], v[80:81], v[124:125]
	v_med3_f32 v100, v100, s41, v1
	v_pk_mul_f32 v[80:81], v[92:93], v[80:81]
	v_med3_f32 v93, v119, s41, v1
	v_cvt_pk_fp8_f32 v92, v68, v93
	v_med3_f32 v101, v101, s41, v1
	v_cvt_pk_fp8_f32 v93, v100, v101
	v_med3_f32 v68, v128, s41, v1
	v_med3_f32 v118, v129, s41, v1
	v_cvt_pk_fp8_f32 v92, v68, v118 op_sel:[0,0,1]
	v_med3_f32 v68, v80, s41, v1
	v_med3_f32 v80, v81, s41, v1
	v_cvt_pk_fp8_f32 v93, v68, v80 op_sel:[0,0,1]
	v_add_co_u32_e32 v80, vcc, s72, v70
	s_waitcnt vmcnt(20)
	v_cvt_pk_f32_fp8_e32 v[140:141], v114
	v_addc_co_u32_e32 v81, vcc, 0, v71, vcc
	global_store_dwordx2 v[80:81], v[92:93], off offset:768
	v_pk_fma_f32 v[92:93], v[62:63], v[138:139], v[14:15]
	v_cvt_pk_f32_fp8_sdwa v[124:125], v114 src0_sel:WORD_1
	v_pk_fma_f32 v[92:93], v[50:51], v[136:137], v[92:93]
	v_cvt_pk_f32_fp8_e32 v[118:119], v115
	v_pk_fma_f32 v[138:139], v[34:35], v[140:141], v[92:93]
	v_cvt_pk_f32_fp8_sdwa v[80:81], v115 src0_sel:WORD_1
	v_exp_f32_e32 v68, v138
	v_exp_f32_e32 v142, v139
	s_waitcnt vmcnt(20)
	v_cvt_pk_f32_fp8_e32 v[128:129], v110
	v_add_f32_e32 v68, 1.0, v68
	v_cvt_pk_f32_fp8_sdwa v[114:115], v110 src0_sel:WORD_1
	v_rcp_f32_e32 v110, v68
	v_add_f32_e32 v68, 1.0, v142
	v_cvt_pk_f32_fp8_e32 v[100:101], v111
	v_cvt_pk_f32_fp8_sdwa v[92:93], v111 src0_sel:WORD_1
	v_rcp_f32_e32 v111, v68
	v_pk_fma_f32 v[134:135], v[64:65], v[134:135], v[16:17]
	v_pk_fma_f32 v[130:131], v[58:59], v[130:131], v[10:11]
	v_pk_fma_f32 v[134:135], v[52:53], v[126:127], v[134:135]
	v_pk_mul_f32 v[110:111], v[138:139], v[110:111]
	v_pk_fma_f32 v[134:135], v[36:37], v[124:125], v[134:135]
	v_pk_fma_f32 v[130:131], v[42:43], v[132:133], v[130:131]
	v_exp_f32_e32 v68, v134
	v_exp_f32_e32 v138, v135
	v_pk_fma_f32 v[130:131], v[26:27], v[128:129], v[130:131]
	v_add_f32_e32 v68, 1.0, v68
	v_pk_fma_f32 v[116:117], v[54:55], v[116:117], v[6:7]
	v_pk_mul_f32 v[110:111], v[130:131], v[110:111]
	v_rcp_f32_e32 v130, v68
	v_add_f32_e32 v68, 1.0, v138
	v_rcp_f32_e32 v131, v68
	v_pk_fma_f32 v[116:117], v[38:39], v[112:113], v[116:117]
	v_pk_fma_f32 v[120:121], v[60:61], v[120:121], v[12:13]
	v_pk_fma_f32 v[116:117], v[22:23], v[118:119], v[116:117]
	v_pk_mul_f32 v[130:131], v[134:135], v[130:131]
	v_exp_f32_e32 v68, v116
	v_exp_f32_e32 v134, v117
	v_pk_fma_f32 v[120:121], v[44:45], v[122:123], v[120:121]
	v_add_f32_e32 v68, 1.0, v68
	v_pk_fma_f32 v[120:121], v[28:29], v[114:115], v[120:121]
	v_pk_fma_f32 v[76:77], v[56:57], v[76:77], v[8:9]
	s_nop 0
	v_pk_fma_f32 v[76:77], v[40:41], v[84:85], v[76:77]
	v_pk_mul_f32 v[120:121], v[120:121], v[130:131]
	v_rcp_f32_e32 v130, v68
	v_add_f32_e32 v68, 1.0, v134
	v_rcp_f32_e32 v131, v68
	v_pk_fma_f32 v[76:77], v[24:25], v[80:81], v[76:77]
	v_pk_fma_f32 v[104:105], v[46:47], v[104:105], v[2:3]
	v_pk_mul_f32 v[116:117], v[116:117], v[130:131]
	v_exp_f32_e32 v68, v76
	v_exp_f32_e32 v130, v77
	v_pk_fma_f32 v[104:105], v[30:31], v[108:109], v[104:105]
	v_add_f32_e32 v68, 1.0, v68
	v_pk_fma_f32 v[104:105], v[18:19], v[100:101], v[104:105]
	v_pk_fma_f32 v[96:97], v[48:49], v[96:97], v[4:5]
	s_nop 0
	v_pk_fma_f32 v[96:97], v[32:33], v[88:89], v[96:97]
	v_pk_mul_f32 v[104:105], v[104:105], v[116:117]
	v_rcp_f32_e32 v116, v68
	v_add_f32_e32 v68, 1.0, v130
	v_rcp_f32_e32 v117, v68
	v_pk_fma_f32 v[96:97], v[20:21], v[92:93], v[96:97]
	v_med3_f32 v68, v110, s41, v1
	v_pk_mul_f32 v[76:77], v[76:77], v[116:117]
	v_med3_f32 v104, v104, s41, v1
	v_pk_mul_f32 v[76:77], v[96:97], v[76:77]
	v_med3_f32 v97, v111, s41, v1
	v_cvt_pk_fp8_f32 v96, v68, v97
	v_med3_f32 v105, v105, s41, v1
	v_cvt_pk_fp8_f32 v97, v104, v105
	v_med3_f32 v68, v120, s41, v1
	v_med3_f32 v110, v121, s41, v1
	v_cvt_pk_fp8_f32 v96, v68, v110 op_sel:[0,0,1]
	v_med3_f32 v68, v76, s41, v1
	v_med3_f32 v76, v77, s41, v1
	v_cvt_pk_fp8_f32 v97, v68, v76 op_sel:[0,0,1]
	v_add_co_u32_e32 v76, vcc, s38, v70
	s_waitcnt vmcnt(19)
; __device__ __forceinline__ float clamp448(float x) { return __builtin_amdgcn_fmed3f(x, -448.f, 448.f); }
; __device__ __forceinline__ unsigned pk4_fp8(float a, float b, float c, float d) {
;     int w = __builtin_amdgcn_cvt_pk_fp8_f32(clamp448(a), clamp448(b), 0, false);
;     w = __builtin_amdgcn_cvt_pk_fp8_f32(clamp448(c), clamp448(d), w, true);
;     return (unsigned)w;
; }
	v_cvt_pk_f32_fp8_e32 v[130:131], v106
	v_addc_co_u32_e32 v77, vcc, 0, v71, vcc
	global_store_dwordx2 v[76:77], v[96:97], off offset:3584
	v_pk_fma_f32 v[96:97], v[62:63], v[136:137], v[14:15]
	v_cvt_pk_f32_fp8_sdwa v[116:117], v106 src0_sel:WORD_1
	v_pk_fma_f32 v[96:97], v[50:51], v[140:141], v[96:97]
	v_cvt_pk_f32_fp8_e32 v[110:111], v107
	v_pk_fma_f32 v[134:135], v[34:35], v[130:131], v[96:97]
	v_cvt_pk_f32_fp8_sdwa v[76:77], v107 src0_sel:WORD_1
	v_exp_f32_e32 v68, v134
	v_exp_f32_e32 v136, v135
	s_waitcnt vmcnt(19)
	v_cvt_pk_f32_fp8_e32 v[120:121], v102
	v_add_f32_e32 v68, 1.0, v68
	v_cvt_pk_f32_fp8_sdwa v[106:107], v102 src0_sel:WORD_1
	v_rcp_f32_e32 v102, v68
	v_add_f32_e32 v68, 1.0, v136
	v_cvt_pk_f32_fp8_e32 v[104:105], v103
	v_cvt_pk_f32_fp8_sdwa v[96:97], v103 src0_sel:WORD_1
	v_rcp_f32_e32 v103, v68
	v_pk_fma_f32 v[126:127], v[64:65], v[126:127], v[16:17]
	v_pk_fma_f32 v[132:133], v[58:59], v[132:133], v[10:11]
	v_pk_fma_f32 v[126:127], v[52:53], v[124:125], v[126:127]
	v_pk_mul_f32 v[102:103], v[134:135], v[102:103]
	v_pk_fma_f32 v[126:127], v[36:37], v[116:117], v[126:127]
	v_pk_fma_f32 v[132:133], v[42:43], v[128:129], v[132:133]
	v_exp_f32_e32 v68, v126
	v_exp_f32_e32 v134, v127
	v_pk_fma_f32 v[132:133], v[26:27], v[120:121], v[132:133]
	v_add_f32_e32 v68, 1.0, v68
	v_pk_fma_f32 v[112:113], v[54:55], v[112:113], v[6:7]
	v_pk_mul_f32 v[102:103], v[132:133], v[102:103]
	v_rcp_f32_e32 v132, v68
	v_add_f32_e32 v68, 1.0, v134
	v_rcp_f32_e32 v133, v68
	v_pk_fma_f32 v[112:113], v[38:39], v[118:119], v[112:113]
	v_pk_fma_f32 v[122:123], v[60:61], v[122:123], v[12:13]
	v_pk_fma_f32 v[112:113], v[22:23], v[110:111], v[112:113]
	v_pk_mul_f32 v[126:127], v[126:127], v[132:133]
	v_exp_f32_e32 v68, v112
	v_exp_f32_e32 v132, v113
	v_pk_fma_f32 v[122:123], v[44:45], v[114:115], v[122:123]
	v_add_f32_e32 v68, 1.0, v68
	v_pk_fma_f32 v[122:123], v[28:29], v[106:107], v[122:123]
	v_pk_fma_f32 v[84:85], v[56:57], v[84:85], v[8:9]
	s_nop 0
	v_pk_fma_f32 v[84:85], v[40:41], v[80:81], v[84:85]
	v_pk_mul_f32 v[122:123], v[122:123], v[126:127]
	v_rcp_f32_e32 v126, v68
	v_add_f32_e32 v68, 1.0, v132
	v_rcp_f32_e32 v127, v68
	v_pk_fma_f32 v[84:85], v[24:25], v[76:77], v[84:85]
	v_pk_fma_f32 v[108:109], v[46:47], v[108:109], v[2:3]
	v_pk_mul_f32 v[112:113], v[112:113], v[126:127]
	v_exp_f32_e32 v68, v84
	v_exp_f32_e32 v126, v85
	v_pk_fma_f32 v[108:109], v[30:31], v[100:101], v[108:109]
	v_add_f32_e32 v68, 1.0, v68
	v_pk_fma_f32 v[108:109], v[18:19], v[104:105], v[108:109]
	v_pk_fma_f32 v[88:89], v[48:49], v[88:89], v[4:5]
	s_nop 0
	v_pk_fma_f32 v[88:89], v[32:33], v[92:93], v[88:89]
	v_pk_mul_f32 v[108:109], v[108:109], v[112:113]
	v_rcp_f32_e32 v112, v68
	v_add_f32_e32 v68, 1.0, v126
	v_rcp_f32_e32 v113, v68
	v_pk_fma_f32 v[88:89], v[20:21], v[96:97], v[88:89]
	v_med3_f32 v68, v102, s41, v1
	v_pk_mul_f32 v[84:85], v[84:85], v[112:113]
	v_med3_f32 v102, v123, s41, v1
	v_pk_mul_f32 v[84:85], v[88:89], v[84:85]
	v_med3_f32 v89, v103, s41, v1
	v_cvt_pk_fp8_f32 v88, v68, v89
	v_med3_f32 v103, v108, s41, v1
	v_med3_f32 v108, v109, s41, v1
	v_cvt_pk_fp8_f32 v89, v103, v108
	v_med3_f32 v68, v122, s41, v1
	v_cvt_pk_fp8_f32 v88, v68, v102 op_sel:[0,0,1]
	v_med3_f32 v68, v84, s41, v1
	v_med3_f32 v84, v85, s41, v1
	v_cvt_pk_fp8_f32 v89, v68, v84 op_sel:[0,0,1]
	v_add_co_u32_e32 v84, vcc, s73, v70
	s_waitcnt vmcnt(18)
	v_cvt_pk_f32_fp8_e32 v[126:127], v98
	v_addc_co_u32_e32 v85, vcc, 0, v71, vcc
	global_store_dwordx2 v[84:85], v[88:89], off offset:2304
	v_pk_fma_f32 v[88:89], v[62:63], v[140:141], v[14:15]
	v_cvt_pk_f32_fp8_sdwa v[112:113], v98 src0_sel:WORD_1
	v_pk_fma_f32 v[88:89], v[50:51], v[130:131], v[88:89]
	s_waitcnt vmcnt(18)
	v_cvt_pk_f32_fp8_e32 v[122:123], v94
	v_pk_fma_f32 v[132:133], v[34:35], v[126:127], v[88:89]
	v_cvt_pk_f32_fp8_sdwa v[108:109], v94 src0_sel:WORD_1
	v_exp_f32_e32 v68, v132
	v_exp_f32_e32 v134, v133
	v_cvt_pk_f32_fp8_e32 v[102:103], v99
	v_add_f32_e32 v68, 1.0, v68
	v_rcp_f32_e32 v94, v68
	v_add_f32_e32 v68, 1.0, v134
	v_cvt_pk_f32_fp8_sdwa v[84:85], v99 src0_sel:WORD_1
	v_cvt_pk_f32_fp8_e32 v[98:99], v95
	v_cvt_pk_f32_fp8_sdwa v[88:89], v95 src0_sel:WORD_1
	v_rcp_f32_e32 v95, v68
	v_pk_fma_f32 v[124:125], v[64:65], v[124:125], v[16:17]
	v_pk_fma_f32 v[128:129], v[58:59], v[128:129], v[10:11]
	v_pk_fma_f32 v[124:125], v[52:53], v[116:117], v[124:125]
	v_pk_mul_f32 v[94:95], v[132:133], v[94:95]
	v_pk_fma_f32 v[124:125], v[36:37], v[112:113], v[124:125]
	v_pk_fma_f32 v[128:129], v[42:43], v[120:121], v[128:129]
	v_exp_f32_e32 v68, v124
	v_exp_f32_e32 v132, v125
	v_pk_fma_f32 v[128:129], v[26:27], v[122:123], v[128:129]
	v_add_f32_e32 v68, 1.0, v68
	v_pk_fma_f32 v[118:119], v[54:55], v[118:119], v[6:7]
	v_pk_mul_f32 v[94:95], v[128:129], v[94:95]
	v_rcp_f32_e32 v128, v68
	v_add_f32_e32 v68, 1.0, v132
	v_rcp_f32_e32 v129, v68
	v_pk_fma_f32 v[118:119], v[38:39], v[110:111], v[118:119]
	v_pk_fma_f32 v[114:115], v[60:61], v[114:115], v[12:13]
	v_pk_fma_f32 v[118:119], v[22:23], v[102:103], v[118:119]
	v_pk_mul_f32 v[124:125], v[124:125], v[128:129]
	v_exp_f32_e32 v68, v118
	v_exp_f32_e32 v128, v119
	v_pk_fma_f32 v[114:115], v[44:45], v[106:107], v[114:115]
	v_add_f32_e32 v68, 1.0, v68
	v_pk_fma_f32 v[114:115], v[28:29], v[108:109], v[114:115]
	v_pk_fma_f32 v[80:81], v[56:57], v[80:81], v[8:9]
	s_nop 0
	v_pk_fma_f32 v[80:81], v[40:41], v[76:77], v[80:81]
	v_pk_mul_f32 v[114:115], v[114:115], v[124:125]
	v_rcp_f32_e32 v124, v68
	v_add_f32_e32 v68, 1.0, v128
	v_rcp_f32_e32 v125, v68
	v_pk_fma_f32 v[80:81], v[24:25], v[84:85], v[80:81]
	v_pk_fma_f32 v[100:101], v[46:47], v[100:101], v[2:3]
	v_pk_mul_f32 v[118:119], v[118:119], v[124:125]
	v_exp_f32_e32 v68, v80
	v_exp_f32_e32 v124, v81
	v_pk_fma_f32 v[100:101], v[30:31], v[104:105], v[100:101]
	v_add_f32_e32 v68, 1.0, v68
	v_pk_fma_f32 v[100:101], v[18:19], v[98:99], v[100:101]
	v_pk_fma_f32 v[92:93], v[48:49], v[92:93], v[4:5]
	s_nop 0
	v_pk_fma_f32 v[92:93], v[32:33], v[96:97], v[92:93]
	v_pk_mul_f32 v[100:101], v[100:101], v[118:119]
	v_rcp_f32_e32 v118, v68
	v_add_f32_e32 v68, 1.0, v124
	v_rcp_f32_e32 v119, v68
	v_pk_fma_f32 v[92:93], v[20:21], v[88:89], v[92:93]
	v_med3_f32 v68, v94, s41, v1
	v_pk_mul_f32 v[80:81], v[80:81], v[118:119]
	s_waitcnt vmcnt(17)
; __device__ __forceinline__ float clamp448(float x) { return __builtin_amdgcn_fmed3f(x, -448.f, 448.f); }
; __device__ __forceinline__ unsigned pk4_fp8(float a, float b, float c, float d) {
;     int w = __builtin_amdgcn_cvt_pk_fp8_f32(clamp448(a), clamp448(b), 0, false);
;     w = __builtin_amdgcn_cvt_pk_fp8_f32(clamp448(c), clamp448(d), w, true);
;     return (unsigned)w;
; }
	v_cvt_pk_f32_fp8_e32 v[118:119], v90
	v_pk_mul_f32 v[80:81], v[92:93], v[80:81]
	v_med3_f32 v93, v95, s41, v1
	v_cvt_pk_fp8_f32 v92, v68, v93
	v_med3_f32 v95, v100, s41, v1
	v_med3_f32 v100, v101, s41, v1
	v_cvt_pk_fp8_f32 v93, v95, v100
	v_pk_fma_f32 v[124:125], v[62:63], v[130:131], v[14:15]
	v_med3_f32 v68, v114, s41, v1
	v_med3_f32 v94, v115, s41, v1
	v_pk_fma_f32 v[124:125], v[50:51], v[126:127], v[124:125]
	v_cvt_pk_fp8_f32 v92, v68, v94 op_sel:[0,0,1]
	v_med3_f32 v68, v80, s41, v1
	v_med3_f32 v80, v81, s41, v1
	v_pk_fma_f32 v[124:125], v[34:35], v[118:119], v[124:125]
	v_cvt_pk_fp8_f32 v93, v68, v80 op_sel:[0,0,1]
	s_waitcnt vmcnt(16)
	v_cvt_pk_f32_fp8_e32 v[114:115], v86
	v_cvt_pk_f32_fp8_sdwa v[94:95], v86 src0_sel:WORD_1
	v_exp_f32_e32 v68, v124
	v_exp_f32_e32 v129, v125
	v_cvt_pk_f32_fp8_sdwa v[100:101], v90 src0_sel:WORD_1
	v_add_f32_e32 v68, 1.0, v68
	v_rcp_f32_e32 v128, v68
	v_add_f32_e32 v68, 1.0, v129
	v_rcp_f32_e32 v129, v68
	v_pk_fma_f32 v[116:117], v[64:65], v[116:117], v[16:17]
	v_pk_fma_f32 v[120:121], v[58:59], v[120:121], v[10:11]
	v_pk_fma_f32 v[116:117], v[52:53], v[112:113], v[116:117]
	v_pk_mul_f32 v[124:125], v[124:125], v[128:129]
	v_pk_fma_f32 v[116:117], v[36:37], v[100:101], v[116:117]
	v_add_co_u32_e32 v80, vcc, s39, v70
	v_exp_f32_e32 v68, v116
	v_exp_f32_e32 v128, v117
	v_pk_fma_f32 v[120:121], v[42:43], v[122:123], v[120:121]
	v_addc_co_u32_e32 v81, vcc, 0, v71, vcc
	v_pk_fma_f32 v[120:121], v[26:27], v[114:115], v[120:121]
	global_store_dwordx2 v[80:81], v[92:93], off offset:1024
	v_cvt_pk_f32_fp8_e32 v[92:93], v91
	v_add_f32_e32 v68, 1.0, v68
	v_pk_mul_f32 v[120:121], v[120:121], v[124:125]
	v_rcp_f32_e32 v124, v68
	v_add_f32_e32 v68, 1.0, v128
	v_rcp_f32_e32 v125, v68
	v_pk_fma_f32 v[110:111], v[54:55], v[110:111], v[6:7]
	v_pk_fma_f32 v[106:107], v[60:61], v[106:107], v[12:13]
	v_pk_fma_f32 v[110:111], v[38:39], v[102:103], v[110:111]
	v_pk_mul_f32 v[116:117], v[116:117], v[124:125]
	v_pk_fma_f32 v[110:111], v[22:23], v[92:93], v[110:111]
	v_pk_fma_f32 v[106:107], v[44:45], v[108:109], v[106:107]
	v_exp_f32_e32 v68, v110
	v_exp_f32_e32 v124, v111
	v_pk_fma_f32 v[106:107], v[28:29], v[94:95], v[106:107]
	v_cvt_pk_f32_fp8_sdwa v[80:81], v91 src0_sel:WORD_1
	v_add_f32_e32 v68, 1.0, v68
	v_pk_mul_f32 v[106:107], v[106:107], v[116:117]
	v_rcp_f32_e32 v116, v68
	v_add_f32_e32 v68, 1.0, v124
	v_rcp_f32_e32 v117, v68
	v_pk_fma_f32 v[76:77], v[56:57], v[76:77], v[8:9]
	v_cvt_pk_f32_fp8_e32 v[90:91], v87
	v_pk_fma_f32 v[76:77], v[40:41], v[84:85], v[76:77]
	v_pk_mul_f32 v[110:111], v[110:111], v[116:117]
	v_pk_fma_f32 v[76:77], v[24:25], v[80:81], v[76:77]
	v_pk_fma_f32 v[104:105], v[46:47], v[104:105], v[2:3]
	v_exp_f32_e32 v68, v76
	v_exp_f32_e32 v116, v77
	v_pk_fma_f32 v[104:105], v[30:31], v[98:99], v[104:105]
	v_add_f32_e32 v68, 1.0, v68
	v_pk_fma_f32 v[104:105], v[18:19], v[90:91], v[104:105]
	v_cvt_pk_f32_fp8_sdwa v[86:87], v87 src0_sel:WORD_1
	v_pk_fma_f32 v[96:97], v[48:49], v[96:97], v[4:5]
	v_pk_mul_f32 v[104:105], v[104:105], v[110:111]
	v_rcp_f32_e32 v110, v68
	v_add_f32_e32 v68, 1.0, v116
	v_rcp_f32_e32 v111, v68
	v_pk_fma_f32 v[96:97], v[32:33], v[88:89], v[96:97]
	v_med3_f32 v68, v120, s41, v1
	v_pk_fma_f32 v[96:97], v[20:21], v[86:87], v[96:97]
	v_pk_mul_f32 v[76:77], v[76:77], v[110:111]
	v_med3_f32 v104, v104, s41, v1
	v_pk_mul_f32 v[76:77], v[96:97], v[76:77]
	v_med3_f32 v97, v121, s41, v1
	v_cvt_pk_fp8_f32 v96, v68, v97
	v_med3_f32 v105, v105, s41, v1
	v_cvt_pk_fp8_f32 v97, v104, v105
	v_med3_f32 v68, v106, s41, v1
	v_med3_f32 v106, v107, s41, v1
	v_cvt_pk_fp8_f32 v96, v68, v106 op_sel:[0,0,1]
	v_med3_f32 v68, v76, s41, v1
	v_med3_f32 v76, v77, s41, v1
	v_cvt_pk_fp8_f32 v97, v68, v76 op_sel:[0,0,1]
	v_add_co_u32_e32 v76, vcc, s74, v70
	v_pk_fma_f32 v[120:121], v[62:63], v[126:127], v[14:15]
	s_nop 0
	v_addc_co_u32_e32 v77, vcc, 0, v71, vcc
	global_store_dwordx2 v[76:77], v[96:97], off offset:3840
	s_waitcnt vmcnt(17)
	v_cvt_pk_f32_fp8_e32 v[76:77], v82
	v_pk_fma_f32 v[120:121], v[50:51], v[118:119], v[120:121]
	s_waitcnt vmcnt(16)
; #define CV_LOAD(G_, V_, r0_) do { _Pragma("unroll") for (int i_ = 0; i_ < 8; ++i_) { G_[i_] = *(const GAS v2u*)(ap + (size_t)((r0_) + i_) * F2); V_[i_] = *(const GAS v2u*)(ap + (size_t)((r0_) + i_) * F2 + 128); } } while (0)
; __device__ __forceinline__ void conv_phase(Frame& F) {
;     ...
;         CV_LOAD(GA, VA, 0); CV_LOAD(GB, VB, 8); CV_COMP(GA, VA, 0); CV_LOAD(GA, VA, 16); CV_COMP(GB, VB, 8); CV_LOAD(GB, VB, 24); CV_COMP(GA, VA, 16); CV_COMP(GB, VB, 24);
;     ...
;     }
	v_cvt_pk_f32_fp8_e32 v[106:107], v78
	v_cvt_pk_f32_fp8_sdwa v[110:111], v78 src0_sel:WORD_1
	v_pk_fma_f32 v[120:121], v[34:35], v[76:77], v[120:121]
	v_cvt_pk_f32_fp8_sdwa v[96:97], v82 src0_sel:WORD_1
	v_exp_f32_e32 v68, v120
	v_exp_f32_e32 v125, v121
	v_pk_fma_f32 v[112:113], v[64:65], v[112:113], v[16:17]
	v_add_f32_e32 v68, 1.0, v68
	v_rcp_f32_e32 v124, v68
	v_add_f32_e32 v68, 1.0, v125
	v_rcp_f32_e32 v125, v68
	v_pk_fma_f32 v[112:113], v[52:53], v[100:101], v[112:113]
	v_pk_fma_f32 v[122:123], v[58:59], v[122:123], v[10:11]
	v_pk_fma_f32 v[112:113], v[36:37], v[96:97], v[112:113]
	v_pk_mul_f32 v[120:121], v[120:121], v[124:125]
	v_exp_f32_e32 v68, v112
	v_exp_f32_e32 v124, v113
	v_pk_fma_f32 v[122:123], v[42:43], v[114:115], v[122:123]
	v_cvt_pk_f32_fp8_e32 v[104:105], v83
	v_pk_fma_f32 v[122:123], v[26:27], v[106:107], v[122:123]
	v_add_f32_e32 v68, 1.0, v68
	v_pk_fma_f32 v[102:103], v[54:55], v[102:103], v[6:7]
	v_pk_mul_f32 v[120:121], v[122:123], v[120:121]
	v_rcp_f32_e32 v122, v68
	v_add_f32_e32 v68, 1.0, v124
	v_rcp_f32_e32 v123, v68
	v_pk_fma_f32 v[102:103], v[38:39], v[92:93], v[102:103]
	v_pk_fma_f32 v[108:109], v[60:61], v[108:109], v[12:13]
	v_pk_fma_f32 v[102:103], v[22:23], v[104:105], v[102:103]
	v_pk_mul_f32 v[112:113], v[112:113], v[122:123]
	v_exp_f32_e32 v68, v102
	v_exp_f32_e32 v122, v103
	v_pk_fma_f32 v[108:109], v[44:45], v[94:95], v[108:109]
	v_cvt_pk_f32_fp8_sdwa v[82:83], v83 src0_sel:WORD_1
	v_pk_fma_f32 v[108:109], v[28:29], v[110:111], v[108:109]
	v_add_f32_e32 v68, 1.0, v68
	v_pk_fma_f32 v[84:85], v[56:57], v[84:85], v[8:9]
	v_pk_mul_f32 v[108:109], v[108:109], v[112:113]
	v_rcp_f32_e32 v112, v68
	v_add_f32_e32 v68, 1.0, v122
	v_rcp_f32_e32 v113, v68
	v_pk_fma_f32 v[84:85], v[40:41], v[80:81], v[84:85]
	v_cvt_pk_f32_fp8_e32 v[116:117], v79
	v_pk_fma_f32 v[84:85], v[24:25], v[82:83], v[84:85]
	v_pk_mul_f32 v[102:103], v[102:103], v[112:113]
	v_exp_f32_e32 v68, v84
	v_pk_fma_f32 v[98:99], v[46:47], v[98:99], v[2:3]
	v_exp_f32_e32 v112, v85
	v_pk_fma_f32 v[98:99], v[30:31], v[90:91], v[98:99]
	v_add_f32_e32 v68, 1.0, v68
	v_pk_fma_f32 v[98:99], v[18:19], v[116:117], v[98:99]
	v_cvt_pk_f32_fp8_sdwa v[78:79], v79 src0_sel:WORD_1
	v_pk_fma_f32 v[88:89], v[48:49], v[88:89], v[4:5]
	v_pk_mul_f32 v[98:99], v[98:99], v[102:103]
	v_rcp_f32_e32 v102, v68
	v_add_f32_e32 v68, 1.0, v112
	v_rcp_f32_e32 v103, v68
	v_pk_fma_f32 v[88:89], v[32:33], v[86:87], v[88:89]
	v_med3_f32 v68, v120, s41, v1
	v_pk_fma_f32 v[88:89], v[20:21], v[78:79], v[88:89]
	v_pk_mul_f32 v[84:85], v[84:85], v[102:103]
	v_med3_f32 v98, v98, s41, v1
	v_pk_mul_f32 v[84:85], v[88:89], v[84:85]
	v_med3_f32 v89, v121, s41, v1
	v_cvt_pk_fp8_f32 v88, v68, v89
	v_med3_f32 v99, v99, s41, v1
	v_cvt_pk_fp8_f32 v89, v98, v99
	v_med3_f32 v68, v108, s41, v1
	v_med3_f32 v102, v109, s41, v1
	v_cvt_pk_fp8_f32 v88, v68, v102 op_sel:[0,0,1]
	v_med3_f32 v68, v84, s41, v1
	v_med3_f32 v84, v85, s41, v1
	v_cvt_pk_fp8_f32 v89, v68, v84 op_sel:[0,0,1]
	v_add_co_u32_e32 v84, vcc, s40, v70
	v_pk_fma_f32 v[14:15], v[62:63], v[118:119], v[14:15]
	s_nop 0
	v_addc_co_u32_e32 v85, vcc, 0, v71, vcc
	global_store_dwordx2 v[84:85], v[88:89], off offset:2560
	s_waitcnt vmcnt(16)
	v_cvt_pk_f32_fp8_e32 v[84:85], v74
	v_pk_fma_f32 v[14:15], v[50:51], v[76:77], v[14:15]
	v_cvt_pk_f32_fp8_sdwa v[88:89], v74 src0_sel:WORD_1
	s_waitcnt vmcnt(15)
	v_cvt_pk_f32_fp8_e32 v[102:103], v72
	v_pk_fma_f32 v[14:15], v[34:35], v[84:85], v[14:15]
	v_pk_fma_f32 v[16:17], v[64:65], v[100:101], v[16:17]
	v_exp_f32_e32 v50, v14
	v_exp_f32_e32 v51, v15
	v_pk_fma_f32 v[10:11], v[58:59], v[114:115], v[10:11]
	v_pk_fma_f32 v[16:17], v[52:53], v[96:97], v[16:17]
	v_add_f32_e32 v50, 1.0, v50
	v_add_f32_e32 v51, 1.0, v51
	v_pk_fma_f32 v[10:11], v[42:43], v[106:107], v[10:11]
	v_pk_fma_f32 v[16:17], v[36:37], v[88:89], v[16:17]
	v_rcp_f32_e32 v50, v50
	v_rcp_f32_e32 v51, v51
	v_pk_fma_f32 v[10:11], v[26:27], v[102:103], v[10:11]
	v_exp_f32_e32 v26, v16
	v_exp_f32_e32 v27, v17
	v_pk_mul_f32 v[14:15], v[14:15], v[50:51]
	v_cvt_pk_f32_fp8_e32 v[98:99], v75
	v_pk_mul_f32 v[10:11], v[10:11], v[14:15]
	v_add_f32_e32 v14, 1.0, v26
	v_add_f32_e32 v15, 1.0, v27
	v_rcp_f32_e32 v14, v14
	v_rcp_f32_e32 v15, v15
	v_pk_fma_f32 v[6:7], v[54:55], v[92:93], v[6:7]
	v_cvt_pk_f32_fp8_sdwa v[108:109], v72 src0_sel:WORD_1
	v_pk_fma_f32 v[6:7], v[38:39], v[104:105], v[6:7]
	v_pk_mul_f32 v[14:15], v[16:17], v[14:15]
	v_pk_fma_f32 v[6:7], v[22:23], v[98:99], v[6:7]
	v_pk_fma_f32 v[12:13], v[60:61], v[94:95], v[12:13]
	v_exp_f32_e32 v16, v6
	v_exp_f32_e32 v17, v7
	v_pk_fma_f32 v[12:13], v[44:45], v[110:111], v[12:13]
	v_cvt_pk_f32_fp8_sdwa v[74:75], v75 src0_sel:WORD_1
	v_pk_fma_f32 v[12:13], v[28:29], v[108:109], v[12:13]
	v_pk_fma_f32 v[8:9], v[56:57], v[80:81], v[8:9]
	s_nop 0
	v_pk_fma_f32 v[8:9], v[40:41], v[82:83], v[8:9]
	v_pk_mul_f32 v[12:13], v[12:13], v[14:15]
	v_add_f32_e32 v14, 1.0, v16
	v_add_f32_e32 v15, 1.0, v17
	v_rcp_f32_e32 v14, v14
	v_rcp_f32_e32 v15, v15
	v_cvt_pk_f32_fp8_e32 v[112:113], v73
	v_pk_fma_f32 v[8:9], v[24:25], v[74:75], v[8:9]
	v_pk_fma_f32 v[2:3], v[46:47], v[90:91], v[2:3]
	v_pk_mul_f32 v[6:7], v[6:7], v[14:15]
	v_exp_f32_e32 v14, v8
	v_exp_f32_e32 v15, v9
	v_pk_fma_f32 v[2:3], v[30:31], v[116:117], v[2:3]
	v_cvt_pk_f32_fp8_sdwa v[34:35], v73 src0_sel:WORD_1
	v_pk_fma_f32 v[2:3], v[18:19], v[112:113], v[2:3]
	v_pk_fma_f32 v[4:5], v[48:49], v[86:87], v[4:5]
	s_nop 0
	v_pk_fma_f32 v[4:5], v[32:33], v[78:79], v[4:5]
	v_pk_mul_f32 v[2:3], v[2:3], v[6:7]
	v_add_f32_e32 v6, 1.0, v14
	v_add_f32_e32 v7, 1.0, v15
	v_rcp_f32_e32 v6, v6
	v_rcp_f32_e32 v7, v7
	v_pk_fma_f32 v[4:5], v[20:21], v[34:35], v[4:5]
	v_med3_f32 v2, v2, s41, v1
	v_pk_mul_f32 v[6:7], v[8:9], v[6:7]
	v_med3_f32 v8, v11, s41, v1
	v_pk_mul_f32 v[4:5], v[4:5], v[6:7]
	v_med3_f32 v7, v10, s41, v1
	v_cvt_pk_fp8_f32 v6, v7, v8
	v_med3_f32 v3, v3, s41, v1
	v_cvt_pk_fp8_f32 v7, v2, v3
	v_med3_f32 v8, v12, s41, v1
	v_med3_f32 v9, v13, s41, v1
	v_med3_f32 v2, v4, s41, v1
	v_med3_f32 v3, v5, s41, v1
	v_cvt_pk_fp8_f32 v6, v8, v9 op_sel:[0,0,1]
	v_cvt_pk_fp8_f32 v7, v2, v3 op_sel:[0,0,1]
	v_add_co_u32_e32 v2, vcc, 0x53000, v70
	v_lshl_add_u64 v[66:67], v[66:67], 0, s[18:19]
	s_nop 0
	v_addc_co_u32_e32 v3, vcc, 0, v71, vcc
	global_store_dwordx2 v[2:3], v[6:7], off offset:1280
	s_mov_b64 s[22:23], 0x55fff
	v_cmp_lt_u64_e32 vcc, s[22:23], v[66:67]
	s_or_b64 s[16:17], vcc, s[16:17]
	s_andn2_b64 exec, exec, s[16:17]
	s_cbranch_execz .LBB0_2571
